# baseline (speedup 1.0000x reference)
.Llight_path:
	s_lshr_b32 s27, s7, 8
	s_waitcnt vmcnt(16)
	v_mul_u32_u24_e32 v236, 36, v228
	v_add_u32_e32 v236, v236, v230
	v_add_u32_e32 v237, s7, v229
	v_mul_u32_u24_e32 v238, 0x104, v228
	v_add_u32_e32 v238, v238, v237
	v_add_u32_e32 v238, 0xb840, v238
	v_add_u32_e32 v231, s7, v229
	v_add_u32_e32 v231, 0xb840, v231
	v_add_u32_e32 v211, s6, v210
	s_nop 0
	s_load_dwordx8 s[4:11], s[0:1], 0x10
	v_add_u32_e32 v232, 0x24e80, v228
	ds_read_b32 v244, v232
	ds_read_b32 v245, v232 offset:128
	ds_read_b128 v[194:197], v237 offset:36928
	ds_read_b128 v[198:201], v237 offset:36944
	ds_read_b128 v[202:205], v237 offset:36960
	ds_read_b128 v[206:209], v237 offset:36976
	ds_read_b128 v[212:215], v237 offset:37056
	ds_read_b128 v[216:219], v237 offset:37072
	ds_read_b128 v[220:223], v237 offset:37088
	ds_read_b128 v[224:227], v237 offset:37104
	ds_read_b128 v[162:165], v236 offset:16384
	ds_read_b128 v[166:169], v236 offset:16416
	ds_read_b128 v[170:173], v236 offset:16448
	ds_read_b128 v[174:177], v236 offset:16480
	s_waitcnt lgkmcnt(0)
	v_mfma_f32_32x32x16_bf16 v[2:17], v[94:97], v[162:165], v[194:209]
	v_mfma_f32_32x32x16_bf16 v[18:33], v[46:49], v[162:165], v[212:227]
	v_mfma_f32_32x32x16_bf16 v[2:17], v[90:93], v[166:169], v[2:17]
	v_mfma_f32_32x32x16_bf16 v[18:33], v[42:45], v[166:169], v[18:33]
	v_mfma_f32_32x32x16_bf16 v[2:17], v[86:89], v[170:173], v[2:17]
	ds_read_b128 v[178:181], v236 offset:20992
	v_mfma_f32_32x32x16_bf16 v[18:33], v[38:41], v[170:173], v[18:33]
	ds_read_b128 v[182:185], v236 offset:21024
	v_mfma_f32_32x32x16_bf16 v[2:17], v[82:85], v[174:177], v[2:17]
	ds_read_b128 v[186:189], v236 offset:21056
	v_mfma_f32_32x32x16_bf16 v[18:33], v[34:37], v[174:177], v[18:33]
	ds_read_b128 v[190:193], v236 offset:21088
	s_waitcnt lgkmcnt(0)
	v_mfma_f32_32x32x16_bf16 v[130:145], v[94:97], v[178:181], v[194:209]
	v_mfma_f32_32x32x16_bf16 v[146:161], v[46:49], v[178:181], v[212:227]
	v_mfma_f32_32x32x16_bf16 v[130:145], v[90:93], v[182:185], v[130:145]
	v_mfma_f32_32x32x16_bf16 v[146:161], v[42:45], v[182:185], v[146:161]
	s_nop 7
	ds_write_b128 v238, v[2:5] offset:0
	ds_write_b128 v238, v[6:9] offset:16
	ds_write_b128 v238, v[10:13] offset:32
	ds_write_b128 v238, v[14:17] offset:48
	ds_write_b128 v238, v[18:21] offset:128
	ds_write_b128 v238, v[22:25] offset:144
	ds_write_b128 v238, v[26:29] offset:160
	ds_write_b128 v238, v[30:33] offset:176
	v_mfma_f32_32x32x16_bf16 v[130:145], v[86:89], v[186:189], v[130:145]
	ds_read_b128 v[162:165], v236 offset:25600
	v_mfma_f32_32x32x16_bf16 v[146:161], v[38:41], v[186:189], v[146:161]
	ds_read_b128 v[166:169], v236 offset:25632
	v_mfma_f32_32x32x16_bf16 v[130:145], v[82:85], v[190:193], v[130:145]
	ds_read_b128 v[170:173], v236 offset:25664
	v_mfma_f32_32x32x16_bf16 v[146:161], v[34:37], v[190:193], v[146:161]
	ds_read_b128 v[174:177], v236 offset:25696
	s_waitcnt lgkmcnt(0)
	v_mfma_f32_32x32x16_bf16 v[2:17], v[94:97], v[162:165], v[194:209]
	v_mfma_f32_32x32x16_bf16 v[18:33], v[46:49], v[162:165], v[212:227]
	v_mfma_f32_32x32x16_bf16 v[2:17], v[90:93], v[166:169], v[2:17]
	v_mfma_f32_32x32x16_bf16 v[18:33], v[42:45], v[166:169], v[18:33]
	s_nop 7
	v_add_u32_e32 v239, 0x8200, v238
	ds_write_b128 v239, v[130:133] offset:0
	ds_write_b128 v239, v[134:137] offset:16
	ds_write_b128 v239, v[138:141] offset:32
	ds_write_b128 v239, v[142:145] offset:48
	ds_write_b128 v239, v[146:149] offset:128
	ds_write_b128 v239, v[150:153] offset:144
	ds_write_b128 v239, v[154:157] offset:160
	ds_write_b128 v239, v[158:161] offset:176
	v_mfma_f32_32x32x16_bf16 v[2:17], v[86:89], v[170:173], v[2:17]
	ds_read_b128 v[178:181], v236 offset:30208
	v_mfma_f32_32x32x16_bf16 v[18:33], v[38:41], v[170:173], v[18:33]
	ds_read_b128 v[182:185], v236 offset:30240
	v_mfma_f32_32x32x16_bf16 v[2:17], v[82:85], v[174:177], v[2:17]
	ds_read_b128 v[186:189], v236 offset:30272
	v_mfma_f32_32x32x16_bf16 v[18:33], v[34:37], v[174:177], v[18:33]
	ds_read_b128 v[190:193], v236 offset:30304
	s_waitcnt lgkmcnt(0)
	v_mfma_f32_32x32x16_bf16 v[130:145], v[94:97], v[178:181], v[194:209]
	v_mfma_f32_32x32x16_bf16 v[146:161], v[46:49], v[178:181], v[212:227]
	v_mfma_f32_32x32x16_bf16 v[130:145], v[90:93], v[182:185], v[130:145]
	v_mfma_f32_32x32x16_bf16 v[146:161], v[42:45], v[182:185], v[146:161]
	s_nop 7
	v_add_u32_e32 v239, 0x10400, v238
	ds_write_b128 v239, v[2:5] offset:0
	ds_write_b128 v239, v[6:9] offset:16
	ds_write_b128 v239, v[10:13] offset:32
	ds_write_b128 v239, v[14:17] offset:48
	ds_write_b128 v239, v[18:21] offset:128
	ds_write_b128 v239, v[22:25] offset:144
	ds_write_b128 v239, v[26:29] offset:160
	ds_write_b128 v239, v[30:33] offset:176
	v_mfma_f32_32x32x16_bf16 v[130:145], v[86:89], v[186:189], v[130:145]
	v_mfma_f32_32x32x16_bf16 v[146:161], v[38:41], v[186:189], v[146:161]
	v_mfma_f32_32x32x16_bf16 v[130:145], v[82:85], v[190:193], v[130:145]
	v_mfma_f32_32x32x16_bf16 v[146:161], v[34:37], v[190:193], v[146:161]
	s_nop 7
	s_nop 7
	v_cmp_gt_u32_e32 vcc, 16, v228
	s_and_saveexec_b64 s[20:21], vcc
	v_add_u32_e32 v239, 0x18600, v238
	ds_write_b128 v239, v[130:133] offset:0
	ds_write_b128 v239, v[134:137] offset:16
	ds_write_b128 v239, v[138:141] offset:32
	ds_write_b128 v239, v[142:145] offset:48
	ds_write_b128 v239, v[146:149] offset:128
	ds_write_b128 v239, v[150:153] offset:144
	ds_write_b128 v239, v[154:157] offset:160
	ds_write_b128 v239, v[158:161] offset:176
	s_or_b64 exec, exec, s[20:21]
	s_mov_b32 s12, 0xbeb17218
	v_mov_b32_e32 v235, 0xc038aa3b
	v_add_u32_e32 v233, v231, v244
	v_add_u32_e32 v234, v231, v245
	ds_read_b128 v[2:5], v233 offset:0
	ds_read_b128 v[6:9], v233 offset:16
	ds_read_b128 v[10:13], v233 offset:32
	ds_read_b128 v[14:17], v233 offset:48
	ds_read_b128 v[18:21], v233 offset:128
	ds_read_b128 v[22:25], v233 offset:144
	ds_read_b128 v[26:29], v233 offset:160
	ds_read_b128 v[30:33], v233 offset:176
	ds_read_b128 v[34:37], v234 offset:0
	ds_read_b128 v[38:41], v234 offset:16
	ds_read_b128 v[42:45], v234 offset:32
	ds_read_b128 v[46:49], v234 offset:48
	v_mov_b32_e32 v194, 0
	v_mov_b32_e32 v195, 0
	v_mov_b32_e32 v196, 0
	v_mov_b32_e32 v197, 0
	v_mov_b32_e32 v198, 0
	v_mov_b32_e32 v199, 0
	v_mov_b32_e32 v200, 0
	v_mov_b32_e32 v201, 0
	v_mov_b32_e32 v202, 0
	v_mov_b32_e32 v203, 0
	v_mov_b32_e32 v204, 0
	v_mov_b32_e32 v205, 0
	v_mov_b32_e32 v206, 0
	v_mov_b32_e32 v207, 0
	v_mov_b32_e32 v208, 0
	v_mov_b32_e32 v209, 0
	v_add_u32_e32 v232, 0x100, v232
	s_movk_i32 s16, 18
	s_waitcnt vmcnt(0) lgkmcnt(0)
	s_cmp_eq_u32 s27, 1
	s_cbranch_scc1 .Llight_w1
	s_cmp_eq_u32 s27, 2
	s_cbranch_scc1 .Llight_w2
	s_cmp_eq_u32 s27, 3
	s_cbranch_scc1 .Llight_w3
	ds_read_b128 v[82:85], v234 offset:128
	ds_read_b128 v[86:89], v234 offset:144
	ds_read_b128 v[90:93], v234 offset:160
	ds_read_b128 v[94:97], v234 offset:176
	ds_read2_b32 v[244:245], v232 offset1:32
	v_exp_f32_e32 v212, v4
	v_exp_f32_e32 v213, v8
	v_exp_f32_e32 v214, v12
	v_exp_f32_e32 v215, v16
	v_exp_f32_e32 v216, v2
	v_fma_f32 v251, v212, s12, s12
	v_exp_f32_e32 v217, v6
	v_fma_f32 v252, v213, s12, s12
	v_exp_f32_e32 v218, v10
	v_fma_f32 v253, v214, s12, s12
	v_exp_f32_e32 v219, v14
	v_fma_f32 v254, v215, s12, s12
	v_fmac_f32_e32 v251, v216, v251
	v_fmac_f32_e32 v252, v217, v252
	v_fmac_f32_e32 v253, v218, v253
	v_fmac_f32_e32 v254, v219, v254
	v_rcp_f32_e32 v216, v251
	v_rcp_f32_e32 v217, v252
	v_rcp_f32_e32 v218, v253
	v_rcp_f32_e32 v219, v254
	v_exp_f32_e32 v246, v5
	v_fma_f32 v194, -v212, v216, v216
	v_exp_f32_e32 v247, v9
	v_fma_f32 v195, -v213, v217, v217
	v_exp_f32_e32 v248, v13
	v_fma_f32 v196, -v214, v218, v218
	v_exp_f32_e32 v249, v17
	v_fma_f32 v197, -v215, v219, v219
	v_exp_f32_e32 v212, v194
	v_add_f32_e32 v246, 1.0, v246
	v_exp_f32_e32 v213, v195
	v_add_f32_e32 v247, 1.0, v247
	v_exp_f32_e32 v214, v196
	v_add_f32_e32 v248, 1.0, v248
	v_exp_f32_e32 v215, v197
	v_add_f32_e32 v249, 1.0, v249
	v_fmac_f32_e32 v246, v246, v212
	v_fmac_f32_e32 v247, v247, v213
	v_fmac_f32_e32 v248, v248, v214
	v_fmac_f32_e32 v249, v249, v215
	v_rcp_f32_e32 v246, v246
	v_rcp_f32_e32 v247, v247
	v_rcp_f32_e32 v248, v248
	v_rcp_f32_e32 v249, v249
	v_fma_f32 v246, -v212, v246, v246
	v_fma_f32 v247, -v213, v247, v247
	v_fma_f32 v248, -v214, v248, v248
	v_fma_f32 v249, -v215, v249, v249
	v_cvt_pk_bf16_f32 v236, v246, v247
	v_cvt_pk_bf16_f32 v237, v248, v249
	s_waitcnt lgkmcnt(0)
	v_add_u32_e32 v233, v231, v244
	ds_read_b128 v[2:5], v233 offset:0
	ds_read_b128 v[6:9], v233 offset:16
	ds_read_b128 v[10:13], v233 offset:32
	ds_read_b128 v[14:17], v233 offset:48
	v_exp_f32_e32 v212, v20
	v_exp_f32_e32 v213, v24
	v_exp_f32_e32 v214, v28
	v_exp_f32_e32 v215, v32
	v_exp_f32_e32 v216, v18
	v_fma_f32 v251, v212, s12, s12
	v_exp_f32_e32 v217, v22
	v_fma_f32 v252, v213, s12, s12
	v_exp_f32_e32 v218, v26
	v_fma_f32 v253, v214, s12, s12
	v_exp_f32_e32 v219, v30
	v_fma_f32 v254, v215, s12, s12
	v_fmac_f32_e32 v251, v216, v251
	v_fmac_f32_e32 v252, v217, v252
	v_fmac_f32_e32 v253, v218, v253
	v_fmac_f32_e32 v254, v219, v254
	v_rcp_f32_e32 v216, v251
	v_rcp_f32_e32 v217, v252
	v_rcp_f32_e32 v218, v253
	v_rcp_f32_e32 v219, v254
	v_exp_f32_e32 v246, v21
	v_fma_f32 v198, -v212, v216, v216
	v_exp_f32_e32 v247, v25
	v_fma_f32 v199, -v213, v217, v217
	v_exp_f32_e32 v248, v29
	v_fma_f32 v200, -v214, v218, v218
	v_exp_f32_e32 v249, v33
	v_fma_f32 v201, -v215, v219, v219
	v_exp_f32_e32 v212, v198
	v_add_f32_e32 v246, 1.0, v246
	v_exp_f32_e32 v213, v199
	v_add_f32_e32 v247, 1.0, v247
	v_exp_f32_e32 v214, v200
	v_add_f32_e32 v248, 1.0, v248
	v_exp_f32_e32 v215, v201
	v_add_f32_e32 v249, 1.0, v249
	v_fmac_f32_e32 v246, v246, v212
	v_fmac_f32_e32 v247, v247, v213
	v_fmac_f32_e32 v248, v248, v214
	v_fmac_f32_e32 v249, v249, v215
	v_rcp_f32_e32 v246, v246
	v_rcp_f32_e32 v247, v247
	v_rcp_f32_e32 v248, v248
	v_rcp_f32_e32 v249, v249
	v_fma_f32 v246, -v212, v246, v246
	v_fma_f32 v247, -v213, v247, v247
	v_fma_f32 v248, -v214, v248, v248
	v_fma_f32 v249, -v215, v249, v249
	v_cvt_pk_bf16_f32 v238, v246, v247
	v_cvt_pk_bf16_f32 v239, v248, v249
	ds_write_b128 v211, v[236:239] offset:0
	ds_read_b128 v[18:21], v233 offset:128
	ds_read_b128 v[22:25], v233 offset:144
	ds_read_b128 v[26:29], v233 offset:160
	ds_read_b128 v[30:33], v233 offset:176
	v_exp_f32_e32 v212, v36
	v_exp_f32_e32 v213, v40
	v_exp_f32_e32 v214, v44
	v_exp_f32_e32 v215, v48
	s_waitcnt lgkmcnt(4)
	s_barrier
	ds_read_b128 v[134:137], v210 offset:1024
	v_exp_f32_e32 v216, v34
	v_fma_f32 v251, v212, s12, s12
	v_exp_f32_e32 v217, v38
	v_fma_f32 v252, v213, s12, s12
	v_exp_f32_e32 v218, v42
	v_fma_f32 v253, v214, s12, s12
	v_exp_f32_e32 v219, v46
	v_fma_f32 v254, v215, s12, s12
	ds_read_b128 v[138:141], v210 offset:2048
	ds_read_b128 v[142:145], v210 offset:3072
	v_fmac_f32_e32 v251, v216, v251
	v_fmac_f32_e32 v252, v217, v252
	v_fmac_f32_e32 v253, v218, v253
	v_fmac_f32_e32 v254, v219, v254
	ds_read_b128 v[146:149], v210 offset:4096
	ds_read_b128 v[150:153], v210 offset:5120
	v_rcp_f32_e32 v216, v251
	v_rcp_f32_e32 v217, v252
	v_rcp_f32_e32 v218, v253
	v_rcp_f32_e32 v219, v254
	ds_read_b128 v[154:157], v210 offset:6144
	ds_read_b128 v[158:161], v210 offset:7168
	v_exp_f32_e32 v246, v37
	v_fma_f32 v202, -v212, v216, v216
	v_exp_f32_e32 v247, v41
	v_fma_f32 v203, -v213, v217, v217
	v_exp_f32_e32 v248, v45
	v_fma_f32 v204, -v214, v218, v218
	v_exp_f32_e32 v249, v49
	v_fma_f32 v205, -v215, v219, v219
	v_exp_f32_e32 v212, v202
	v_add_f32_e32 v246, 1.0, v246
	v_exp_f32_e32 v213, v203
	v_add_f32_e32 v247, 1.0, v247
	v_exp_f32_e32 v214, v204
	v_add_f32_e32 v248, 1.0, v248
	v_exp_f32_e32 v215, v205
	v_add_f32_e32 v249, 1.0, v249
	v_fmac_f32_e32 v246, v246, v212
	v_fmac_f32_e32 v247, v247, v213
	v_fmac_f32_e32 v248, v248, v214
	v_fmac_f32_e32 v249, v249, v215
	v_rcp_f32_e32 v246, v246
	v_rcp_f32_e32 v247, v247
	v_rcp_f32_e32 v248, v248
	v_rcp_f32_e32 v249, v249
	v_fma_f32 v246, -v212, v246, v246
	v_fma_f32 v247, -v213, v247, v247
	v_fma_f32 v248, -v214, v248, v248
	v_fma_f32 v249, -v215, v249, v249
	v_cvt_pk_bf16_f32 v224, v246, v247
	v_cvt_pk_bf16_f32 v225, v248, v249
	s_waitcnt lgkmcnt(0)
	v_mfma_f32_32x32x16_bf16 v[2:17], v[126:129], v[236:239], v[2:17]
	v_add_u32_e32 v234, v231, v245
	ds_read_b128 v[34:37], v234 offset:0
	ds_read_b128 v[38:41], v234 offset:16
	ds_read_b128 v[42:45], v234 offset:32
	ds_read_b128 v[46:49], v234 offset:48
	v_add_u32_e32 v232, 0x100, v232
	v_exp_f32_e32 v212, v84
	v_exp_f32_e32 v213, v88
	v_exp_f32_e32 v214, v92
	v_exp_f32_e32 v215, v96
	v_mfma_f32_32x32x16_bf16 v[2:17], v[122:125], v[134:137], v[2:17]
	v_exp_f32_e32 v216, v82
	v_fma_f32 v251, v212, s12, s12
	v_exp_f32_e32 v217, v86
	v_fma_f32 v252, v213, s12, s12
	v_exp_f32_e32 v218, v90
	v_fma_f32 v253, v214, s12, s12
	v_exp_f32_e32 v219, v94
	v_fma_f32 v254, v215, s12, s12
	v_mfma_f32_32x32x16_bf16 v[2:17], v[118:121], v[138:141], v[2:17]
	v_fmac_f32_e32 v251, v216, v251
	v_fmac_f32_e32 v252, v217, v252
	v_fmac_f32_e32 v253, v218, v253
	v_fmac_f32_e32 v254, v219, v254
	v_mfma_f32_32x32x16_bf16 v[2:17], v[114:117], v[142:145], v[2:17]
	v_rcp_f32_e32 v216, v251
	v_rcp_f32_e32 v217, v252
	v_rcp_f32_e32 v218, v253
	v_rcp_f32_e32 v219, v254
	v_mfma_f32_32x32x16_bf16 v[2:17], v[110:113], v[146:149], v[2:17]
	v_exp_f32_e32 v246, v85
	v_fma_f32 v206, -v212, v216, v216
	v_exp_f32_e32 v247, v89
	v_fma_f32 v207, -v213, v217, v217
	v_exp_f32_e32 v248, v93
	v_fma_f32 v208, -v214, v218, v218
	v_exp_f32_e32 v249, v97
	v_fma_f32 v209, -v215, v219, v219
	v_mfma_f32_32x32x16_bf16 v[2:17], v[106:109], v[150:153], v[2:17]
	v_mfma_f32_32x32x16_bf16 v[2:17], v[102:105], v[154:157], v[2:17]
	v_exp_f32_e32 v212, v206
	v_add_f32_e32 v246, 1.0, v246
	v_exp_f32_e32 v213, v207
	v_add_f32_e32 v247, 1.0, v247
	v_exp_f32_e32 v214, v208
	v_add_f32_e32 v248, 1.0, v248
	v_exp_f32_e32 v215, v209
	v_add_f32_e32 v249, 1.0, v249
	v_fmac_f32_e32 v246, v246, v212
	v_fmac_f32_e32 v247, v247, v213
	v_fmac_f32_e32 v248, v248, v214
	v_fmac_f32_e32 v249, v249, v215
	v_mfma_f32_32x32x16_bf16 v[2:17], v[98:101], v[158:161], v[2:17]
	v_rcp_f32_e32 v246, v246
	v_rcp_f32_e32 v247, v247
	v_rcp_f32_e32 v248, v248
	v_rcp_f32_e32 v249, v249
	v_fma_f32 v246, -v212, v246, v246
	v_fma_f32 v247, -v213, v247, v247
	v_fma_f32 v248, -v214, v248, v248
	v_fma_f32 v249, -v215, v249, v249
	v_cvt_pk_bf16_f32 v226, v246, v247
	v_cvt_pk_bf16_f32 v227, v248, v249
	ds_write_b128 v211, v[224:227] offset:8192
	.p2align 6
.Llight_loop_w0:
	v_mfma_f32_32x32x16_bf16 v[18:33], v[78:81], v[236:239], v[18:33]
	ds_read_b128 v[82:85], v234 offset:128
	ds_read_b128 v[86:89], v234 offset:144
	ds_read_b128 v[90:93], v234 offset:160
	ds_read_b128 v[94:97], v234 offset:176
	ds_read2_b32 v[244:245], v232 offset1:32
	v_exp_f32_e32 v212, v4
	v_exp_f32_e32 v213, v8
	v_exp_f32_e32 v214, v12
	v_exp_f32_e32 v215, v16
	s_waitcnt lgkmcnt(5)
	s_barrier
	v_mfma_f32_32x32x16_bf16 v[18:33], v[74:77], v[134:137], v[18:33]
	ds_read_b128 v[166:169], v210 offset:9216
	v_exp_f32_e32 v216, v2
	v_fma_f32 v251, v212, s12, s12
	v_exp_f32_e32 v217, v6
	v_fma_f32 v252, v213, s12, s12
	v_exp_f32_e32 v218, v10
	v_fma_f32 v253, v214, s12, s12
	v_exp_f32_e32 v219, v14
	v_fma_f32 v254, v215, s12, s12
	v_mfma_f32_32x32x16_bf16 v[18:33], v[70:73], v[138:141], v[18:33]
	ds_read_b128 v[170:173], v210 offset:10240
	ds_read_b128 v[174:177], v210 offset:11264
	v_exp_f32_e32 v220, v3
	v_fmac_f32_e32 v251, v216, v251
	v_exp_f32_e32 v221, v7
	v_fmac_f32_e32 v252, v217, v252
	v_exp_f32_e32 v222, v11
	v_fmac_f32_e32 v253, v218, v253
	v_exp_f32_e32 v223, v15
	v_fmac_f32_e32 v254, v219, v254
	v_mfma_f32_32x32x16_bf16 v[18:33], v[66:69], v[142:145], v[18:33]
	ds_read_b128 v[178:181], v210 offset:12288
	ds_read_b128 v[182:185], v210 offset:13312
	v_rcp_f32_e32 v216, v251
	v_add_f32_e32 v220, 1.0, v220
	v_rcp_f32_e32 v217, v252
	v_add_f32_e32 v221, 1.0, v221
	v_rcp_f32_e32 v218, v253
	v_add_f32_e32 v222, 1.0, v222
	v_rcp_f32_e32 v219, v254
	v_add_f32_e32 v223, 1.0, v223
	v_mfma_f32_32x32x16_bf16 v[18:33], v[62:65], v[146:149], v[18:33]
	ds_read_b128 v[186:189], v210 offset:14336
	ds_read_b128 v[190:193], v210 offset:15360
	v_rcp_f32_e32 v220, v220
	v_fma_f32 v240, -v212, v216, v216
	v_rcp_f32_e32 v221, v221
	v_fma_f32 v241, -v213, v217, v217
	v_rcp_f32_e32 v222, v222
	v_fma_f32 v242, -v214, v218, v218
	v_rcp_f32_e32 v223, v223
	v_fma_f32 v243, -v215, v219, v219
	v_mfma_f32_32x32x16_bf16 v[18:33], v[58:61], v[150:153], v[18:33]
	v_exp_f32_e32 v246, v5
	v_fma_f32 v194, v220, v194, v240
	v_exp_f32_e32 v247, v9
	v_fma_f32 v195, v221, v195, v241
	v_exp_f32_e32 v248, v13
	v_fma_f32 v196, v222, v196, v242
	v_exp_f32_e32 v249, v17
	v_fma_f32 v197, v223, v197, v243
	v_mfma_f32_32x32x16_bf16 v[18:33], v[54:57], v[154:157], v[18:33]
	v_exp_f32_e32 v212, v194
	v_add_f32_e32 v246, 1.0, v246
	v_exp_f32_e32 v213, v195
	v_add_f32_e32 v247, 1.0, v247
	v_exp_f32_e32 v214, v196
	v_add_f32_e32 v248, 1.0, v248
	v_exp_f32_e32 v215, v197
	v_add_f32_e32 v249, 1.0, v249
	v_fmac_f32_e32 v246, v246, v212
	v_fmac_f32_e32 v247, v247, v213
	v_fmac_f32_e32 v248, v248, v214
	v_fmac_f32_e32 v249, v249, v215
	v_mfma_f32_32x32x16_bf16 v[18:33], v[50:53], v[158:161], v[18:33]
	v_rcp_f32_e32 v246, v246
	v_rcp_f32_e32 v247, v247
	v_rcp_f32_e32 v248, v248
	v_rcp_f32_e32 v249, v249
	v_fma_f32 v246, -v212, v246, v246
	v_fma_f32 v247, -v213, v247, v247
	v_fma_f32 v248, -v214, v248, v248
	v_fma_f32 v249, -v215, v249, v249
	v_cvt_pk_bf16_f32 v236, v246, v247
	v_cvt_pk_bf16_f32 v237, v248, v249
	s_waitcnt lgkmcnt(0)
	v_mfma_f32_32x32x16_bf16 v[34:49], v[126:129], v[224:227], v[34:49]
	v_add_u32_e32 v233, v231, v244
	ds_read_b128 v[2:5], v233 offset:0
	ds_read_b128 v[6:9], v233 offset:16
	ds_read_b128 v[10:13], v233 offset:32
	ds_read_b128 v[14:17], v233 offset:48
	v_exp_f32_e32 v212, v20
	v_exp_f32_e32 v213, v24
	v_exp_f32_e32 v214, v28
	v_exp_f32_e32 v215, v32
	v_mfma_f32_32x32x16_bf16 v[34:49], v[122:125], v[166:169], v[34:49]
	v_exp_f32_e32 v216, v18
	v_fma_f32 v251, v212, s12, s12
	v_exp_f32_e32 v217, v22
	v_fma_f32 v252, v213, s12, s12
	v_exp_f32_e32 v218, v26
	v_fma_f32 v253, v214, s12, s12
	v_exp_f32_e32 v219, v30
	v_fma_f32 v254, v215, s12, s12
	v_mfma_f32_32x32x16_bf16 v[34:49], v[118:121], v[170:173], v[34:49]
	v_exp_f32_e32 v220, v19
	v_fmac_f32_e32 v251, v216, v251
	v_exp_f32_e32 v221, v23
	v_fmac_f32_e32 v252, v217, v252
	v_exp_f32_e32 v222, v27
	v_fmac_f32_e32 v253, v218, v253
	v_exp_f32_e32 v223, v31
	v_fmac_f32_e32 v254, v219, v254
	v_mfma_f32_32x32x16_bf16 v[34:49], v[114:117], v[174:177], v[34:49]
	v_rcp_f32_e32 v216, v251
	v_add_f32_e32 v220, 1.0, v220
	v_rcp_f32_e32 v217, v252
	v_add_f32_e32 v221, 1.0, v221
	v_rcp_f32_e32 v218, v253
	v_add_f32_e32 v222, 1.0, v222
	v_rcp_f32_e32 v219, v254
	v_add_f32_e32 v223, 1.0, v223
	v_mfma_f32_32x32x16_bf16 v[34:49], v[110:113], v[178:181], v[34:49]
	v_rcp_f32_e32 v220, v220
	v_fma_f32 v240, -v212, v216, v216
	v_rcp_f32_e32 v221, v221
	v_fma_f32 v241, -v213, v217, v217
	v_rcp_f32_e32 v222, v222
	v_fma_f32 v242, -v214, v218, v218
	v_rcp_f32_e32 v223, v223
	v_fma_f32 v243, -v215, v219, v219
	v_mfma_f32_32x32x16_bf16 v[34:49], v[106:109], v[182:185], v[34:49]
	v_exp_f32_e32 v246, v21
	v_fma_f32 v198, v220, v198, v240
	v_exp_f32_e32 v247, v25
	v_fma_f32 v199, v221, v199, v241
	v_exp_f32_e32 v248, v29
	v_fma_f32 v200, v222, v200, v242
	v_exp_f32_e32 v249, v33
	v_fma_f32 v201, v223, v201, v243
	v_mfma_f32_32x32x16_bf16 v[34:49], v[102:105], v[186:189], v[34:49]
	v_exp_f32_e32 v212, v198
	v_add_f32_e32 v246, 1.0, v246
	v_exp_f32_e32 v213, v199
	v_add_f32_e32 v247, 1.0, v247
	v_exp_f32_e32 v214, v200
	v_add_f32_e32 v248, 1.0, v248
	v_exp_f32_e32 v215, v201
	v_add_f32_e32 v249, 1.0, v249
	v_fmac_f32_e32 v246, v246, v212
	v_fmac_f32_e32 v247, v247, v213
	v_fmac_f32_e32 v248, v248, v214
	v_fmac_f32_e32 v249, v249, v215
	v_mfma_f32_32x32x16_bf16 v[34:49], v[98:101], v[190:193], v[34:49]
	v_rcp_f32_e32 v246, v246
	v_rcp_f32_e32 v247, v247
	v_rcp_f32_e32 v248, v248
	v_rcp_f32_e32 v249, v249
	v_fma_f32 v246, -v212, v246, v246
	v_fma_f32 v247, -v213, v247, v247
	v_fma_f32 v248, -v214, v248, v248
	v_fma_f32 v249, -v215, v249, v249
	v_cvt_pk_bf16_f32 v238, v246, v247
	v_cvt_pk_bf16_f32 v239, v248, v249
	ds_write_b128 v211, v[236:239] offset:0
	v_mfma_f32_32x32x16_bf16 v[82:97], v[78:81], v[224:227], v[82:97]
	ds_read_b128 v[18:21], v233 offset:128
	ds_read_b128 v[22:25], v233 offset:144
	ds_read_b128 v[26:29], v233 offset:160
	ds_read_b128 v[30:33], v233 offset:176
	v_exp_f32_e32 v212, v36
	v_exp_f32_e32 v213, v40
	v_exp_f32_e32 v214, v44
	v_exp_f32_e32 v215, v48
	s_waitcnt lgkmcnt(4)
	s_barrier
	v_mfma_f32_32x32x16_bf16 v[82:97], v[74:77], v[166:169], v[82:97]
	ds_read_b128 v[134:137], v210 offset:1024
	v_exp_f32_e32 v216, v34
	v_fma_f32 v251, v212, s12, s12
	v_exp_f32_e32 v217, v38
	v_fma_f32 v252, v213, s12, s12
	v_exp_f32_e32 v218, v42
	v_fma_f32 v253, v214, s12, s12
	v_exp_f32_e32 v219, v46
	v_fma_f32 v254, v215, s12, s12
	v_mfma_f32_32x32x16_bf16 v[82:97], v[70:73], v[170:173], v[82:97]
	ds_read_b128 v[138:141], v210 offset:2048
	ds_read_b128 v[142:145], v210 offset:3072
	v_exp_f32_e32 v220, v35
	v_fmac_f32_e32 v251, v216, v251
	v_exp_f32_e32 v221, v39
	v_fmac_f32_e32 v252, v217, v252
	v_exp_f32_e32 v222, v43
	v_fmac_f32_e32 v253, v218, v253
	v_exp_f32_e32 v223, v47
	v_fmac_f32_e32 v254, v219, v254
	v_mfma_f32_32x32x16_bf16 v[82:97], v[66:69], v[174:177], v[82:97]
	ds_read_b128 v[146:149], v210 offset:4096
	ds_read_b128 v[150:153], v210 offset:5120
	v_rcp_f32_e32 v216, v251
	v_add_f32_e32 v220, 1.0, v220
	v_rcp_f32_e32 v217, v252
	v_add_f32_e32 v221, 1.0, v221
	v_rcp_f32_e32 v218, v253
	v_add_f32_e32 v222, 1.0, v222
	v_rcp_f32_e32 v219, v254
	v_add_f32_e32 v223, 1.0, v223
	v_mfma_f32_32x32x16_bf16 v[82:97], v[62:65], v[178:181], v[82:97]
	ds_read_b128 v[154:157], v210 offset:6144
	ds_read_b128 v[158:161], v210 offset:7168
	v_rcp_f32_e32 v220, v220
	v_fma_f32 v240, -v212, v216, v216
	v_rcp_f32_e32 v221, v221
	v_fma_f32 v241, -v213, v217, v217
	v_rcp_f32_e32 v222, v222
	v_fma_f32 v242, -v214, v218, v218
	v_rcp_f32_e32 v223, v223
	v_fma_f32 v243, -v215, v219, v219
	v_mfma_f32_32x32x16_bf16 v[82:97], v[58:61], v[182:185], v[82:97]
	v_exp_f32_e32 v246, v37
	v_fma_f32 v202, v220, v202, v240
	v_exp_f32_e32 v247, v41
	v_fma_f32 v203, v221, v203, v241
	v_exp_f32_e32 v248, v45
	v_fma_f32 v204, v222, v204, v242
	v_exp_f32_e32 v249, v49
	v_fma_f32 v205, v223, v205, v243
	v_mfma_f32_32x32x16_bf16 v[82:97], v[54:57], v[186:189], v[82:97]
	v_exp_f32_e32 v212, v202
	v_add_f32_e32 v246, 1.0, v246
	v_exp_f32_e32 v213, v203
	v_add_f32_e32 v247, 1.0, v247
	v_exp_f32_e32 v214, v204
	v_add_f32_e32 v248, 1.0, v248
	v_exp_f32_e32 v215, v205
	v_add_f32_e32 v249, 1.0, v249
	v_fmac_f32_e32 v246, v246, v212
	v_fmac_f32_e32 v247, v247, v213
	v_fmac_f32_e32 v248, v248, v214
	v_fmac_f32_e32 v249, v249, v215
	v_mfma_f32_32x32x16_bf16 v[82:97], v[50:53], v[190:193], v[82:97]
	v_rcp_f32_e32 v246, v246
	v_rcp_f32_e32 v247, v247
	v_rcp_f32_e32 v248, v248
	v_rcp_f32_e32 v249, v249
	v_fma_f32 v246, -v212, v246, v246
	v_fma_f32 v247, -v213, v247, v247
	v_fma_f32 v248, -v214, v248, v248
	v_fma_f32 v249, -v215, v249, v249
	v_cvt_pk_bf16_f32 v224, v246, v247
	v_cvt_pk_bf16_f32 v225, v248, v249
	s_waitcnt lgkmcnt(0)
	v_mfma_f32_32x32x16_bf16 v[2:17], v[126:129], v[236:239], v[2:17]
	v_add_u32_e32 v234, v231, v245
	ds_read_b128 v[34:37], v234 offset:0
	ds_read_b128 v[38:41], v234 offset:16
	ds_read_b128 v[42:45], v234 offset:32
	ds_read_b128 v[46:49], v234 offset:48
	v_add_u32_e32 v232, 0x100, v232
	v_exp_f32_e32 v212, v84
	v_exp_f32_e32 v213, v88
	v_exp_f32_e32 v214, v92
	v_exp_f32_e32 v215, v96
	v_mfma_f32_32x32x16_bf16 v[2:17], v[122:125], v[134:137], v[2:17]
	v_exp_f32_e32 v216, v82
	v_fma_f32 v251, v212, s12, s12
	v_exp_f32_e32 v217, v86
	v_fma_f32 v252, v213, s12, s12
	v_exp_f32_e32 v218, v90
	v_fma_f32 v253, v214, s12, s12
	v_exp_f32_e32 v219, v94
	v_fma_f32 v254, v215, s12, s12
	v_mfma_f32_32x32x16_bf16 v[2:17], v[118:121], v[138:141], v[2:17]
	v_exp_f32_e32 v220, v83
	v_fmac_f32_e32 v251, v216, v251
	v_exp_f32_e32 v221, v87
	v_fmac_f32_e32 v252, v217, v252
	v_exp_f32_e32 v222, v91
	v_fmac_f32_e32 v253, v218, v253
	v_exp_f32_e32 v223, v95
	v_fmac_f32_e32 v254, v219, v254
	v_mfma_f32_32x32x16_bf16 v[2:17], v[114:117], v[142:145], v[2:17]
	v_rcp_f32_e32 v216, v251
	v_add_f32_e32 v220, 1.0, v220
	v_rcp_f32_e32 v217, v252
	v_add_f32_e32 v221, 1.0, v221
	v_rcp_f32_e32 v218, v253
	v_add_f32_e32 v222, 1.0, v222
	v_rcp_f32_e32 v219, v254
	v_add_f32_e32 v223, 1.0, v223
	v_mfma_f32_32x32x16_bf16 v[2:17], v[110:113], v[146:149], v[2:17]
	v_rcp_f32_e32 v220, v220
	v_fma_f32 v240, -v212, v216, v216
	v_rcp_f32_e32 v221, v221
	v_fma_f32 v241, -v213, v217, v217
	v_rcp_f32_e32 v222, v222
	v_fma_f32 v242, -v214, v218, v218
	v_rcp_f32_e32 v223, v223
	v_fma_f32 v243, -v215, v219, v219
	v_mfma_f32_32x32x16_bf16 v[2:17], v[106:109], v[150:153], v[2:17]
	v_exp_f32_e32 v246, v85
	v_fma_f32 v206, v220, v206, v240
	v_exp_f32_e32 v247, v89
	v_fma_f32 v207, v221, v207, v241
	v_exp_f32_e32 v248, v93
	v_fma_f32 v208, v222, v208, v242
	v_exp_f32_e32 v249, v97
	v_fma_f32 v209, v223, v209, v243
	v_mfma_f32_32x32x16_bf16 v[2:17], v[102:105], v[154:157], v[2:17]
	v_exp_f32_e32 v212, v206
	v_add_f32_e32 v246, 1.0, v246
	v_exp_f32_e32 v213, v207
	v_add_f32_e32 v247, 1.0, v247
	v_exp_f32_e32 v214, v208
	v_add_f32_e32 v248, 1.0, v248
	v_exp_f32_e32 v215, v209
	v_add_f32_e32 v249, 1.0, v249
	v_fmac_f32_e32 v246, v246, v212
	v_fmac_f32_e32 v247, v247, v213
	v_fmac_f32_e32 v248, v248, v214
	v_fmac_f32_e32 v249, v249, v215
	v_mfma_f32_32x32x16_bf16 v[2:17], v[98:101], v[158:161], v[2:17]
	v_rcp_f32_e32 v246, v246
	v_rcp_f32_e32 v247, v247
	v_rcp_f32_e32 v248, v248
	v_rcp_f32_e32 v249, v249
	v_fma_f32 v246, -v212, v246, v246
	v_fma_f32 v247, -v213, v247, v247
	v_fma_f32 v248, -v214, v248, v248
	v_fma_f32 v249, -v215, v249, v249
	v_cvt_pk_bf16_f32 v226, v246, v247
	v_cvt_pk_bf16_f32 v227, v248, v249
	ds_write_b128 v211, v[224:227] offset:8192
	s_sub_u32 s16, s16, 1
	s_cmp_lg_u32 s16, 0
	s_cbranch_scc1 .Llight_loop_w0
	v_mfma_f32_32x32x16_bf16 v[18:33], v[78:81], v[236:239], v[18:33]
	ds_read_b128 v[82:85], v234 offset:128
	ds_read_b128 v[86:89], v234 offset:144
	ds_read_b128 v[90:93], v234 offset:160
	ds_read_b128 v[94:97], v234 offset:176
	v_exp_f32_e32 v212, v4
	v_exp_f32_e32 v213, v8
	v_exp_f32_e32 v214, v12
	v_exp_f32_e32 v215, v16
	s_waitcnt lgkmcnt(4)
	s_barrier
	v_mfma_f32_32x32x16_bf16 v[18:33], v[74:77], v[134:137], v[18:33]
	ds_read_b128 v[166:169], v210 offset:9216
	v_exp_f32_e32 v216, v2
	v_fma_f32 v251, v212, s12, s12
	v_exp_f32_e32 v217, v6
	v_fma_f32 v252, v213, s12, s12
	v_exp_f32_e32 v218, v10
	v_fma_f32 v253, v214, s12, s12
	v_exp_f32_e32 v219, v14
	v_fma_f32 v254, v215, s12, s12
	v_mfma_f32_32x32x16_bf16 v[18:33], v[70:73], v[138:141], v[18:33]
	ds_read_b128 v[170:173], v210 offset:10240
	ds_read_b128 v[174:177], v210 offset:11264
	v_exp_f32_e32 v220, v3
	v_fmac_f32_e32 v251, v216, v251
	v_exp_f32_e32 v221, v7
	v_fmac_f32_e32 v252, v217, v252
	v_exp_f32_e32 v222, v11
	v_fmac_f32_e32 v253, v218, v253
	v_exp_f32_e32 v223, v15
	v_fmac_f32_e32 v254, v219, v254
	v_mfma_f32_32x32x16_bf16 v[18:33], v[66:69], v[142:145], v[18:33]
	ds_read_b128 v[178:181], v210 offset:12288
	ds_read_b128 v[182:185], v210 offset:13312
	v_rcp_f32_e32 v216, v251
	v_add_f32_e32 v220, 1.0, v220
	v_rcp_f32_e32 v217, v252
	v_add_f32_e32 v221, 1.0, v221
	v_rcp_f32_e32 v218, v253
	v_add_f32_e32 v222, 1.0, v222
	v_rcp_f32_e32 v219, v254
	v_add_f32_e32 v223, 1.0, v223
	v_mfma_f32_32x32x16_bf16 v[18:33], v[62:65], v[146:149], v[18:33]
	ds_read_b128 v[186:189], v210 offset:14336
	ds_read_b128 v[190:193], v210 offset:15360
	v_rcp_f32_e32 v220, v220
	v_fma_f32 v240, -v212, v216, v216
	v_rcp_f32_e32 v221, v221
	v_fma_f32 v241, -v213, v217, v217
	v_rcp_f32_e32 v222, v222
	v_fma_f32 v242, -v214, v218, v218
	v_rcp_f32_e32 v223, v223
	v_fma_f32 v243, -v215, v219, v219
	v_mfma_f32_32x32x16_bf16 v[18:33], v[58:61], v[150:153], v[18:33]
	v_exp_f32_e32 v246, v5
	v_fma_f32 v194, v220, v194, v240
	v_exp_f32_e32 v247, v9
	v_fma_f32 v195, v221, v195, v241
	v_exp_f32_e32 v248, v13
	v_fma_f32 v196, v222, v196, v242
	v_exp_f32_e32 v249, v17
	v_fma_f32 v197, v223, v197, v243
	v_mfma_f32_32x32x16_bf16 v[18:33], v[54:57], v[154:157], v[18:33]
	v_exp_f32_e32 v212, v194
	v_add_f32_e32 v246, 1.0, v246
	v_exp_f32_e32 v213, v195
	v_add_f32_e32 v247, 1.0, v247
	v_exp_f32_e32 v214, v196
	v_add_f32_e32 v248, 1.0, v248
	v_exp_f32_e32 v215, v197
	v_add_f32_e32 v249, 1.0, v249
	v_fmac_f32_e32 v246, v246, v212
	v_fmac_f32_e32 v247, v247, v213
	v_fmac_f32_e32 v248, v248, v214
	v_fmac_f32_e32 v249, v249, v215
	v_mfma_f32_32x32x16_bf16 v[18:33], v[50:53], v[158:161], v[18:33]
	v_rcp_f32_e32 v246, v246
	v_rcp_f32_e32 v247, v247
	v_rcp_f32_e32 v248, v248
	v_rcp_f32_e32 v249, v249
	v_fma_f32 v246, -v212, v246, v246
	v_fma_f32 v247, -v213, v247, v247
	v_fma_f32 v248, -v214, v248, v248
	v_fma_f32 v249, -v215, v249, v249
	v_cvt_pk_bf16_f32 v236, v246, v247
	v_cvt_pk_bf16_f32 v237, v248, v249
	s_waitcnt lgkmcnt(0)
	v_mfma_f32_32x32x16_bf16 v[34:49], v[126:129], v[224:227], v[34:49]
	v_exp_f32_e32 v212, v20
	v_exp_f32_e32 v213, v24
	v_exp_f32_e32 v214, v28
	v_exp_f32_e32 v215, v32
	v_mfma_f32_32x32x16_bf16 v[34:49], v[122:125], v[166:169], v[34:49]
	v_exp_f32_e32 v216, v18
	v_fma_f32 v251, v212, s12, s12
	v_exp_f32_e32 v217, v22
	v_fma_f32 v252, v213, s12, s12
	v_exp_f32_e32 v218, v26
	v_fma_f32 v253, v214, s12, s12
	v_exp_f32_e32 v219, v30
	v_fma_f32 v254, v215, s12, s12
	v_mfma_f32_32x32x16_bf16 v[34:49], v[118:121], v[170:173], v[34:49]
	v_exp_f32_e32 v220, v19
	v_fmac_f32_e32 v251, v216, v251
	v_exp_f32_e32 v221, v23
	v_fmac_f32_e32 v252, v217, v252
	v_exp_f32_e32 v222, v27
	v_fmac_f32_e32 v253, v218, v253
	v_exp_f32_e32 v223, v31
	v_fmac_f32_e32 v254, v219, v254
	v_mfma_f32_32x32x16_bf16 v[34:49], v[114:117], v[174:177], v[34:49]
	v_rcp_f32_e32 v216, v251
	v_add_f32_e32 v220, 1.0, v220
	v_rcp_f32_e32 v217, v252
	v_add_f32_e32 v221, 1.0, v221
	v_rcp_f32_e32 v218, v253
	v_add_f32_e32 v222, 1.0, v222
	v_rcp_f32_e32 v219, v254
	v_add_f32_e32 v223, 1.0, v223
	v_mfma_f32_32x32x16_bf16 v[34:49], v[110:113], v[178:181], v[34:49]
	v_rcp_f32_e32 v220, v220
	v_fma_f32 v240, -v212, v216, v216
	v_rcp_f32_e32 v221, v221
	v_fma_f32 v241, -v213, v217, v217
	v_rcp_f32_e32 v222, v222
	v_fma_f32 v242, -v214, v218, v218
	v_rcp_f32_e32 v223, v223
	v_fma_f32 v243, -v215, v219, v219
	v_mfma_f32_32x32x16_bf16 v[34:49], v[106:109], v[182:185], v[34:49]
	v_exp_f32_e32 v246, v21
	v_fma_f32 v198, v220, v198, v240
	v_exp_f32_e32 v247, v25
	v_fma_f32 v199, v221, v199, v241
	v_exp_f32_e32 v248, v29
	v_fma_f32 v200, v222, v200, v242
	v_exp_f32_e32 v249, v33
	v_fma_f32 v201, v223, v201, v243
	v_mfma_f32_32x32x16_bf16 v[34:49], v[102:105], v[186:189], v[34:49]
	v_exp_f32_e32 v212, v198
	v_add_f32_e32 v246, 1.0, v246
	v_exp_f32_e32 v213, v199
	v_add_f32_e32 v247, 1.0, v247
	v_exp_f32_e32 v214, v200
	v_add_f32_e32 v248, 1.0, v248
	v_exp_f32_e32 v215, v201
	v_add_f32_e32 v249, 1.0, v249
	v_fmac_f32_e32 v246, v246, v212
	v_fmac_f32_e32 v247, v247, v213
	v_fmac_f32_e32 v248, v248, v214
	v_fmac_f32_e32 v249, v249, v215
	v_mfma_f32_32x32x16_bf16 v[34:49], v[98:101], v[190:193], v[34:49]
	v_rcp_f32_e32 v246, v246
	v_rcp_f32_e32 v247, v247
	v_rcp_f32_e32 v248, v248
	v_rcp_f32_e32 v249, v249
	v_fma_f32 v246, -v212, v246, v246
	v_fma_f32 v247, -v213, v247, v247
	v_fma_f32 v248, -v214, v248, v248
	v_fma_f32 v249, -v215, v249, v249
	v_cvt_pk_bf16_f32 v238, v246, v247
	v_cvt_pk_bf16_f32 v239, v248, v249
	ds_write_b128 v211, v[236:239] offset:0
	s_waitcnt lgkmcnt(0)
	s_barrier
	s_bfe_u32 s20, s19, 0x10006
	s_lshl_b32 s21, s20, 7
	s_lshl_b32 s20, s20, 13
	s_add_u32 s20, s20, 0x30000
	s_add_u32 s22, s14, s20
	s_addc_u32 s23, s15, 0
	s_add_u32 s24, s22, 0x1000
	s_addc_u32 s25, s23, 0
	global_load_dwordx4 v[98:101], v210, s[22:23] offset:0
	global_load_dwordx4 v[102:105], v210, s[22:23] offset:1024
	global_load_dwordx4 v[106:109], v210, s[22:23] offset:2048
	global_load_dwordx4 v[110:113], v210, s[22:23] offset:3072
	global_load_dwordx4 v[114:117], v210, s[24:25] offset:0
	global_load_dwordx4 v[118:121], v210, s[24:25] offset:1024
	global_load_dwordx4 v[122:125], v210, s[24:25] offset:2048
	global_load_dwordx4 v[126:129], v210, s[24:25] offset:3072
	v_or_b32_e32 v250, s21, v230
	global_load_dwordx4 v[130:133], v250, s[4:5] offset:0
	global_load_dwordx4 v[134:137], v250, s[4:5] offset:32
	global_load_dwordx4 v[138:141], v250, s[4:5] offset:64
	global_load_dwordx4 v[142:145], v250, s[4:5] offset:96
	global_load_dwordx4 v[146:149], v250, s[6:7] offset:0
	global_load_dwordx4 v[150:153], v250, s[6:7] offset:32
	global_load_dwordx4 v[154:157], v250, s[6:7] offset:64
	global_load_dwordx4 v[158:161], v250, s[6:7] offset:96
	s_load_dword s26, s[8:9], 0x0
	v_mfma_f32_32x32x16_bf16 v[82:97], v[78:81], v[224:227], v[82:97]
	v_exp_f32_e32 v212, v36
	v_exp_f32_e32 v213, v40
	v_exp_f32_e32 v214, v44
	v_exp_f32_e32 v215, v48
	v_mfma_f32_32x32x16_bf16 v[82:97], v[74:77], v[166:169], v[82:97]
	v_exp_f32_e32 v216, v34
	v_fma_f32 v251, v212, s12, s12
	v_exp_f32_e32 v217, v38
	v_fma_f32 v252, v213, s12, s12
	v_exp_f32_e32 v218, v42
	v_fma_f32 v253, v214, s12, s12
	v_exp_f32_e32 v219, v46
	v_fma_f32 v254, v215, s12, s12
	v_mfma_f32_32x32x16_bf16 v[82:97], v[70:73], v[170:173], v[82:97]
	v_exp_f32_e32 v220, v35
	v_fmac_f32_e32 v251, v216, v251
	v_exp_f32_e32 v221, v39
	v_fmac_f32_e32 v252, v217, v252
	v_exp_f32_e32 v222, v43
	v_fmac_f32_e32 v253, v218, v253
	v_exp_f32_e32 v223, v47
	v_fmac_f32_e32 v254, v219, v254
	v_mfma_f32_32x32x16_bf16 v[82:97], v[66:69], v[174:177], v[82:97]
	v_rcp_f32_e32 v216, v251
	v_add_f32_e32 v220, 1.0, v220
	v_rcp_f32_e32 v217, v252
	v_add_f32_e32 v221, 1.0, v221
	v_rcp_f32_e32 v218, v253
	v_add_f32_e32 v222, 1.0, v222
	v_rcp_f32_e32 v219, v254
	v_add_f32_e32 v223, 1.0, v223
	v_mfma_f32_32x32x16_bf16 v[82:97], v[62:65], v[178:181], v[82:97]
	v_rcp_f32_e32 v220, v220
	v_fma_f32 v240, -v212, v216, v216
	v_rcp_f32_e32 v221, v221
	v_fma_f32 v241, -v213, v217, v217
	v_rcp_f32_e32 v222, v222
	v_fma_f32 v242, -v214, v218, v218
	v_rcp_f32_e32 v223, v223
	v_fma_f32 v243, -v215, v219, v219
	v_mfma_f32_32x32x16_bf16 v[82:97], v[58:61], v[182:185], v[82:97]
	v_exp_f32_e32 v246, v37
	v_fma_f32 v202, v220, v202, v240
	v_exp_f32_e32 v247, v41
	v_fma_f32 v203, v221, v203, v241
	v_exp_f32_e32 v248, v45
	v_fma_f32 v204, v222, v204, v242
	v_exp_f32_e32 v249, v49
	v_fma_f32 v205, v223, v205, v243
	v_mfma_f32_32x32x16_bf16 v[82:97], v[54:57], v[186:189], v[82:97]
	v_exp_f32_e32 v212, v202
	v_add_f32_e32 v246, 1.0, v246
	v_exp_f32_e32 v213, v203
	v_add_f32_e32 v247, 1.0, v247
	v_exp_f32_e32 v214, v204
	v_add_f32_e32 v248, 1.0, v248
	v_exp_f32_e32 v215, v205
	v_add_f32_e32 v249, 1.0, v249
	v_fmac_f32_e32 v246, v246, v212
	v_fmac_f32_e32 v247, v247, v213
	v_fmac_f32_e32 v248, v248, v214
	v_fmac_f32_e32 v249, v249, v215
	v_mfma_f32_32x32x16_bf16 v[82:97], v[50:53], v[190:193], v[82:97]
	v_rcp_f32_e32 v246, v246
	v_rcp_f32_e32 v247, v247
	v_rcp_f32_e32 v248, v248
	v_rcp_f32_e32 v249, v249
	v_fma_f32 v246, -v212, v246, v246
	v_fma_f32 v247, -v213, v247, v247
	v_fma_f32 v248, -v214, v248, v248
	v_fma_f32 v249, -v215, v249, v249
	v_cvt_pk_bf16_f32 v224, v246, v247
	v_cvt_pk_bf16_f32 v225, v248, v249
	s_waitcnt lgkmcnt(0)
	v_exp_f32_e32 v212, v84
	v_exp_f32_e32 v213, v88
	v_exp_f32_e32 v214, v92
	v_exp_f32_e32 v215, v96
	v_exp_f32_e32 v216, v82
	v_fma_f32 v251, v212, s12, s12
	v_exp_f32_e32 v217, v86
	v_fma_f32 v252, v213, s12, s12
	v_exp_f32_e32 v218, v90
	v_fma_f32 v253, v214, s12, s12
	v_exp_f32_e32 v219, v94
	v_fma_f32 v254, v215, s12, s12
	v_exp_f32_e32 v220, v83
	v_fmac_f32_e32 v251, v216, v251
	v_exp_f32_e32 v221, v87
	v_fmac_f32_e32 v252, v217, v252
	v_exp_f32_e32 v222, v91
	v_fmac_f32_e32 v253, v218, v253
	v_exp_f32_e32 v223, v95
	v_fmac_f32_e32 v254, v219, v254
	v_rcp_f32_e32 v216, v251
	v_add_f32_e32 v220, 1.0, v220
	v_rcp_f32_e32 v217, v252
	v_add_f32_e32 v221, 1.0, v221
	v_rcp_f32_e32 v218, v253
	v_add_f32_e32 v222, 1.0, v222
	v_rcp_f32_e32 v219, v254
	v_add_f32_e32 v223, 1.0, v223
	v_rcp_f32_e32 v220, v220
	v_fma_f32 v240, -v212, v216, v216
	v_rcp_f32_e32 v221, v221
	v_fma_f32 v241, -v213, v217, v217
	v_rcp_f32_e32 v222, v222
	v_fma_f32 v242, -v214, v218, v218
	v_rcp_f32_e32 v223, v223
	v_fma_f32 v243, -v215, v219, v219
	v_exp_f32_e32 v246, v85
	v_fma_f32 v206, v220, v206, v240
	v_exp_f32_e32 v247, v89
	v_fma_f32 v207, v221, v207, v241
	v_exp_f32_e32 v248, v93
	v_fma_f32 v208, v222, v208, v242
	v_exp_f32_e32 v249, v97
	v_fma_f32 v209, v223, v209, v243
	v_exp_f32_e32 v212, v206
	v_add_f32_e32 v246, 1.0, v246
	v_exp_f32_e32 v213, v207
	v_add_f32_e32 v247, 1.0, v247
	v_exp_f32_e32 v214, v208
	v_add_f32_e32 v248, 1.0, v248
	v_exp_f32_e32 v215, v209
	v_add_f32_e32 v249, 1.0, v249
	v_fmac_f32_e32 v246, v246, v212
	v_fmac_f32_e32 v247, v247, v213
	v_fmac_f32_e32 v248, v248, v214
	v_fmac_f32_e32 v249, v249, v215
	v_rcp_f32_e32 v246, v246
	v_rcp_f32_e32 v247, v247
	v_rcp_f32_e32 v248, v248
	v_rcp_f32_e32 v249, v249
	v_fma_f32 v246, -v212, v246, v246
	v_fma_f32 v247, -v213, v247, v247
	v_fma_f32 v248, -v214, v248, v248
	v_fma_f32 v249, -v215, v249, v249
	v_cvt_pk_bf16_f32 v226, v246, v247
	v_cvt_pk_bf16_f32 v227, v248, v249
	ds_write_b128 v211, v[224:227] offset:8192
	s_waitcnt lgkmcnt(0)
	s_barrier
	s_lshl_b32 s20, s19, 6
	s_and_b32 s20, s20, 0x2000
	v_or_b32_e32 v20, s20, v210
	ds_read_b128 v[162:165], v20 offset:0
	ds_read_b128 v[166:169], v20 offset:1024
	ds_read_b128 v[170:173], v20 offset:2048
	ds_read_b128 v[174:177], v20 offset:3072
	ds_read_b128 v[178:181], v20 offset:4096
	ds_read_b128 v[182:185], v20 offset:5120
	ds_read_b128 v[186:189], v20 offset:6144
	ds_read_b128 v[190:193], v20 offset:7168
	s_bfe_u32 s20, s19, 0x10006
	s_lshl_b32 s20, s20, 9
	s_and_b32 s21, s19, 0x80
	s_or_b32 s20, s20, s21
	v_lshlrev_b32_e32 v19, 2, v229
	v_add3_u32 v19, s20, v19, v228
	s_waitcnt vmcnt(0)
	s_waitcnt lgkmcnt(7)
	v_mfma_f32_32x32x16_bf16 v[2:17], v[98:101], v[162:165], 0
	s_waitcnt lgkmcnt(6)
	v_mfma_f32_32x32x16_bf16 v[2:17], v[102:105], v[166:169], v[2:17]
	s_waitcnt lgkmcnt(5)
	v_mfma_f32_32x32x16_bf16 v[2:17], v[106:109], v[170:173], v[2:17]
	s_waitcnt lgkmcnt(4)
	v_mfma_f32_32x32x16_bf16 v[2:17], v[110:113], v[174:177], v[2:17]
	s_waitcnt lgkmcnt(3)
	v_mfma_f32_32x32x16_bf16 v[2:17], v[114:117], v[178:181], v[2:17]
	s_waitcnt lgkmcnt(2)
	v_mfma_f32_32x32x16_bf16 v[2:17], v[118:121], v[182:185], v[2:17]
	s_waitcnt lgkmcnt(1)
	v_mfma_f32_32x32x16_bf16 v[2:17], v[122:125], v[186:189], v[2:17]
	s_waitcnt lgkmcnt(0)
	v_mfma_f32_32x32x16_bf16 v[2:17], v[126:129], v[190:193], v[2:17]
	s_nop 15
	s_nop 3
	v_add_f32_e32 v2, v2, v130
	v_add_f32_e32 v3, v3, v131
	v_add_f32_e32 v4, v4, v132
	v_add_f32_e32 v5, v5, v133
	v_add_f32_e32 v6, v6, v134
	v_add_f32_e32 v7, v7, v135
	v_add_f32_e32 v8, v8, v136
	v_add_f32_e32 v9, v9, v137
	v_add_f32_e32 v10, v10, v138
	v_add_f32_e32 v11, v11, v139
	v_add_f32_e32 v12, v12, v140
	v_add_f32_e32 v13, v13, v141
	v_add_f32_e32 v14, v14, v142
	v_add_f32_e32 v15, v15, v143
	v_add_f32_e32 v16, v16, v144
	v_add_f32_e32 v17, v17, v145
	v_max_f32_e32 v2, 0, v2
	v_max_f32_e32 v3, 0, v3
	v_max_f32_e32 v4, 0, v4
	v_max_f32_e32 v5, 0, v5
	v_max_f32_e32 v6, 0, v6
	v_max_f32_e32 v7, 0, v7
	v_max_f32_e32 v8, 0, v8
	v_max_f32_e32 v9, 0, v9
	v_max_f32_e32 v10, 0, v10
	v_max_f32_e32 v11, 0, v11
	v_max_f32_e32 v12, 0, v12
	v_max_f32_e32 v13, 0, v13
	v_max_f32_e32 v14, 0, v14
	v_max_f32_e32 v15, 0, v15
	v_max_f32_e32 v16, 0, v16
	v_max_f32_e32 v17, 0, v17
	v_fma_f32 v18, v2, v146, 0
	v_fmac_f32_e32 v18, v3, v147
	v_fmac_f32_e32 v18, v4, v148
	v_fmac_f32_e32 v18, v5, v149
	v_fmac_f32_e32 v18, v6, v150
	v_fmac_f32_e32 v18, v7, v151
	v_fmac_f32_e32 v18, v8, v152
	v_fmac_f32_e32 v18, v9, v153
	v_fmac_f32_e32 v18, v10, v154
	v_fmac_f32_e32 v18, v11, v155
	v_fmac_f32_e32 v18, v12, v156
	v_fmac_f32_e32 v18, v13, v157
	v_fmac_f32_e32 v18, v14, v158
	v_fmac_f32_e32 v18, v15, v159
	v_fmac_f32_e32 v18, v16, v160
	v_fmac_f32_e32 v18, v17, v161
	ds_write_b32 v19, v18 offset:35904
	s_branch .LBB1_40
.Llight_w1:
	ds_read_b128 v[82:85], v234 offset:128
	ds_read_b128 v[86:89], v234 offset:144
	ds_read_b128 v[90:93], v234 offset:160
	ds_read_b128 v[94:97], v234 offset:176
	ds_read2_b32 v[244:245], v232 offset1:32
	v_exp_f32_e32 v212, v4
	v_exp_f32_e32 v213, v8
	v_exp_f32_e32 v214, v12
	v_exp_f32_e32 v215, v16
	v_exp_f32_e32 v216, v2
	v_fma_f32 v251, v212, s12, s12
	v_exp_f32_e32 v217, v6
	v_fma_f32 v252, v213, s12, s12
	v_exp_f32_e32 v218, v10
	v_fma_f32 v253, v214, s12, s12
	v_exp_f32_e32 v219, v14
	v_fma_f32 v254, v215, s12, s12
	v_fmac_f32_e32 v251, v216, v251
	v_fmac_f32_e32 v252, v217, v252
	v_fmac_f32_e32 v253, v218, v253
	v_fmac_f32_e32 v254, v219, v254
	v_rcp_f32_e32 v216, v251
	v_rcp_f32_e32 v217, v252
	v_rcp_f32_e32 v218, v253
	v_rcp_f32_e32 v219, v254
	v_exp_f32_e32 v246, v5
	v_fma_f32 v194, -v212, v216, v216
	v_exp_f32_e32 v247, v9
	v_fma_f32 v195, -v213, v217, v217
	v_exp_f32_e32 v248, v13
	v_fma_f32 v196, -v214, v218, v218
	v_exp_f32_e32 v249, v17
	v_fma_f32 v197, -v215, v219, v219
	v_exp_f32_e32 v212, v194
	v_add_f32_e32 v246, 1.0, v246
	v_exp_f32_e32 v213, v195
	v_add_f32_e32 v247, 1.0, v247
	v_exp_f32_e32 v214, v196
	v_add_f32_e32 v248, 1.0, v248
	v_exp_f32_e32 v215, v197
	v_add_f32_e32 v249, 1.0, v249
	v_fmac_f32_e32 v246, v246, v212
	v_fmac_f32_e32 v247, v247, v213
	v_fmac_f32_e32 v248, v248, v214
	v_fmac_f32_e32 v249, v249, v215
	v_rcp_f32_e32 v246, v246
	v_rcp_f32_e32 v247, v247
	v_rcp_f32_e32 v248, v248
	v_rcp_f32_e32 v249, v249
	v_fma_f32 v246, -v212, v246, v246
	v_fma_f32 v247, -v213, v247, v247
	v_fma_f32 v248, -v214, v248, v248
	v_fma_f32 v249, -v215, v249, v249
	v_cvt_pk_bf16_f32 v236, v246, v247
	v_cvt_pk_bf16_f32 v237, v248, v249
	s_waitcnt lgkmcnt(0)
	v_add_u32_e32 v233, v231, v244
	ds_read_b128 v[2:5], v233 offset:0
	ds_read_b128 v[6:9], v233 offset:16
	ds_read_b128 v[10:13], v233 offset:32
	ds_read_b128 v[14:17], v233 offset:48
	v_exp_f32_e32 v212, v20
	v_exp_f32_e32 v213, v24
	v_exp_f32_e32 v214, v28
	v_exp_f32_e32 v215, v32
	v_exp_f32_e32 v216, v18
	v_fma_f32 v251, v212, s12, s12
	v_exp_f32_e32 v217, v22
	v_fma_f32 v252, v213, s12, s12
	v_exp_f32_e32 v218, v26
	v_fma_f32 v253, v214, s12, s12
	v_exp_f32_e32 v219, v30
	v_fma_f32 v254, v215, s12, s12
	v_fmac_f32_e32 v251, v216, v251
	v_fmac_f32_e32 v252, v217, v252
	v_fmac_f32_e32 v253, v218, v253
	v_fmac_f32_e32 v254, v219, v254
	v_rcp_f32_e32 v216, v251
	v_rcp_f32_e32 v217, v252
	v_rcp_f32_e32 v218, v253
	v_rcp_f32_e32 v219, v254
	v_exp_f32_e32 v246, v21
	v_fma_f32 v198, -v212, v216, v216
	v_exp_f32_e32 v247, v25
	v_fma_f32 v199, -v213, v217, v217
	v_exp_f32_e32 v248, v29
	v_fma_f32 v200, -v214, v218, v218
	v_exp_f32_e32 v249, v33
	v_fma_f32 v201, -v215, v219, v219
	v_exp_f32_e32 v212, v198
	v_add_f32_e32 v246, 1.0, v246
	v_exp_f32_e32 v213, v199
	v_add_f32_e32 v247, 1.0, v247
	v_exp_f32_e32 v214, v200
	v_add_f32_e32 v248, 1.0, v248
	v_exp_f32_e32 v215, v201
	v_add_f32_e32 v249, 1.0, v249
	v_fmac_f32_e32 v246, v246, v212
	v_fmac_f32_e32 v247, v247, v213
	v_fmac_f32_e32 v248, v248, v214
	v_fmac_f32_e32 v249, v249, v215
	v_rcp_f32_e32 v246, v246
	v_rcp_f32_e32 v247, v247
	v_rcp_f32_e32 v248, v248
	v_rcp_f32_e32 v249, v249
	v_fma_f32 v246, -v212, v246, v246
	v_fma_f32 v247, -v213, v247, v247
	v_fma_f32 v248, -v214, v248, v248
	v_fma_f32 v249, -v215, v249, v249
	v_cvt_pk_bf16_f32 v238, v246, v247
	v_cvt_pk_bf16_f32 v239, v248, v249
	ds_write_b128 v211, v[236:239] offset:0
	ds_read_b128 v[18:21], v233 offset:128
	ds_read_b128 v[22:25], v233 offset:144
	ds_read_b128 v[26:29], v233 offset:160
	ds_read_b128 v[30:33], v233 offset:176
	v_exp_f32_e32 v212, v36
	v_exp_f32_e32 v213, v40
	v_exp_f32_e32 v214, v44
	v_exp_f32_e32 v215, v48
	s_waitcnt lgkmcnt(4)
	s_barrier
	ds_read_b128 v[130:133], v210 offset:0
	v_exp_f32_e32 v216, v34
	v_fma_f32 v251, v212, s12, s12
	v_exp_f32_e32 v217, v38
	v_fma_f32 v252, v213, s12, s12
	v_exp_f32_e32 v218, v42
	v_fma_f32 v253, v214, s12, s12
	v_exp_f32_e32 v219, v46
	v_fma_f32 v254, v215, s12, s12
	ds_read_b128 v[138:141], v210 offset:2048
	ds_read_b128 v[142:145], v210 offset:3072
	v_fmac_f32_e32 v251, v216, v251
	v_fmac_f32_e32 v252, v217, v252
	v_fmac_f32_e32 v253, v218, v253
	v_fmac_f32_e32 v254, v219, v254
	ds_read_b128 v[146:149], v210 offset:4096
	ds_read_b128 v[150:153], v210 offset:5120
	v_rcp_f32_e32 v216, v251
	v_rcp_f32_e32 v217, v252
	v_rcp_f32_e32 v218, v253
	v_rcp_f32_e32 v219, v254
	ds_read_b128 v[154:157], v210 offset:6144
	ds_read_b128 v[158:161], v210 offset:7168
	v_exp_f32_e32 v246, v37
	v_fma_f32 v202, -v212, v216, v216
	v_exp_f32_e32 v247, v41
	v_fma_f32 v203, -v213, v217, v217
	v_exp_f32_e32 v248, v45
	v_fma_f32 v204, -v214, v218, v218
	v_exp_f32_e32 v249, v49
	v_fma_f32 v205, -v215, v219, v219
	v_exp_f32_e32 v212, v202
	v_add_f32_e32 v246, 1.0, v246
	v_exp_f32_e32 v213, v203
	v_add_f32_e32 v247, 1.0, v247
	v_exp_f32_e32 v214, v204
	v_add_f32_e32 v248, 1.0, v248
	v_exp_f32_e32 v215, v205
	v_add_f32_e32 v249, 1.0, v249
	v_fmac_f32_e32 v246, v246, v212
	v_fmac_f32_e32 v247, v247, v213
	v_fmac_f32_e32 v248, v248, v214
	v_fmac_f32_e32 v249, v249, v215
	v_rcp_f32_e32 v246, v246
	v_rcp_f32_e32 v247, v247
	v_rcp_f32_e32 v248, v248
	v_rcp_f32_e32 v249, v249
	v_fma_f32 v246, -v212, v246, v246
	v_fma_f32 v247, -v213, v247, v247
	v_fma_f32 v248, -v214, v248, v248
	v_fma_f32 v249, -v215, v249, v249
	v_cvt_pk_bf16_f32 v224, v246, v247
	v_cvt_pk_bf16_f32 v225, v248, v249
	s_waitcnt lgkmcnt(0)
	v_mfma_f32_32x32x16_bf16 v[2:17], v[126:129], v[130:133], v[2:17]
	v_add_u32_e32 v234, v231, v245
	ds_read_b128 v[34:37], v234 offset:0
	ds_read_b128 v[38:41], v234 offset:16
	ds_read_b128 v[42:45], v234 offset:32
	ds_read_b128 v[46:49], v234 offset:48
	v_add_u32_e32 v232, 0x100, v232
	v_exp_f32_e32 v212, v84
	v_exp_f32_e32 v213, v88
	v_exp_f32_e32 v214, v92
	v_exp_f32_e32 v215, v96
	v_mfma_f32_32x32x16_bf16 v[2:17], v[122:125], v[236:239], v[2:17]
	v_exp_f32_e32 v216, v82
	v_fma_f32 v251, v212, s12, s12
	v_exp_f32_e32 v217, v86
	v_fma_f32 v252, v213, s12, s12
	v_exp_f32_e32 v218, v90
	v_fma_f32 v253, v214, s12, s12
	v_exp_f32_e32 v219, v94
	v_fma_f32 v254, v215, s12, s12
	v_mfma_f32_32x32x16_bf16 v[2:17], v[118:121], v[138:141], v[2:17]
	v_fmac_f32_e32 v251, v216, v251
	v_fmac_f32_e32 v252, v217, v252
	v_fmac_f32_e32 v253, v218, v253
	v_fmac_f32_e32 v254, v219, v254
	v_mfma_f32_32x32x16_bf16 v[2:17], v[114:117], v[142:145], v[2:17]
	v_rcp_f32_e32 v216, v251
	v_rcp_f32_e32 v217, v252
	v_rcp_f32_e32 v218, v253
	v_rcp_f32_e32 v219, v254
	v_mfma_f32_32x32x16_bf16 v[2:17], v[110:113], v[146:149], v[2:17]
	v_exp_f32_e32 v246, v85
	v_fma_f32 v206, -v212, v216, v216
	v_exp_f32_e32 v247, v89
	v_fma_f32 v207, -v213, v217, v217
	v_exp_f32_e32 v248, v93
	v_fma_f32 v208, -v214, v218, v218
	v_exp_f32_e32 v249, v97
	v_fma_f32 v209, -v215, v219, v219
	v_mfma_f32_32x32x16_bf16 v[2:17], v[106:109], v[150:153], v[2:17]
	v_mfma_f32_32x32x16_bf16 v[2:17], v[102:105], v[154:157], v[2:17]
	v_exp_f32_e32 v212, v206
	v_add_f32_e32 v246, 1.0, v246
	v_exp_f32_e32 v213, v207
	v_add_f32_e32 v247, 1.0, v247
	v_exp_f32_e32 v214, v208
	v_add_f32_e32 v248, 1.0, v248
	v_exp_f32_e32 v215, v209
	v_add_f32_e32 v249, 1.0, v249
	v_fmac_f32_e32 v246, v246, v212
	v_fmac_f32_e32 v247, v247, v213
	v_fmac_f32_e32 v248, v248, v214
	v_fmac_f32_e32 v249, v249, v215
	v_mfma_f32_32x32x16_bf16 v[2:17], v[98:101], v[158:161], v[2:17]
	v_rcp_f32_e32 v246, v246
	v_rcp_f32_e32 v247, v247
	v_rcp_f32_e32 v248, v248
	v_rcp_f32_e32 v249, v249
	v_fma_f32 v246, -v212, v246, v246
	v_fma_f32 v247, -v213, v247, v247
	v_fma_f32 v248, -v214, v248, v248
	v_fma_f32 v249, -v215, v249, v249
	v_cvt_pk_bf16_f32 v226, v246, v247
	v_cvt_pk_bf16_f32 v227, v248, v249
	ds_write_b128 v211, v[224:227] offset:8192
	.p2align 6
.Llight_loop_w1:
	v_mfma_f32_32x32x16_bf16 v[18:33], v[78:81], v[130:133], v[18:33]
	ds_read_b128 v[82:85], v234 offset:128
	ds_read_b128 v[86:89], v234 offset:144
	ds_read_b128 v[90:93], v234 offset:160
	ds_read_b128 v[94:97], v234 offset:176
	ds_read2_b32 v[244:245], v232 offset1:32
	v_exp_f32_e32 v212, v4
	v_exp_f32_e32 v213, v8
	v_exp_f32_e32 v214, v12
	v_exp_f32_e32 v215, v16
	s_waitcnt lgkmcnt(5)
	s_barrier
	v_mfma_f32_32x32x16_bf16 v[18:33], v[74:77], v[236:239], v[18:33]
	ds_read_b128 v[162:165], v210 offset:8192
	v_exp_f32_e32 v216, v2
	v_fma_f32 v251, v212, s12, s12
	v_exp_f32_e32 v217, v6
	v_fma_f32 v252, v213, s12, s12
	v_exp_f32_e32 v218, v10
	v_fma_f32 v253, v214, s12, s12
	v_exp_f32_e32 v219, v14
	v_fma_f32 v254, v215, s12, s12
	v_mfma_f32_32x32x16_bf16 v[18:33], v[70:73], v[138:141], v[18:33]
	ds_read_b128 v[170:173], v210 offset:10240
	ds_read_b128 v[174:177], v210 offset:11264
	v_exp_f32_e32 v220, v3
	v_fmac_f32_e32 v251, v216, v251
	v_exp_f32_e32 v221, v7
	v_fmac_f32_e32 v252, v217, v252
	v_exp_f32_e32 v222, v11
	v_fmac_f32_e32 v253, v218, v253
	v_exp_f32_e32 v223, v15
	v_fmac_f32_e32 v254, v219, v254
	v_mfma_f32_32x32x16_bf16 v[18:33], v[66:69], v[142:145], v[18:33]
	ds_read_b128 v[178:181], v210 offset:12288
	ds_read_b128 v[182:185], v210 offset:13312
	v_rcp_f32_e32 v216, v251
	v_add_f32_e32 v220, 1.0, v220
	v_rcp_f32_e32 v217, v252
	v_add_f32_e32 v221, 1.0, v221
	v_rcp_f32_e32 v218, v253
	v_add_f32_e32 v222, 1.0, v222
	v_rcp_f32_e32 v219, v254
	v_add_f32_e32 v223, 1.0, v223
	v_mfma_f32_32x32x16_bf16 v[18:33], v[62:65], v[146:149], v[18:33]
	ds_read_b128 v[186:189], v210 offset:14336
	ds_read_b128 v[190:193], v210 offset:15360
	v_rcp_f32_e32 v220, v220
	v_fma_f32 v240, -v212, v216, v216
	v_rcp_f32_e32 v221, v221
	v_fma_f32 v241, -v213, v217, v217
	v_rcp_f32_e32 v222, v222
	v_fma_f32 v242, -v214, v218, v218
	v_rcp_f32_e32 v223, v223
	v_fma_f32 v243, -v215, v219, v219
	v_mfma_f32_32x32x16_bf16 v[18:33], v[58:61], v[150:153], v[18:33]
	v_exp_f32_e32 v246, v5
	v_fma_f32 v194, v220, v194, v240
	v_exp_f32_e32 v247, v9
	v_fma_f32 v195, v221, v195, v241
	v_exp_f32_e32 v248, v13
	v_fma_f32 v196, v222, v196, v242
	v_exp_f32_e32 v249, v17
	v_fma_f32 v197, v223, v197, v243
	v_mfma_f32_32x32x16_bf16 v[18:33], v[54:57], v[154:157], v[18:33]
	v_exp_f32_e32 v212, v194
	v_add_f32_e32 v246, 1.0, v246
	v_exp_f32_e32 v213, v195
	v_add_f32_e32 v247, 1.0, v247
	v_exp_f32_e32 v214, v196
	v_add_f32_e32 v248, 1.0, v248
	v_exp_f32_e32 v215, v197
	v_add_f32_e32 v249, 1.0, v249
	v_fmac_f32_e32 v246, v246, v212
	v_fmac_f32_e32 v247, v247, v213
	v_fmac_f32_e32 v248, v248, v214
	v_fmac_f32_e32 v249, v249, v215
	v_mfma_f32_32x32x16_bf16 v[18:33], v[50:53], v[158:161], v[18:33]
	v_rcp_f32_e32 v246, v246
	v_rcp_f32_e32 v247, v247
	v_rcp_f32_e32 v248, v248
	v_rcp_f32_e32 v249, v249
	v_fma_f32 v246, -v212, v246, v246
	v_fma_f32 v247, -v213, v247, v247
	v_fma_f32 v248, -v214, v248, v248
	v_fma_f32 v249, -v215, v249, v249
	v_cvt_pk_bf16_f32 v236, v246, v247
	v_cvt_pk_bf16_f32 v237, v248, v249
	s_waitcnt lgkmcnt(0)
	v_mfma_f32_32x32x16_bf16 v[34:49], v[126:129], v[162:165], v[34:49]
	v_add_u32_e32 v233, v231, v244
	ds_read_b128 v[2:5], v233 offset:0
	ds_read_b128 v[6:9], v233 offset:16
	ds_read_b128 v[10:13], v233 offset:32
	ds_read_b128 v[14:17], v233 offset:48
	v_exp_f32_e32 v212, v20
	v_exp_f32_e32 v213, v24
	v_exp_f32_e32 v214, v28
	v_exp_f32_e32 v215, v32
	v_mfma_f32_32x32x16_bf16 v[34:49], v[122:125], v[224:227], v[34:49]
	v_exp_f32_e32 v216, v18
	v_fma_f32 v251, v212, s12, s12
	v_exp_f32_e32 v217, v22
	v_fma_f32 v252, v213, s12, s12
	v_exp_f32_e32 v218, v26
	v_fma_f32 v253, v214, s12, s12
	v_exp_f32_e32 v219, v30
	v_fma_f32 v254, v215, s12, s12
	v_mfma_f32_32x32x16_bf16 v[34:49], v[118:121], v[170:173], v[34:49]
	v_exp_f32_e32 v220, v19
	v_fmac_f32_e32 v251, v216, v251
	v_exp_f32_e32 v221, v23
	v_fmac_f32_e32 v252, v217, v252
	v_exp_f32_e32 v222, v27
	v_fmac_f32_e32 v253, v218, v253
	v_exp_f32_e32 v223, v31
	v_fmac_f32_e32 v254, v219, v254
	v_mfma_f32_32x32x16_bf16 v[34:49], v[114:117], v[174:177], v[34:49]
	v_rcp_f32_e32 v216, v251
	v_add_f32_e32 v220, 1.0, v220
	v_rcp_f32_e32 v217, v252
	v_add_f32_e32 v221, 1.0, v221
	v_rcp_f32_e32 v218, v253
	v_add_f32_e32 v222, 1.0, v222
	v_rcp_f32_e32 v219, v254
	v_add_f32_e32 v223, 1.0, v223
	v_mfma_f32_32x32x16_bf16 v[34:49], v[110:113], v[178:181], v[34:49]
	v_rcp_f32_e32 v220, v220
	v_fma_f32 v240, -v212, v216, v216
	v_rcp_f32_e32 v221, v221
	v_fma_f32 v241, -v213, v217, v217
	v_rcp_f32_e32 v222, v222
	v_fma_f32 v242, -v214, v218, v218
	v_rcp_f32_e32 v223, v223
	v_fma_f32 v243, -v215, v219, v219
	v_mfma_f32_32x32x16_bf16 v[34:49], v[106:109], v[182:185], v[34:49]
	v_exp_f32_e32 v246, v21
	v_fma_f32 v198, v220, v198, v240
	v_exp_f32_e32 v247, v25
	v_fma_f32 v199, v221, v199, v241
	v_exp_f32_e32 v248, v29
	v_fma_f32 v200, v222, v200, v242
	v_exp_f32_e32 v249, v33
	v_fma_f32 v201, v223, v201, v243
	v_mfma_f32_32x32x16_bf16 v[34:49], v[102:105], v[186:189], v[34:49]
	v_exp_f32_e32 v212, v198
	v_add_f32_e32 v246, 1.0, v246
	v_exp_f32_e32 v213, v199
	v_add_f32_e32 v247, 1.0, v247
	v_exp_f32_e32 v214, v200
	v_add_f32_e32 v248, 1.0, v248
	v_exp_f32_e32 v215, v201
	v_add_f32_e32 v249, 1.0, v249
	v_fmac_f32_e32 v246, v246, v212
	v_fmac_f32_e32 v247, v247, v213
	v_fmac_f32_e32 v248, v248, v214
	v_fmac_f32_e32 v249, v249, v215
	v_mfma_f32_32x32x16_bf16 v[34:49], v[98:101], v[190:193], v[34:49]
	v_rcp_f32_e32 v246, v246
	v_rcp_f32_e32 v247, v247
	v_rcp_f32_e32 v248, v248
	v_rcp_f32_e32 v249, v249
	v_fma_f32 v246, -v212, v246, v246
	v_fma_f32 v247, -v213, v247, v247
	v_fma_f32 v248, -v214, v248, v248
	v_fma_f32 v249, -v215, v249, v249
	v_cvt_pk_bf16_f32 v238, v246, v247
	v_cvt_pk_bf16_f32 v239, v248, v249
	ds_write_b128 v211, v[236:239] offset:0
	v_mfma_f32_32x32x16_bf16 v[82:97], v[78:81], v[162:165], v[82:97]
	ds_read_b128 v[18:21], v233 offset:128
	ds_read_b128 v[22:25], v233 offset:144
	ds_read_b128 v[26:29], v233 offset:160
	ds_read_b128 v[30:33], v233 offset:176
	v_exp_f32_e32 v212, v36
	v_exp_f32_e32 v213, v40
	v_exp_f32_e32 v214, v44
	v_exp_f32_e32 v215, v48
	s_waitcnt lgkmcnt(4)
	s_barrier
	v_mfma_f32_32x32x16_bf16 v[82:97], v[74:77], v[224:227], v[82:97]
	ds_read_b128 v[130:133], v210 offset:0
	v_exp_f32_e32 v216, v34
	v_fma_f32 v251, v212, s12, s12
	v_exp_f32_e32 v217, v38
	v_fma_f32 v252, v213, s12, s12
	v_exp_f32_e32 v218, v42
	v_fma_f32 v253, v214, s12, s12
	v_exp_f32_e32 v219, v46
	v_fma_f32 v254, v215, s12, s12
	v_mfma_f32_32x32x16_bf16 v[82:97], v[70:73], v[170:173], v[82:97]
	ds_read_b128 v[138:141], v210 offset:2048
	ds_read_b128 v[142:145], v210 offset:3072
	v_exp_f32_e32 v220, v35
	v_fmac_f32_e32 v251, v216, v251
	v_exp_f32_e32 v221, v39
	v_fmac_f32_e32 v252, v217, v252
	v_exp_f32_e32 v222, v43
	v_fmac_f32_e32 v253, v218, v253
	v_exp_f32_e32 v223, v47
	v_fmac_f32_e32 v254, v219, v254
	v_mfma_f32_32x32x16_bf16 v[82:97], v[66:69], v[174:177], v[82:97]
	ds_read_b128 v[146:149], v210 offset:4096
	ds_read_b128 v[150:153], v210 offset:5120
	v_rcp_f32_e32 v216, v251
	v_add_f32_e32 v220, 1.0, v220
	v_rcp_f32_e32 v217, v252
	v_add_f32_e32 v221, 1.0, v221
	v_rcp_f32_e32 v218, v253
	v_add_f32_e32 v222, 1.0, v222
	v_rcp_f32_e32 v219, v254
	v_add_f32_e32 v223, 1.0, v223
	v_mfma_f32_32x32x16_bf16 v[82:97], v[62:65], v[178:181], v[82:97]
	ds_read_b128 v[154:157], v210 offset:6144
	ds_read_b128 v[158:161], v210 offset:7168
	v_rcp_f32_e32 v220, v220
	v_fma_f32 v240, -v212, v216, v216
	v_rcp_f32_e32 v221, v221
	v_fma_f32 v241, -v213, v217, v217
	v_rcp_f32_e32 v222, v222
	v_fma_f32 v242, -v214, v218, v218
	v_rcp_f32_e32 v223, v223
	v_fma_f32 v243, -v215, v219, v219
	v_mfma_f32_32x32x16_bf16 v[82:97], v[58:61], v[182:185], v[82:97]
	v_exp_f32_e32 v246, v37
	v_fma_f32 v202, v220, v202, v240
	v_exp_f32_e32 v247, v41
	v_fma_f32 v203, v221, v203, v241
	v_exp_f32_e32 v248, v45
	v_fma_f32 v204, v222, v204, v242
	v_exp_f32_e32 v249, v49
	v_fma_f32 v205, v223, v205, v243
	v_mfma_f32_32x32x16_bf16 v[82:97], v[54:57], v[186:189], v[82:97]
	v_exp_f32_e32 v212, v202
	v_add_f32_e32 v246, 1.0, v246
	v_exp_f32_e32 v213, v203
	v_add_f32_e32 v247, 1.0, v247
	v_exp_f32_e32 v214, v204
	v_add_f32_e32 v248, 1.0, v248
	v_exp_f32_e32 v215, v205
	v_add_f32_e32 v249, 1.0, v249
	v_fmac_f32_e32 v246, v246, v212
	v_fmac_f32_e32 v247, v247, v213
	v_fmac_f32_e32 v248, v248, v214
	v_fmac_f32_e32 v249, v249, v215
	v_mfma_f32_32x32x16_bf16 v[82:97], v[50:53], v[190:193], v[82:97]
	v_rcp_f32_e32 v246, v246
	v_rcp_f32_e32 v247, v247
	v_rcp_f32_e32 v248, v248
	v_rcp_f32_e32 v249, v249
	v_fma_f32 v246, -v212, v246, v246
	v_fma_f32 v247, -v213, v247, v247
	v_fma_f32 v248, -v214, v248, v248
	v_fma_f32 v249, -v215, v249, v249
	v_cvt_pk_bf16_f32 v224, v246, v247
	v_cvt_pk_bf16_f32 v225, v248, v249
	s_waitcnt lgkmcnt(0)
	v_mfma_f32_32x32x16_bf16 v[2:17], v[126:129], v[130:133], v[2:17]
	v_add_u32_e32 v234, v231, v245
	ds_read_b128 v[34:37], v234 offset:0
	ds_read_b128 v[38:41], v234 offset:16
	ds_read_b128 v[42:45], v234 offset:32
	ds_read_b128 v[46:49], v234 offset:48
	v_add_u32_e32 v232, 0x100, v232
	v_exp_f32_e32 v212, v84
	v_exp_f32_e32 v213, v88
	v_exp_f32_e32 v214, v92
	v_exp_f32_e32 v215, v96
	v_mfma_f32_32x32x16_bf16 v[2:17], v[122:125], v[236:239], v[2:17]
	v_exp_f32_e32 v216, v82
	v_fma_f32 v251, v212, s12, s12
	v_exp_f32_e32 v217, v86
	v_fma_f32 v252, v213, s12, s12
	v_exp_f32_e32 v218, v90
	v_fma_f32 v253, v214, s12, s12
	v_exp_f32_e32 v219, v94
	v_fma_f32 v254, v215, s12, s12
	v_mfma_f32_32x32x16_bf16 v[2:17], v[118:121], v[138:141], v[2:17]
	v_exp_f32_e32 v220, v83
	v_fmac_f32_e32 v251, v216, v251
	v_exp_f32_e32 v221, v87
	v_fmac_f32_e32 v252, v217, v252
	v_exp_f32_e32 v222, v91
	v_fmac_f32_e32 v253, v218, v253
	v_exp_f32_e32 v223, v95
	v_fmac_f32_e32 v254, v219, v254
	v_mfma_f32_32x32x16_bf16 v[2:17], v[114:117], v[142:145], v[2:17]
	v_rcp_f32_e32 v216, v251
	v_add_f32_e32 v220, 1.0, v220
	v_rcp_f32_e32 v217, v252
	v_add_f32_e32 v221, 1.0, v221
	v_rcp_f32_e32 v218, v253
	v_add_f32_e32 v222, 1.0, v222
	v_rcp_f32_e32 v219, v254
	v_add_f32_e32 v223, 1.0, v223
	v_mfma_f32_32x32x16_bf16 v[2:17], v[110:113], v[146:149], v[2:17]
	v_rcp_f32_e32 v220, v220
	v_fma_f32 v240, -v212, v216, v216
	v_rcp_f32_e32 v221, v221
	v_fma_f32 v241, -v213, v217, v217
	v_rcp_f32_e32 v222, v222
	v_fma_f32 v242, -v214, v218, v218
	v_rcp_f32_e32 v223, v223
	v_fma_f32 v243, -v215, v219, v219
	v_mfma_f32_32x32x16_bf16 v[2:17], v[106:109], v[150:153], v[2:17]
	v_exp_f32_e32 v246, v85
	v_fma_f32 v206, v220, v206, v240
	v_exp_f32_e32 v247, v89
	v_fma_f32 v207, v221, v207, v241
	v_exp_f32_e32 v248, v93
	v_fma_f32 v208, v222, v208, v242
	v_exp_f32_e32 v249, v97
	v_fma_f32 v209, v223, v209, v243
	v_mfma_f32_32x32x16_bf16 v[2:17], v[102:105], v[154:157], v[2:17]
	v_exp_f32_e32 v212, v206
	v_add_f32_e32 v246, 1.0, v246
	v_exp_f32_e32 v213, v207
	v_add_f32_e32 v247, 1.0, v247
	v_exp_f32_e32 v214, v208
	v_add_f32_e32 v248, 1.0, v248
	v_exp_f32_e32 v215, v209
	v_add_f32_e32 v249, 1.0, v249
	v_fmac_f32_e32 v246, v246, v212
	v_fmac_f32_e32 v247, v247, v213
	v_fmac_f32_e32 v248, v248, v214
	v_fmac_f32_e32 v249, v249, v215
	v_mfma_f32_32x32x16_bf16 v[2:17], v[98:101], v[158:161], v[2:17]
	v_rcp_f32_e32 v246, v246
	v_rcp_f32_e32 v247, v247
	v_rcp_f32_e32 v248, v248
	v_rcp_f32_e32 v249, v249
	v_fma_f32 v246, -v212, v246, v246
	v_fma_f32 v247, -v213, v247, v247
	v_fma_f32 v248, -v214, v248, v248
	v_fma_f32 v249, -v215, v249, v249
	v_cvt_pk_bf16_f32 v226, v246, v247
	v_cvt_pk_bf16_f32 v227, v248, v249
	ds_write_b128 v211, v[224:227] offset:8192
	s_sub_u32 s16, s16, 1
	s_cmp_lg_u32 s16, 0
	s_cbranch_scc1 .Llight_loop_w1
	v_mfma_f32_32x32x16_bf16 v[18:33], v[78:81], v[130:133], v[18:33]
	ds_read_b128 v[82:85], v234 offset:128
	ds_read_b128 v[86:89], v234 offset:144
	ds_read_b128 v[90:93], v234 offset:160
	ds_read_b128 v[94:97], v234 offset:176
	v_exp_f32_e32 v212, v4
	v_exp_f32_e32 v213, v8
	v_exp_f32_e32 v214, v12
	v_exp_f32_e32 v215, v16
	s_waitcnt lgkmcnt(4)
	s_barrier
	v_mfma_f32_32x32x16_bf16 v[18:33], v[74:77], v[236:239], v[18:33]
	ds_read_b128 v[162:165], v210 offset:8192
	v_exp_f32_e32 v216, v2
	v_fma_f32 v251, v212, s12, s12
	v_exp_f32_e32 v217, v6
	v_fma_f32 v252, v213, s12, s12
	v_exp_f32_e32 v218, v10
	v_fma_f32 v253, v214, s12, s12
	v_exp_f32_e32 v219, v14
	v_fma_f32 v254, v215, s12, s12
	v_mfma_f32_32x32x16_bf16 v[18:33], v[70:73], v[138:141], v[18:33]
	ds_read_b128 v[170:173], v210 offset:10240
	ds_read_b128 v[174:177], v210 offset:11264
	v_exp_f32_e32 v220, v3
	v_fmac_f32_e32 v251, v216, v251
	v_exp_f32_e32 v221, v7
	v_fmac_f32_e32 v252, v217, v252
	v_exp_f32_e32 v222, v11
	v_fmac_f32_e32 v253, v218, v253
	v_exp_f32_e32 v223, v15
	v_fmac_f32_e32 v254, v219, v254
	v_mfma_f32_32x32x16_bf16 v[18:33], v[66:69], v[142:145], v[18:33]
	ds_read_b128 v[178:181], v210 offset:12288
	ds_read_b128 v[182:185], v210 offset:13312
	v_rcp_f32_e32 v216, v251
	v_add_f32_e32 v220, 1.0, v220
	v_rcp_f32_e32 v217, v252
	v_add_f32_e32 v221, 1.0, v221
	v_rcp_f32_e32 v218, v253
	v_add_f32_e32 v222, 1.0, v222
	v_rcp_f32_e32 v219, v254
	v_add_f32_e32 v223, 1.0, v223
	v_mfma_f32_32x32x16_bf16 v[18:33], v[62:65], v[146:149], v[18:33]
	ds_read_b128 v[186:189], v210 offset:14336
	ds_read_b128 v[190:193], v210 offset:15360
	v_rcp_f32_e32 v220, v220
	v_fma_f32 v240, -v212, v216, v216
	v_rcp_f32_e32 v221, v221
	v_fma_f32 v241, -v213, v217, v217
	v_rcp_f32_e32 v222, v222
	v_fma_f32 v242, -v214, v218, v218
	v_rcp_f32_e32 v223, v223
	v_fma_f32 v243, -v215, v219, v219
	v_mfma_f32_32x32x16_bf16 v[18:33], v[58:61], v[150:153], v[18:33]
	v_exp_f32_e32 v246, v5
	v_fma_f32 v194, v220, v194, v240
	v_exp_f32_e32 v247, v9
	v_fma_f32 v195, v221, v195, v241
	v_exp_f32_e32 v248, v13
	v_fma_f32 v196, v222, v196, v242
	v_exp_f32_e32 v249, v17
	v_fma_f32 v197, v223, v197, v243
	v_mfma_f32_32x32x16_bf16 v[18:33], v[54:57], v[154:157], v[18:33]
	v_exp_f32_e32 v212, v194
	v_add_f32_e32 v246, 1.0, v246
	v_exp_f32_e32 v213, v195
	v_add_f32_e32 v247, 1.0, v247
	v_exp_f32_e32 v214, v196
	v_add_f32_e32 v248, 1.0, v248
	v_exp_f32_e32 v215, v197
	v_add_f32_e32 v249, 1.0, v249
	v_fmac_f32_e32 v246, v246, v212
	v_fmac_f32_e32 v247, v247, v213
	v_fmac_f32_e32 v248, v248, v214
	v_fmac_f32_e32 v249, v249, v215
	v_mfma_f32_32x32x16_bf16 v[18:33], v[50:53], v[158:161], v[18:33]
	v_rcp_f32_e32 v246, v246
	v_rcp_f32_e32 v247, v247
	v_rcp_f32_e32 v248, v248
	v_rcp_f32_e32 v249, v249
	v_fma_f32 v246, -v212, v246, v246
	v_fma_f32 v247, -v213, v247, v247
	v_fma_f32 v248, -v214, v248, v248
	v_fma_f32 v249, -v215, v249, v249
	v_cvt_pk_bf16_f32 v236, v246, v247
	v_cvt_pk_bf16_f32 v237, v248, v249
	s_waitcnt lgkmcnt(0)
	v_mfma_f32_32x32x16_bf16 v[34:49], v[126:129], v[162:165], v[34:49]
	v_exp_f32_e32 v212, v20
	v_exp_f32_e32 v213, v24
	v_exp_f32_e32 v214, v28
	v_exp_f32_e32 v215, v32
	v_mfma_f32_32x32x16_bf16 v[34:49], v[122:125], v[224:227], v[34:49]
	v_exp_f32_e32 v216, v18
	v_fma_f32 v251, v212, s12, s12
	v_exp_f32_e32 v217, v22
	v_fma_f32 v252, v213, s12, s12
	v_exp_f32_e32 v218, v26
	v_fma_f32 v253, v214, s12, s12
	v_exp_f32_e32 v219, v30
	v_fma_f32 v254, v215, s12, s12
	v_mfma_f32_32x32x16_bf16 v[34:49], v[118:121], v[170:173], v[34:49]
	v_exp_f32_e32 v220, v19
	v_fmac_f32_e32 v251, v216, v251
	v_exp_f32_e32 v221, v23
	v_fmac_f32_e32 v252, v217, v252
	v_exp_f32_e32 v222, v27
	v_fmac_f32_e32 v253, v218, v253
	v_exp_f32_e32 v223, v31
	v_fmac_f32_e32 v254, v219, v254
	v_mfma_f32_32x32x16_bf16 v[34:49], v[114:117], v[174:177], v[34:49]
	v_rcp_f32_e32 v216, v251
	v_add_f32_e32 v220, 1.0, v220
	v_rcp_f32_e32 v217, v252
	v_add_f32_e32 v221, 1.0, v221
	v_rcp_f32_e32 v218, v253
	v_add_f32_e32 v222, 1.0, v222
	v_rcp_f32_e32 v219, v254
	v_add_f32_e32 v223, 1.0, v223
	v_mfma_f32_32x32x16_bf16 v[34:49], v[110:113], v[178:181], v[34:49]
	v_rcp_f32_e32 v220, v220
	v_fma_f32 v240, -v212, v216, v216
	v_rcp_f32_e32 v221, v221
	v_fma_f32 v241, -v213, v217, v217
	v_rcp_f32_e32 v222, v222
	v_fma_f32 v242, -v214, v218, v218
	v_rcp_f32_e32 v223, v223
	v_fma_f32 v243, -v215, v219, v219
	v_mfma_f32_32x32x16_bf16 v[34:49], v[106:109], v[182:185], v[34:49]
	v_exp_f32_e32 v246, v21
	v_fma_f32 v198, v220, v198, v240
	v_exp_f32_e32 v247, v25
	v_fma_f32 v199, v221, v199, v241
	v_exp_f32_e32 v248, v29
	v_fma_f32 v200, v222, v200, v242
	v_exp_f32_e32 v249, v33
	v_fma_f32 v201, v223, v201, v243
	v_mfma_f32_32x32x16_bf16 v[34:49], v[102:105], v[186:189], v[34:49]
	v_exp_f32_e32 v212, v198
	v_add_f32_e32 v246, 1.0, v246
	v_exp_f32_e32 v213, v199
	v_add_f32_e32 v247, 1.0, v247
	v_exp_f32_e32 v214, v200
	v_add_f32_e32 v248, 1.0, v248
	v_exp_f32_e32 v215, v201
	v_add_f32_e32 v249, 1.0, v249
	v_fmac_f32_e32 v246, v246, v212
	v_fmac_f32_e32 v247, v247, v213
	v_fmac_f32_e32 v248, v248, v214
	v_fmac_f32_e32 v249, v249, v215
	v_mfma_f32_32x32x16_bf16 v[34:49], v[98:101], v[190:193], v[34:49]
	v_rcp_f32_e32 v246, v246
	v_rcp_f32_e32 v247, v247
	v_rcp_f32_e32 v248, v248
	v_rcp_f32_e32 v249, v249
	v_fma_f32 v246, -v212, v246, v246
	v_fma_f32 v247, -v213, v247, v247
	v_fma_f32 v248, -v214, v248, v248
	v_fma_f32 v249, -v215, v249, v249
	v_cvt_pk_bf16_f32 v238, v246, v247
	v_cvt_pk_bf16_f32 v239, v248, v249
	ds_write_b128 v211, v[236:239] offset:0
	s_waitcnt lgkmcnt(0)
	s_barrier
	s_bfe_u32 s20, s19, 0x10006
	s_lshl_b32 s21, s20, 7
	s_lshl_b32 s20, s20, 13
	s_add_u32 s20, s20, 0x30000
	s_add_u32 s22, s14, s20
	s_addc_u32 s23, s15, 0
	s_add_u32 s24, s22, 0x1000
	s_addc_u32 s25, s23, 0
	global_load_dwordx4 v[98:101], v210, s[22:23] offset:0
	global_load_dwordx4 v[102:105], v210, s[22:23] offset:1024
	global_load_dwordx4 v[106:109], v210, s[22:23] offset:2048
	global_load_dwordx4 v[110:113], v210, s[22:23] offset:3072
	global_load_dwordx4 v[114:117], v210, s[24:25] offset:0
	global_load_dwordx4 v[118:121], v210, s[24:25] offset:1024
	global_load_dwordx4 v[122:125], v210, s[24:25] offset:2048
	global_load_dwordx4 v[126:129], v210, s[24:25] offset:3072
	v_or_b32_e32 v250, s21, v230
	global_load_dwordx4 v[130:133], v250, s[4:5] offset:0
	global_load_dwordx4 v[134:137], v250, s[4:5] offset:32
	global_load_dwordx4 v[138:141], v250, s[4:5] offset:64
	global_load_dwordx4 v[142:145], v250, s[4:5] offset:96
	global_load_dwordx4 v[146:149], v250, s[6:7] offset:0
	global_load_dwordx4 v[150:153], v250, s[6:7] offset:32
	global_load_dwordx4 v[154:157], v250, s[6:7] offset:64
	global_load_dwordx4 v[158:161], v250, s[6:7] offset:96
	s_load_dword s26, s[8:9], 0x0
	v_mfma_f32_32x32x16_bf16 v[82:97], v[78:81], v[162:165], v[82:97]
	v_exp_f32_e32 v212, v36
	v_exp_f32_e32 v213, v40
	v_exp_f32_e32 v214, v44
	v_exp_f32_e32 v215, v48
	v_mfma_f32_32x32x16_bf16 v[82:97], v[74:77], v[224:227], v[82:97]
	v_exp_f32_e32 v216, v34
	v_fma_f32 v251, v212, s12, s12
	v_exp_f32_e32 v217, v38
	v_fma_f32 v252, v213, s12, s12
	v_exp_f32_e32 v218, v42
	v_fma_f32 v253, v214, s12, s12
	v_exp_f32_e32 v219, v46
	v_fma_f32 v254, v215, s12, s12
	v_mfma_f32_32x32x16_bf16 v[82:97], v[70:73], v[170:173], v[82:97]
	v_exp_f32_e32 v220, v35
	v_fmac_f32_e32 v251, v216, v251
	v_exp_f32_e32 v221, v39
	v_fmac_f32_e32 v252, v217, v252
	v_exp_f32_e32 v222, v43
	v_fmac_f32_e32 v253, v218, v253
	v_exp_f32_e32 v223, v47
	v_fmac_f32_e32 v254, v219, v254
	v_mfma_f32_32x32x16_bf16 v[82:97], v[66:69], v[174:177], v[82:97]
	v_rcp_f32_e32 v216, v251
	v_add_f32_e32 v220, 1.0, v220
	v_rcp_f32_e32 v217, v252
	v_add_f32_e32 v221, 1.0, v221
	v_rcp_f32_e32 v218, v253
	v_add_f32_e32 v222, 1.0, v222
	v_rcp_f32_e32 v219, v254
	v_add_f32_e32 v223, 1.0, v223
	v_mfma_f32_32x32x16_bf16 v[82:97], v[62:65], v[178:181], v[82:97]
	v_rcp_f32_e32 v220, v220
	v_fma_f32 v240, -v212, v216, v216
	v_rcp_f32_e32 v221, v221
	v_fma_f32 v241, -v213, v217, v217
	v_rcp_f32_e32 v222, v222
	v_fma_f32 v242, -v214, v218, v218
	v_rcp_f32_e32 v223, v223
	v_fma_f32 v243, -v215, v219, v219
	v_mfma_f32_32x32x16_bf16 v[82:97], v[58:61], v[182:185], v[82:97]
	v_exp_f32_e32 v246, v37
	v_fma_f32 v202, v220, v202, v240
	v_exp_f32_e32 v247, v41
	v_fma_f32 v203, v221, v203, v241
	v_exp_f32_e32 v248, v45
	v_fma_f32 v204, v222, v204, v242
	v_exp_f32_e32 v249, v49
	v_fma_f32 v205, v223, v205, v243
	v_mfma_f32_32x32x16_bf16 v[82:97], v[54:57], v[186:189], v[82:97]
	v_exp_f32_e32 v212, v202
	v_add_f32_e32 v246, 1.0, v246
	v_exp_f32_e32 v213, v203
	v_add_f32_e32 v247, 1.0, v247
	v_exp_f32_e32 v214, v204
	v_add_f32_e32 v248, 1.0, v248
	v_exp_f32_e32 v215, v205
	v_add_f32_e32 v249, 1.0, v249
	v_fmac_f32_e32 v246, v246, v212
	v_fmac_f32_e32 v247, v247, v213
	v_fmac_f32_e32 v248, v248, v214
	v_fmac_f32_e32 v249, v249, v215
	v_mfma_f32_32x32x16_bf16 v[82:97], v[50:53], v[190:193], v[82:97]
	v_rcp_f32_e32 v246, v246
	v_rcp_f32_e32 v247, v247
	v_rcp_f32_e32 v248, v248
	v_rcp_f32_e32 v249, v249
	v_fma_f32 v246, -v212, v246, v246
	v_fma_f32 v247, -v213, v247, v247
	v_fma_f32 v248, -v214, v248, v248
	v_fma_f32 v249, -v215, v249, v249
	v_cvt_pk_bf16_f32 v224, v246, v247
	v_cvt_pk_bf16_f32 v225, v248, v249
	s_waitcnt lgkmcnt(0)
	v_exp_f32_e32 v212, v84
	v_exp_f32_e32 v213, v88
	v_exp_f32_e32 v214, v92
	v_exp_f32_e32 v215, v96
	v_exp_f32_e32 v216, v82
	v_fma_f32 v251, v212, s12, s12
	v_exp_f32_e32 v217, v86
	v_fma_f32 v252, v213, s12, s12
	v_exp_f32_e32 v218, v90
	v_fma_f32 v253, v214, s12, s12
	v_exp_f32_e32 v219, v94
	v_fma_f32 v254, v215, s12, s12
	v_exp_f32_e32 v220, v83
	v_fmac_f32_e32 v251, v216, v251
	v_exp_f32_e32 v221, v87
	v_fmac_f32_e32 v252, v217, v252
	v_exp_f32_e32 v222, v91
	v_fmac_f32_e32 v253, v218, v253
	v_exp_f32_e32 v223, v95
	v_fmac_f32_e32 v254, v219, v254
	v_rcp_f32_e32 v216, v251
	v_add_f32_e32 v220, 1.0, v220
	v_rcp_f32_e32 v217, v252
	v_add_f32_e32 v221, 1.0, v221
	v_rcp_f32_e32 v218, v253
	v_add_f32_e32 v222, 1.0, v222
	v_rcp_f32_e32 v219, v254
	v_add_f32_e32 v223, 1.0, v223
	v_rcp_f32_e32 v220, v220
	v_fma_f32 v240, -v212, v216, v216
	v_rcp_f32_e32 v221, v221
	v_fma_f32 v241, -v213, v217, v217
	v_rcp_f32_e32 v222, v222
	v_fma_f32 v242, -v214, v218, v218
	v_rcp_f32_e32 v223, v223
	v_fma_f32 v243, -v215, v219, v219
	v_exp_f32_e32 v246, v85
	v_fma_f32 v206, v220, v206, v240
	v_exp_f32_e32 v247, v89
	v_fma_f32 v207, v221, v207, v241
	v_exp_f32_e32 v248, v93
	v_fma_f32 v208, v222, v208, v242
	v_exp_f32_e32 v249, v97
	v_fma_f32 v209, v223, v209, v243
	v_exp_f32_e32 v212, v206
	v_add_f32_e32 v246, 1.0, v246
	v_exp_f32_e32 v213, v207
	v_add_f32_e32 v247, 1.0, v247
	v_exp_f32_e32 v214, v208
	v_add_f32_e32 v248, 1.0, v248
	v_exp_f32_e32 v215, v209
	v_add_f32_e32 v249, 1.0, v249
	v_fmac_f32_e32 v246, v246, v212
	v_fmac_f32_e32 v247, v247, v213
	v_fmac_f32_e32 v248, v248, v214
	v_fmac_f32_e32 v249, v249, v215
	v_rcp_f32_e32 v246, v246
	v_rcp_f32_e32 v247, v247
	v_rcp_f32_e32 v248, v248
	v_rcp_f32_e32 v249, v249
	v_fma_f32 v246, -v212, v246, v246
	v_fma_f32 v247, -v213, v247, v247
	v_fma_f32 v248, -v214, v248, v248
	v_fma_f32 v249, -v215, v249, v249
	v_cvt_pk_bf16_f32 v226, v246, v247
	v_cvt_pk_bf16_f32 v227, v248, v249
	ds_write_b128 v211, v[224:227] offset:8192
	s_waitcnt lgkmcnt(0)
	s_barrier
	s_lshl_b32 s20, s19, 6
	s_and_b32 s20, s20, 0x2000
	v_or_b32_e32 v20, s20, v210
	ds_read_b128 v[162:165], v20 offset:0
	ds_read_b128 v[166:169], v20 offset:1024
	ds_read_b128 v[170:173], v20 offset:2048
	ds_read_b128 v[174:177], v20 offset:3072
	ds_read_b128 v[178:181], v20 offset:4096
	ds_read_b128 v[182:185], v20 offset:5120
	ds_read_b128 v[186:189], v20 offset:6144
	ds_read_b128 v[190:193], v20 offset:7168
	s_bfe_u32 s20, s19, 0x10006
	s_lshl_b32 s20, s20, 9
	s_and_b32 s21, s19, 0x80
	s_or_b32 s20, s20, s21
	v_lshlrev_b32_e32 v19, 2, v229
	v_add3_u32 v19, s20, v19, v228
	s_waitcnt vmcnt(0)
	s_waitcnt lgkmcnt(7)
	v_mfma_f32_32x32x16_bf16 v[2:17], v[98:101], v[162:165], 0
	s_waitcnt lgkmcnt(6)
	v_mfma_f32_32x32x16_bf16 v[2:17], v[102:105], v[166:169], v[2:17]
	s_waitcnt lgkmcnt(5)
	v_mfma_f32_32x32x16_bf16 v[2:17], v[106:109], v[170:173], v[2:17]
	s_waitcnt lgkmcnt(4)
	v_mfma_f32_32x32x16_bf16 v[2:17], v[110:113], v[174:177], v[2:17]
	s_waitcnt lgkmcnt(3)
	v_mfma_f32_32x32x16_bf16 v[2:17], v[114:117], v[178:181], v[2:17]
	s_waitcnt lgkmcnt(2)
	v_mfma_f32_32x32x16_bf16 v[2:17], v[118:121], v[182:185], v[2:17]
	s_waitcnt lgkmcnt(1)
	v_mfma_f32_32x32x16_bf16 v[2:17], v[122:125], v[186:189], v[2:17]
	s_waitcnt lgkmcnt(0)
	v_mfma_f32_32x32x16_bf16 v[2:17], v[126:129], v[190:193], v[2:17]
	s_nop 15
	s_nop 3
	v_add_f32_e32 v2, v2, v130
	v_add_f32_e32 v3, v3, v131
	v_add_f32_e32 v4, v4, v132
	v_add_f32_e32 v5, v5, v133
	v_add_f32_e32 v6, v6, v134
	v_add_f32_e32 v7, v7, v135
	v_add_f32_e32 v8, v8, v136
	v_add_f32_e32 v9, v9, v137
	v_add_f32_e32 v10, v10, v138
	v_add_f32_e32 v11, v11, v139
	v_add_f32_e32 v12, v12, v140
	v_add_f32_e32 v13, v13, v141
	v_add_f32_e32 v14, v14, v142
	v_add_f32_e32 v15, v15, v143
	v_add_f32_e32 v16, v16, v144
	v_add_f32_e32 v17, v17, v145
	v_max_f32_e32 v2, 0, v2
	v_max_f32_e32 v3, 0, v3
	v_max_f32_e32 v4, 0, v4
	v_max_f32_e32 v5, 0, v5
	v_max_f32_e32 v6, 0, v6
	v_max_f32_e32 v7, 0, v7
	v_max_f32_e32 v8, 0, v8
	v_max_f32_e32 v9, 0, v9
	v_max_f32_e32 v10, 0, v10
	v_max_f32_e32 v11, 0, v11
	v_max_f32_e32 v12, 0, v12
	v_max_f32_e32 v13, 0, v13
	v_max_f32_e32 v14, 0, v14
	v_max_f32_e32 v15, 0, v15
	v_max_f32_e32 v16, 0, v16
	v_max_f32_e32 v17, 0, v17
	v_fma_f32 v18, v2, v146, 0
	v_fmac_f32_e32 v18, v3, v147
	v_fmac_f32_e32 v18, v4, v148
	v_fmac_f32_e32 v18, v5, v149
	v_fmac_f32_e32 v18, v6, v150
	v_fmac_f32_e32 v18, v7, v151
	v_fmac_f32_e32 v18, v8, v152
	v_fmac_f32_e32 v18, v9, v153
	v_fmac_f32_e32 v18, v10, v154
	v_fmac_f32_e32 v18, v11, v155
	v_fmac_f32_e32 v18, v12, v156
	v_fmac_f32_e32 v18, v13, v157
	v_fmac_f32_e32 v18, v14, v158
	v_fmac_f32_e32 v18, v15, v159
	v_fmac_f32_e32 v18, v16, v160
	v_fmac_f32_e32 v18, v17, v161
	ds_write_b32 v19, v18 offset:35904
	s_branch .LBB1_40
.Llight_w2:
	ds_read_b128 v[82:85], v234 offset:128
	ds_read_b128 v[86:89], v234 offset:144
	ds_read_b128 v[90:93], v234 offset:160
	ds_read_b128 v[94:97], v234 offset:176
	ds_read2_b32 v[244:245], v232 offset1:32
	v_exp_f32_e32 v212, v4
	v_exp_f32_e32 v213, v8
	v_exp_f32_e32 v214, v12
	v_exp_f32_e32 v215, v16
	v_exp_f32_e32 v216, v2
	v_fma_f32 v251, v212, s12, s12
	v_exp_f32_e32 v217, v6
	v_fma_f32 v252, v213, s12, s12
	v_exp_f32_e32 v218, v10
	v_fma_f32 v253, v214, s12, s12
	v_exp_f32_e32 v219, v14
	v_fma_f32 v254, v215, s12, s12
	v_fmac_f32_e32 v251, v216, v251
	v_fmac_f32_e32 v252, v217, v252
	v_fmac_f32_e32 v253, v218, v253
	v_fmac_f32_e32 v254, v219, v254
	v_rcp_f32_e32 v216, v251
	v_rcp_f32_e32 v217, v252
	v_rcp_f32_e32 v218, v253
	v_rcp_f32_e32 v219, v254
	v_exp_f32_e32 v246, v5
	v_fma_f32 v194, -v212, v216, v216
	v_exp_f32_e32 v247, v9
	v_fma_f32 v195, -v213, v217, v217
	v_exp_f32_e32 v248, v13
	v_fma_f32 v196, -v214, v218, v218
	v_exp_f32_e32 v249, v17
	v_fma_f32 v197, -v215, v219, v219
	v_exp_f32_e32 v212, v194
	v_add_f32_e32 v246, 1.0, v246
	v_exp_f32_e32 v213, v195
	v_add_f32_e32 v247, 1.0, v247
	v_exp_f32_e32 v214, v196
	v_add_f32_e32 v248, 1.0, v248
	v_exp_f32_e32 v215, v197
	v_add_f32_e32 v249, 1.0, v249
	v_fmac_f32_e32 v246, v246, v212
	v_fmac_f32_e32 v247, v247, v213
	v_fmac_f32_e32 v248, v248, v214
	v_fmac_f32_e32 v249, v249, v215
	v_rcp_f32_e32 v246, v246
	v_rcp_f32_e32 v247, v247
	v_rcp_f32_e32 v248, v248
	v_rcp_f32_e32 v249, v249
	v_fma_f32 v246, -v212, v246, v246
	v_fma_f32 v247, -v213, v247, v247
	v_fma_f32 v248, -v214, v248, v248
	v_fma_f32 v249, -v215, v249, v249
	v_cvt_pk_bf16_f32 v236, v246, v247
	v_cvt_pk_bf16_f32 v237, v248, v249
	s_waitcnt lgkmcnt(0)
	v_add_u32_e32 v233, v231, v244
	ds_read_b128 v[2:5], v233 offset:0
	ds_read_b128 v[6:9], v233 offset:16
	ds_read_b128 v[10:13], v233 offset:32
	ds_read_b128 v[14:17], v233 offset:48
	v_exp_f32_e32 v212, v20
	v_exp_f32_e32 v213, v24
	v_exp_f32_e32 v214, v28
	v_exp_f32_e32 v215, v32
	v_exp_f32_e32 v216, v18
	v_fma_f32 v251, v212, s12, s12
	v_exp_f32_e32 v217, v22
	v_fma_f32 v252, v213, s12, s12
	v_exp_f32_e32 v218, v26
	v_fma_f32 v253, v214, s12, s12
	v_exp_f32_e32 v219, v30
	v_fma_f32 v254, v215, s12, s12
	v_fmac_f32_e32 v251, v216, v251
	v_fmac_f32_e32 v252, v217, v252
	v_fmac_f32_e32 v253, v218, v253
	v_fmac_f32_e32 v254, v219, v254
	v_rcp_f32_e32 v216, v251
	v_rcp_f32_e32 v217, v252
	v_rcp_f32_e32 v218, v253
	v_rcp_f32_e32 v219, v254
	v_exp_f32_e32 v246, v21
	v_fma_f32 v198, -v212, v216, v216
	v_exp_f32_e32 v247, v25
	v_fma_f32 v199, -v213, v217, v217
	v_exp_f32_e32 v248, v29
	v_fma_f32 v200, -v214, v218, v218
	v_exp_f32_e32 v249, v33
	v_fma_f32 v201, -v215, v219, v219
	v_exp_f32_e32 v212, v198
	v_add_f32_e32 v246, 1.0, v246
	v_exp_f32_e32 v213, v199
	v_add_f32_e32 v247, 1.0, v247
	v_exp_f32_e32 v214, v200
	v_add_f32_e32 v248, 1.0, v248
	v_exp_f32_e32 v215, v201
	v_add_f32_e32 v249, 1.0, v249
	v_fmac_f32_e32 v246, v246, v212
	v_fmac_f32_e32 v247, v247, v213
	v_fmac_f32_e32 v248, v248, v214
	v_fmac_f32_e32 v249, v249, v215
	v_rcp_f32_e32 v246, v246
	v_rcp_f32_e32 v247, v247
	v_rcp_f32_e32 v248, v248
	v_rcp_f32_e32 v249, v249
	v_fma_f32 v246, -v212, v246, v246
	v_fma_f32 v247, -v213, v247, v247
	v_fma_f32 v248, -v214, v248, v248
	v_fma_f32 v249, -v215, v249, v249
	v_cvt_pk_bf16_f32 v238, v246, v247
	v_cvt_pk_bf16_f32 v239, v248, v249
	ds_write_b128 v211, v[236:239] offset:0
	ds_read_b128 v[18:21], v233 offset:128
	ds_read_b128 v[22:25], v233 offset:144
	ds_read_b128 v[26:29], v233 offset:160
	ds_read_b128 v[30:33], v233 offset:176
	v_exp_f32_e32 v212, v36
	v_exp_f32_e32 v213, v40
	v_exp_f32_e32 v214, v44
	v_exp_f32_e32 v215, v48
	s_waitcnt lgkmcnt(4)
	s_barrier
	ds_read_b128 v[130:133], v210 offset:0
	ds_read_b128 v[134:137], v210 offset:1024
	v_exp_f32_e32 v216, v34
	v_fma_f32 v251, v212, s12, s12
	v_exp_f32_e32 v217, v38
	v_fma_f32 v252, v213, s12, s12
	v_exp_f32_e32 v218, v42
	v_fma_f32 v253, v214, s12, s12
	v_exp_f32_e32 v219, v46
	v_fma_f32 v254, v215, s12, s12
	ds_read_b128 v[142:145], v210 offset:3072
	v_fmac_f32_e32 v251, v216, v251
	v_fmac_f32_e32 v252, v217, v252
	v_fmac_f32_e32 v253, v218, v253
	v_fmac_f32_e32 v254, v219, v254
	ds_read_b128 v[146:149], v210 offset:4096
	ds_read_b128 v[150:153], v210 offset:5120
	v_rcp_f32_e32 v216, v251
	v_rcp_f32_e32 v217, v252
	v_rcp_f32_e32 v218, v253
	v_rcp_f32_e32 v219, v254
	ds_read_b128 v[154:157], v210 offset:6144
	ds_read_b128 v[158:161], v210 offset:7168
	v_exp_f32_e32 v246, v37
	v_fma_f32 v202, -v212, v216, v216
	v_exp_f32_e32 v247, v41
	v_fma_f32 v203, -v213, v217, v217
	v_exp_f32_e32 v248, v45
	v_fma_f32 v204, -v214, v218, v218
	v_exp_f32_e32 v249, v49
	v_fma_f32 v205, -v215, v219, v219
	v_exp_f32_e32 v212, v202
	v_add_f32_e32 v246, 1.0, v246
	v_exp_f32_e32 v213, v203
	v_add_f32_e32 v247, 1.0, v247
	v_exp_f32_e32 v214, v204
	v_add_f32_e32 v248, 1.0, v248
	v_exp_f32_e32 v215, v205
	v_add_f32_e32 v249, 1.0, v249
	v_fmac_f32_e32 v246, v246, v212
	v_fmac_f32_e32 v247, v247, v213
	v_fmac_f32_e32 v248, v248, v214
	v_fmac_f32_e32 v249, v249, v215
	v_rcp_f32_e32 v246, v246
	v_rcp_f32_e32 v247, v247
	v_rcp_f32_e32 v248, v248
	v_rcp_f32_e32 v249, v249
	v_fma_f32 v246, -v212, v246, v246
	v_fma_f32 v247, -v213, v247, v247
	v_fma_f32 v248, -v214, v248, v248
	v_fma_f32 v249, -v215, v249, v249
	v_cvt_pk_bf16_f32 v224, v246, v247
	v_cvt_pk_bf16_f32 v225, v248, v249
	s_waitcnt lgkmcnt(0)
	v_mfma_f32_32x32x16_bf16 v[2:17], v[126:129], v[130:133], v[2:17]
	v_add_u32_e32 v234, v231, v245
	ds_read_b128 v[34:37], v234 offset:0
	ds_read_b128 v[38:41], v234 offset:16
	ds_read_b128 v[42:45], v234 offset:32
	ds_read_b128 v[46:49], v234 offset:48
	v_add_u32_e32 v232, 0x100, v232
	v_exp_f32_e32 v212, v84
	v_exp_f32_e32 v213, v88
	v_exp_f32_e32 v214, v92
	v_exp_f32_e32 v215, v96
	v_mfma_f32_32x32x16_bf16 v[2:17], v[122:125], v[134:137], v[2:17]
	v_exp_f32_e32 v216, v82
	v_fma_f32 v251, v212, s12, s12
	v_exp_f32_e32 v217, v86
	v_fma_f32 v252, v213, s12, s12
	v_exp_f32_e32 v218, v90
	v_fma_f32 v253, v214, s12, s12
	v_exp_f32_e32 v219, v94
	v_fma_f32 v254, v215, s12, s12
	v_mfma_f32_32x32x16_bf16 v[2:17], v[118:121], v[236:239], v[2:17]
	v_fmac_f32_e32 v251, v216, v251
	v_fmac_f32_e32 v252, v217, v252
	v_fmac_f32_e32 v253, v218, v253
	v_fmac_f32_e32 v254, v219, v254
	v_mfma_f32_32x32x16_bf16 v[2:17], v[114:117], v[142:145], v[2:17]
	v_rcp_f32_e32 v216, v251
	v_rcp_f32_e32 v217, v252
	v_rcp_f32_e32 v218, v253
	v_rcp_f32_e32 v219, v254
	v_mfma_f32_32x32x16_bf16 v[2:17], v[110:113], v[146:149], v[2:17]
	v_exp_f32_e32 v246, v85
	v_fma_f32 v206, -v212, v216, v216
	v_exp_f32_e32 v247, v89
	v_fma_f32 v207, -v213, v217, v217
	v_exp_f32_e32 v248, v93
	v_fma_f32 v208, -v214, v218, v218
	v_exp_f32_e32 v249, v97
	v_fma_f32 v209, -v215, v219, v219
	v_mfma_f32_32x32x16_bf16 v[2:17], v[106:109], v[150:153], v[2:17]
	v_mfma_f32_32x32x16_bf16 v[2:17], v[102:105], v[154:157], v[2:17]
	v_exp_f32_e32 v212, v206
	v_add_f32_e32 v246, 1.0, v246
	v_exp_f32_e32 v213, v207
	v_add_f32_e32 v247, 1.0, v247
	v_exp_f32_e32 v214, v208
	v_add_f32_e32 v248, 1.0, v248
	v_exp_f32_e32 v215, v209
	v_add_f32_e32 v249, 1.0, v249
	v_fmac_f32_e32 v246, v246, v212
	v_fmac_f32_e32 v247, v247, v213
	v_fmac_f32_e32 v248, v248, v214
	v_fmac_f32_e32 v249, v249, v215
	v_mfma_f32_32x32x16_bf16 v[2:17], v[98:101], v[158:161], v[2:17]
	v_rcp_f32_e32 v246, v246
	v_rcp_f32_e32 v247, v247
	v_rcp_f32_e32 v248, v248
	v_rcp_f32_e32 v249, v249
	v_fma_f32 v246, -v212, v246, v246
	v_fma_f32 v247, -v213, v247, v247
	v_fma_f32 v248, -v214, v248, v248
	v_fma_f32 v249, -v215, v249, v249
	v_cvt_pk_bf16_f32 v226, v246, v247
	v_cvt_pk_bf16_f32 v227, v248, v249
	ds_write_b128 v211, v[224:227] offset:8192
	.p2align 6
.Llight_loop_w2:
	v_mfma_f32_32x32x16_bf16 v[18:33], v[78:81], v[130:133], v[18:33]
	ds_read_b128 v[82:85], v234 offset:128
	ds_read_b128 v[86:89], v234 offset:144
	ds_read_b128 v[90:93], v234 offset:160
	ds_read_b128 v[94:97], v234 offset:176
	ds_read2_b32 v[244:245], v232 offset1:32
	v_exp_f32_e32 v212, v4
	v_exp_f32_e32 v213, v8
	v_exp_f32_e32 v214, v12
	v_exp_f32_e32 v215, v16
	s_waitcnt lgkmcnt(5)
	s_barrier
	v_mfma_f32_32x32x16_bf16 v[18:33], v[74:77], v[134:137], v[18:33]
	ds_read_b128 v[162:165], v210 offset:8192
	ds_read_b128 v[166:169], v210 offset:9216
	v_exp_f32_e32 v216, v2
	v_fma_f32 v251, v212, s12, s12
	v_exp_f32_e32 v217, v6
	v_fma_f32 v252, v213, s12, s12
	v_exp_f32_e32 v218, v10
	v_fma_f32 v253, v214, s12, s12
	v_exp_f32_e32 v219, v14
	v_fma_f32 v254, v215, s12, s12
	v_mfma_f32_32x32x16_bf16 v[18:33], v[70:73], v[236:239], v[18:33]
	ds_read_b128 v[174:177], v210 offset:11264
	v_exp_f32_e32 v220, v3
	v_fmac_f32_e32 v251, v216, v251
	v_exp_f32_e32 v221, v7
	v_fmac_f32_e32 v252, v217, v252
	v_exp_f32_e32 v222, v11
	v_fmac_f32_e32 v253, v218, v253
	v_exp_f32_e32 v223, v15
	v_fmac_f32_e32 v254, v219, v254
	v_mfma_f32_32x32x16_bf16 v[18:33], v[66:69], v[142:145], v[18:33]
	ds_read_b128 v[178:181], v210 offset:12288
	ds_read_b128 v[182:185], v210 offset:13312
	v_rcp_f32_e32 v216, v251
	v_add_f32_e32 v220, 1.0, v220
	v_rcp_f32_e32 v217, v252
	v_add_f32_e32 v221, 1.0, v221
	v_rcp_f32_e32 v218, v253
	v_add_f32_e32 v222, 1.0, v222
	v_rcp_f32_e32 v219, v254
	v_add_f32_e32 v223, 1.0, v223
	v_mfma_f32_32x32x16_bf16 v[18:33], v[62:65], v[146:149], v[18:33]
	ds_read_b128 v[186:189], v210 offset:14336
	ds_read_b128 v[190:193], v210 offset:15360
	v_rcp_f32_e32 v220, v220
	v_fma_f32 v240, -v212, v216, v216
	v_rcp_f32_e32 v221, v221
	v_fma_f32 v241, -v213, v217, v217
	v_rcp_f32_e32 v222, v222
	v_fma_f32 v242, -v214, v218, v218
	v_rcp_f32_e32 v223, v223
	v_fma_f32 v243, -v215, v219, v219
	v_mfma_f32_32x32x16_bf16 v[18:33], v[58:61], v[150:153], v[18:33]
	v_exp_f32_e32 v246, v5
	v_fma_f32 v194, v220, v194, v240
	v_exp_f32_e32 v247, v9
	v_fma_f32 v195, v221, v195, v241
	v_exp_f32_e32 v248, v13
	v_fma_f32 v196, v222, v196, v242
	v_exp_f32_e32 v249, v17
	v_fma_f32 v197, v223, v197, v243
	v_mfma_f32_32x32x16_bf16 v[18:33], v[54:57], v[154:157], v[18:33]
	v_exp_f32_e32 v212, v194
	v_add_f32_e32 v246, 1.0, v246
	v_exp_f32_e32 v213, v195
	v_add_f32_e32 v247, 1.0, v247
	v_exp_f32_e32 v214, v196
	v_add_f32_e32 v248, 1.0, v248
	v_exp_f32_e32 v215, v197
	v_add_f32_e32 v249, 1.0, v249
	v_fmac_f32_e32 v246, v246, v212
	v_fmac_f32_e32 v247, v247, v213
	v_fmac_f32_e32 v248, v248, v214
	v_fmac_f32_e32 v249, v249, v215
	v_mfma_f32_32x32x16_bf16 v[18:33], v[50:53], v[158:161], v[18:33]
	v_rcp_f32_e32 v246, v246
	v_rcp_f32_e32 v247, v247
	v_rcp_f32_e32 v248, v248
	v_rcp_f32_e32 v249, v249
	v_fma_f32 v246, -v212, v246, v246
	v_fma_f32 v247, -v213, v247, v247
	v_fma_f32 v248, -v214, v248, v248
	v_fma_f32 v249, -v215, v249, v249
	v_cvt_pk_bf16_f32 v236, v246, v247
	v_cvt_pk_bf16_f32 v237, v248, v249
	s_waitcnt lgkmcnt(0)
	v_mfma_f32_32x32x16_bf16 v[34:49], v[126:129], v[162:165], v[34:49]
	v_add_u32_e32 v233, v231, v244
	ds_read_b128 v[2:5], v233 offset:0
	ds_read_b128 v[6:9], v233 offset:16
	ds_read_b128 v[10:13], v233 offset:32
	ds_read_b128 v[14:17], v233 offset:48
	v_exp_f32_e32 v212, v20
	v_exp_f32_e32 v213, v24
	v_exp_f32_e32 v214, v28
	v_exp_f32_e32 v215, v32
	v_mfma_f32_32x32x16_bf16 v[34:49], v[122:125], v[166:169], v[34:49]
	v_exp_f32_e32 v216, v18
	v_fma_f32 v251, v212, s12, s12
	v_exp_f32_e32 v217, v22
	v_fma_f32 v252, v213, s12, s12
	v_exp_f32_e32 v218, v26
	v_fma_f32 v253, v214, s12, s12
	v_exp_f32_e32 v219, v30
	v_fma_f32 v254, v215, s12, s12
	v_mfma_f32_32x32x16_bf16 v[34:49], v[118:121], v[224:227], v[34:49]
	v_exp_f32_e32 v220, v19
	v_fmac_f32_e32 v251, v216, v251
	v_exp_f32_e32 v221, v23
	v_fmac_f32_e32 v252, v217, v252
	v_exp_f32_e32 v222, v27
	v_fmac_f32_e32 v253, v218, v253
	v_exp_f32_e32 v223, v31
	v_fmac_f32_e32 v254, v219, v254
	v_mfma_f32_32x32x16_bf16 v[34:49], v[114:117], v[174:177], v[34:49]
	v_rcp_f32_e32 v216, v251
	v_add_f32_e32 v220, 1.0, v220
	v_rcp_f32_e32 v217, v252
	v_add_f32_e32 v221, 1.0, v221
	v_rcp_f32_e32 v218, v253
	v_add_f32_e32 v222, 1.0, v222
	v_rcp_f32_e32 v219, v254
	v_add_f32_e32 v223, 1.0, v223
	v_mfma_f32_32x32x16_bf16 v[34:49], v[110:113], v[178:181], v[34:49]
	v_rcp_f32_e32 v220, v220
	v_fma_f32 v240, -v212, v216, v216
	v_rcp_f32_e32 v221, v221
	v_fma_f32 v241, -v213, v217, v217
	v_rcp_f32_e32 v222, v222
	v_fma_f32 v242, -v214, v218, v218
	v_rcp_f32_e32 v223, v223
	v_fma_f32 v243, -v215, v219, v219
	v_mfma_f32_32x32x16_bf16 v[34:49], v[106:109], v[182:185], v[34:49]
	v_exp_f32_e32 v246, v21
	v_fma_f32 v198, v220, v198, v240
	v_exp_f32_e32 v247, v25
	v_fma_f32 v199, v221, v199, v241
	v_exp_f32_e32 v248, v29
	v_fma_f32 v200, v222, v200, v242
	v_exp_f32_e32 v249, v33
	v_fma_f32 v201, v223, v201, v243
	v_mfma_f32_32x32x16_bf16 v[34:49], v[102:105], v[186:189], v[34:49]
	v_exp_f32_e32 v212, v198
	v_add_f32_e32 v246, 1.0, v246
	v_exp_f32_e32 v213, v199
	v_add_f32_e32 v247, 1.0, v247
	v_exp_f32_e32 v214, v200
	v_add_f32_e32 v248, 1.0, v248
	v_exp_f32_e32 v215, v201
	v_add_f32_e32 v249, 1.0, v249
	v_fmac_f32_e32 v246, v246, v212
	v_fmac_f32_e32 v247, v247, v213
	v_fmac_f32_e32 v248, v248, v214
	v_fmac_f32_e32 v249, v249, v215
	v_mfma_f32_32x32x16_bf16 v[34:49], v[98:101], v[190:193], v[34:49]
	v_rcp_f32_e32 v246, v246
	v_rcp_f32_e32 v247, v247
	v_rcp_f32_e32 v248, v248
	v_rcp_f32_e32 v249, v249
	v_fma_f32 v246, -v212, v246, v246
	v_fma_f32 v247, -v213, v247, v247
	v_fma_f32 v248, -v214, v248, v248
	v_fma_f32 v249, -v215, v249, v249
	v_cvt_pk_bf16_f32 v238, v246, v247
	v_cvt_pk_bf16_f32 v239, v248, v249
	ds_write_b128 v211, v[236:239] offset:0
	v_mfma_f32_32x32x16_bf16 v[82:97], v[78:81], v[162:165], v[82:97]
	ds_read_b128 v[18:21], v233 offset:128
	ds_read_b128 v[22:25], v233 offset:144
	ds_read_b128 v[26:29], v233 offset:160
	ds_read_b128 v[30:33], v233 offset:176
	v_exp_f32_e32 v212, v36
	v_exp_f32_e32 v213, v40
	v_exp_f32_e32 v214, v44
	v_exp_f32_e32 v215, v48
	s_waitcnt lgkmcnt(4)
	s_barrier
	v_mfma_f32_32x32x16_bf16 v[82:97], v[74:77], v[166:169], v[82:97]
	ds_read_b128 v[130:133], v210 offset:0
	ds_read_b128 v[134:137], v210 offset:1024
	v_exp_f32_e32 v216, v34
	v_fma_f32 v251, v212, s12, s12
	v_exp_f32_e32 v217, v38
	v_fma_f32 v252, v213, s12, s12
	v_exp_f32_e32 v218, v42
	v_fma_f32 v253, v214, s12, s12
	v_exp_f32_e32 v219, v46
	v_fma_f32 v254, v215, s12, s12
	v_mfma_f32_32x32x16_bf16 v[82:97], v[70:73], v[224:227], v[82:97]
	ds_read_b128 v[142:145], v210 offset:3072
	v_exp_f32_e32 v220, v35
	v_fmac_f32_e32 v251, v216, v251
	v_exp_f32_e32 v221, v39
	v_fmac_f32_e32 v252, v217, v252
	v_exp_f32_e32 v222, v43
	v_fmac_f32_e32 v253, v218, v253
	v_exp_f32_e32 v223, v47
	v_fmac_f32_e32 v254, v219, v254
	v_mfma_f32_32x32x16_bf16 v[82:97], v[66:69], v[174:177], v[82:97]
	ds_read_b128 v[146:149], v210 offset:4096
	ds_read_b128 v[150:153], v210 offset:5120
	v_rcp_f32_e32 v216, v251
	v_add_f32_e32 v220, 1.0, v220
	v_rcp_f32_e32 v217, v252
	v_add_f32_e32 v221, 1.0, v221
	v_rcp_f32_e32 v218, v253
	v_add_f32_e32 v222, 1.0, v222
	v_rcp_f32_e32 v219, v254
	v_add_f32_e32 v223, 1.0, v223
	v_mfma_f32_32x32x16_bf16 v[82:97], v[62:65], v[178:181], v[82:97]
	ds_read_b128 v[154:157], v210 offset:6144
	ds_read_b128 v[158:161], v210 offset:7168
	v_rcp_f32_e32 v220, v220
	v_fma_f32 v240, -v212, v216, v216
	v_rcp_f32_e32 v221, v221
	v_fma_f32 v241, -v213, v217, v217
	v_rcp_f32_e32 v222, v222
	v_fma_f32 v242, -v214, v218, v218
	v_rcp_f32_e32 v223, v223
	v_fma_f32 v243, -v215, v219, v219
	v_mfma_f32_32x32x16_bf16 v[82:97], v[58:61], v[182:185], v[82:97]
	v_exp_f32_e32 v246, v37
	v_fma_f32 v202, v220, v202, v240
	v_exp_f32_e32 v247, v41
	v_fma_f32 v203, v221, v203, v241
	v_exp_f32_e32 v248, v45
	v_fma_f32 v204, v222, v204, v242
	v_exp_f32_e32 v249, v49
	v_fma_f32 v205, v223, v205, v243
	v_mfma_f32_32x32x16_bf16 v[82:97], v[54:57], v[186:189], v[82:97]
	v_exp_f32_e32 v212, v202
	v_add_f32_e32 v246, 1.0, v246
	v_exp_f32_e32 v213, v203
	v_add_f32_e32 v247, 1.0, v247
	v_exp_f32_e32 v214, v204
	v_add_f32_e32 v248, 1.0, v248
	v_exp_f32_e32 v215, v205
	v_add_f32_e32 v249, 1.0, v249
	v_fmac_f32_e32 v246, v246, v212
	v_fmac_f32_e32 v247, v247, v213
	v_fmac_f32_e32 v248, v248, v214
	v_fmac_f32_e32 v249, v249, v215
	v_mfma_f32_32x32x16_bf16 v[82:97], v[50:53], v[190:193], v[82:97]
	v_rcp_f32_e32 v246, v246
	v_rcp_f32_e32 v247, v247
	v_rcp_f32_e32 v248, v248
	v_rcp_f32_e32 v249, v249
	v_fma_f32 v246, -v212, v246, v246
	v_fma_f32 v247, -v213, v247, v247
	v_fma_f32 v248, -v214, v248, v248
	v_fma_f32 v249, -v215, v249, v249
	v_cvt_pk_bf16_f32 v224, v246, v247
	v_cvt_pk_bf16_f32 v225, v248, v249
	s_waitcnt lgkmcnt(0)
	v_mfma_f32_32x32x16_bf16 v[2:17], v[126:129], v[130:133], v[2:17]
	v_add_u32_e32 v234, v231, v245
	ds_read_b128 v[34:37], v234 offset:0
	ds_read_b128 v[38:41], v234 offset:16
	ds_read_b128 v[42:45], v234 offset:32
	ds_read_b128 v[46:49], v234 offset:48
	v_add_u32_e32 v232, 0x100, v232
	v_exp_f32_e32 v212, v84
	v_exp_f32_e32 v213, v88
	v_exp_f32_e32 v214, v92
	v_exp_f32_e32 v215, v96
	v_mfma_f32_32x32x16_bf16 v[2:17], v[122:125], v[134:137], v[2:17]
	v_exp_f32_e32 v216, v82
	v_fma_f32 v251, v212, s12, s12
	v_exp_f32_e32 v217, v86
	v_fma_f32 v252, v213, s12, s12
	v_exp_f32_e32 v218, v90
	v_fma_f32 v253, v214, s12, s12
	v_exp_f32_e32 v219, v94
	v_fma_f32 v254, v215, s12, s12
	v_mfma_f32_32x32x16_bf16 v[2:17], v[118:121], v[236:239], v[2:17]
	v_exp_f32_e32 v220, v83
	v_fmac_f32_e32 v251, v216, v251
	v_exp_f32_e32 v221, v87
	v_fmac_f32_e32 v252, v217, v252
	v_exp_f32_e32 v222, v91
	v_fmac_f32_e32 v253, v218, v253
	v_exp_f32_e32 v223, v95
	v_fmac_f32_e32 v254, v219, v254
	v_mfma_f32_32x32x16_bf16 v[2:17], v[114:117], v[142:145], v[2:17]
	v_rcp_f32_e32 v216, v251
	v_add_f32_e32 v220, 1.0, v220
	v_rcp_f32_e32 v217, v252
	v_add_f32_e32 v221, 1.0, v221
	v_rcp_f32_e32 v218, v253
	v_add_f32_e32 v222, 1.0, v222
	v_rcp_f32_e32 v219, v254
	v_add_f32_e32 v223, 1.0, v223
	v_mfma_f32_32x32x16_bf16 v[2:17], v[110:113], v[146:149], v[2:17]
	v_rcp_f32_e32 v220, v220
	v_fma_f32 v240, -v212, v216, v216
	v_rcp_f32_e32 v221, v221
	v_fma_f32 v241, -v213, v217, v217
	v_rcp_f32_e32 v222, v222
	v_fma_f32 v242, -v214, v218, v218
	v_rcp_f32_e32 v223, v223
	v_fma_f32 v243, -v215, v219, v219
	v_mfma_f32_32x32x16_bf16 v[2:17], v[106:109], v[150:153], v[2:17]
	v_exp_f32_e32 v246, v85
	v_fma_f32 v206, v220, v206, v240
	v_exp_f32_e32 v247, v89
	v_fma_f32 v207, v221, v207, v241
	v_exp_f32_e32 v248, v93
	v_fma_f32 v208, v222, v208, v242
	v_exp_f32_e32 v249, v97
	v_fma_f32 v209, v223, v209, v243
	v_mfma_f32_32x32x16_bf16 v[2:17], v[102:105], v[154:157], v[2:17]
	v_exp_f32_e32 v212, v206
	v_add_f32_e32 v246, 1.0, v246
	v_exp_f32_e32 v213, v207
	v_add_f32_e32 v247, 1.0, v247
	v_exp_f32_e32 v214, v208
	v_add_f32_e32 v248, 1.0, v248
	v_exp_f32_e32 v215, v209
	v_add_f32_e32 v249, 1.0, v249
	v_fmac_f32_e32 v246, v246, v212
	v_fmac_f32_e32 v247, v247, v213
	v_fmac_f32_e32 v248, v248, v214
	v_fmac_f32_e32 v249, v249, v215
	v_mfma_f32_32x32x16_bf16 v[2:17], v[98:101], v[158:161], v[2:17]
	v_rcp_f32_e32 v246, v246
	v_rcp_f32_e32 v247, v247
	v_rcp_f32_e32 v248, v248
	v_rcp_f32_e32 v249, v249
	v_fma_f32 v246, -v212, v246, v246
	v_fma_f32 v247, -v213, v247, v247
	v_fma_f32 v248, -v214, v248, v248
	v_fma_f32 v249, -v215, v249, v249
	v_cvt_pk_bf16_f32 v226, v246, v247
	v_cvt_pk_bf16_f32 v227, v248, v249
	ds_write_b128 v211, v[224:227] offset:8192
	s_sub_u32 s16, s16, 1
	s_cmp_lg_u32 s16, 0
	s_cbranch_scc1 .Llight_loop_w2
	v_mfma_f32_32x32x16_bf16 v[18:33], v[78:81], v[130:133], v[18:33]
	ds_read_b128 v[82:85], v234 offset:128
	ds_read_b128 v[86:89], v234 offset:144
	ds_read_b128 v[90:93], v234 offset:160
	ds_read_b128 v[94:97], v234 offset:176
	v_exp_f32_e32 v212, v4
	v_exp_f32_e32 v213, v8
	v_exp_f32_e32 v214, v12
	v_exp_f32_e32 v215, v16
	s_waitcnt lgkmcnt(4)
	s_barrier
	v_mfma_f32_32x32x16_bf16 v[18:33], v[74:77], v[134:137], v[18:33]
	ds_read_b128 v[162:165], v210 offset:8192
	ds_read_b128 v[166:169], v210 offset:9216
	v_exp_f32_e32 v216, v2
	v_fma_f32 v251, v212, s12, s12
	v_exp_f32_e32 v217, v6
	v_fma_f32 v252, v213, s12, s12
	v_exp_f32_e32 v218, v10
	v_fma_f32 v253, v214, s12, s12
	v_exp_f32_e32 v219, v14
	v_fma_f32 v254, v215, s12, s12
	v_mfma_f32_32x32x16_bf16 v[18:33], v[70:73], v[236:239], v[18:33]
	ds_read_b128 v[174:177], v210 offset:11264
	v_exp_f32_e32 v220, v3
	v_fmac_f32_e32 v251, v216, v251
	v_exp_f32_e32 v221, v7
	v_fmac_f32_e32 v252, v217, v252
	v_exp_f32_e32 v222, v11
	v_fmac_f32_e32 v253, v218, v253
	v_exp_f32_e32 v223, v15
	v_fmac_f32_e32 v254, v219, v254
	v_mfma_f32_32x32x16_bf16 v[18:33], v[66:69], v[142:145], v[18:33]
	ds_read_b128 v[178:181], v210 offset:12288
	ds_read_b128 v[182:185], v210 offset:13312
	v_rcp_f32_e32 v216, v251
	v_add_f32_e32 v220, 1.0, v220
	v_rcp_f32_e32 v217, v252
	v_add_f32_e32 v221, 1.0, v221
	v_rcp_f32_e32 v218, v253
	v_add_f32_e32 v222, 1.0, v222
	v_rcp_f32_e32 v219, v254
	v_add_f32_e32 v223, 1.0, v223
	v_mfma_f32_32x32x16_bf16 v[18:33], v[62:65], v[146:149], v[18:33]
	ds_read_b128 v[186:189], v210 offset:14336
	ds_read_b128 v[190:193], v210 offset:15360
	v_rcp_f32_e32 v220, v220
	v_fma_f32 v240, -v212, v216, v216
	v_rcp_f32_e32 v221, v221
	v_fma_f32 v241, -v213, v217, v217
	v_rcp_f32_e32 v222, v222
	v_fma_f32 v242, -v214, v218, v218
	v_rcp_f32_e32 v223, v223
	v_fma_f32 v243, -v215, v219, v219
	v_mfma_f32_32x32x16_bf16 v[18:33], v[58:61], v[150:153], v[18:33]
	v_exp_f32_e32 v246, v5
	v_fma_f32 v194, v220, v194, v240
	v_exp_f32_e32 v247, v9
	v_fma_f32 v195, v221, v195, v241
	v_exp_f32_e32 v248, v13
	v_fma_f32 v196, v222, v196, v242
	v_exp_f32_e32 v249, v17
	v_fma_f32 v197, v223, v197, v243
	v_mfma_f32_32x32x16_bf16 v[18:33], v[54:57], v[154:157], v[18:33]
	v_exp_f32_e32 v212, v194
	v_add_f32_e32 v246, 1.0, v246
	v_exp_f32_e32 v213, v195
	v_add_f32_e32 v247, 1.0, v247
	v_exp_f32_e32 v214, v196
	v_add_f32_e32 v248, 1.0, v248
	v_exp_f32_e32 v215, v197
	v_add_f32_e32 v249, 1.0, v249
	v_fmac_f32_e32 v246, v246, v212
	v_fmac_f32_e32 v247, v247, v213
	v_fmac_f32_e32 v248, v248, v214
	v_fmac_f32_e32 v249, v249, v215
	v_mfma_f32_32x32x16_bf16 v[18:33], v[50:53], v[158:161], v[18:33]
	v_rcp_f32_e32 v246, v246
	v_rcp_f32_e32 v247, v247
	v_rcp_f32_e32 v248, v248
	v_rcp_f32_e32 v249, v249
	v_fma_f32 v246, -v212, v246, v246
	v_fma_f32 v247, -v213, v247, v247
	v_fma_f32 v248, -v214, v248, v248
	v_fma_f32 v249, -v215, v249, v249
	v_cvt_pk_bf16_f32 v236, v246, v247
	v_cvt_pk_bf16_f32 v237, v248, v249
	s_waitcnt lgkmcnt(0)
	v_mfma_f32_32x32x16_bf16 v[34:49], v[126:129], v[162:165], v[34:49]
	v_exp_f32_e32 v212, v20
	v_exp_f32_e32 v213, v24
	v_exp_f32_e32 v214, v28
	v_exp_f32_e32 v215, v32
	v_mfma_f32_32x32x16_bf16 v[34:49], v[122:125], v[166:169], v[34:49]
	v_exp_f32_e32 v216, v18
	v_fma_f32 v251, v212, s12, s12
	v_exp_f32_e32 v217, v22
	v_fma_f32 v252, v213, s12, s12
	v_exp_f32_e32 v218, v26
	v_fma_f32 v253, v214, s12, s12
	v_exp_f32_e32 v219, v30
	v_fma_f32 v254, v215, s12, s12
	v_mfma_f32_32x32x16_bf16 v[34:49], v[118:121], v[224:227], v[34:49]
	v_exp_f32_e32 v220, v19
	v_fmac_f32_e32 v251, v216, v251
	v_exp_f32_e32 v221, v23
	v_fmac_f32_e32 v252, v217, v252
	v_exp_f32_e32 v222, v27
	v_fmac_f32_e32 v253, v218, v253
	v_exp_f32_e32 v223, v31
	v_fmac_f32_e32 v254, v219, v254
	v_mfma_f32_32x32x16_bf16 v[34:49], v[114:117], v[174:177], v[34:49]
	v_rcp_f32_e32 v216, v251
	v_add_f32_e32 v220, 1.0, v220
	v_rcp_f32_e32 v217, v252
	v_add_f32_e32 v221, 1.0, v221
	v_rcp_f32_e32 v218, v253
	v_add_f32_e32 v222, 1.0, v222
	v_rcp_f32_e32 v219, v254
	v_add_f32_e32 v223, 1.0, v223
	v_mfma_f32_32x32x16_bf16 v[34:49], v[110:113], v[178:181], v[34:49]
	v_rcp_f32_e32 v220, v220
	v_fma_f32 v240, -v212, v216, v216
	v_rcp_f32_e32 v221, v221
	v_fma_f32 v241, -v213, v217, v217
	v_rcp_f32_e32 v222, v222
	v_fma_f32 v242, -v214, v218, v218
	v_rcp_f32_e32 v223, v223
	v_fma_f32 v243, -v215, v219, v219
	v_mfma_f32_32x32x16_bf16 v[34:49], v[106:109], v[182:185], v[34:49]
	v_exp_f32_e32 v246, v21
	v_fma_f32 v198, v220, v198, v240
	v_exp_f32_e32 v247, v25
	v_fma_f32 v199, v221, v199, v241
	v_exp_f32_e32 v248, v29
	v_fma_f32 v200, v222, v200, v242
	v_exp_f32_e32 v249, v33
	v_fma_f32 v201, v223, v201, v243
	v_mfma_f32_32x32x16_bf16 v[34:49], v[102:105], v[186:189], v[34:49]
	v_exp_f32_e32 v212, v198
	v_add_f32_e32 v246, 1.0, v246
	v_exp_f32_e32 v213, v199
	v_add_f32_e32 v247, 1.0, v247
	v_exp_f32_e32 v214, v200
	v_add_f32_e32 v248, 1.0, v248
	v_exp_f32_e32 v215, v201
	v_add_f32_e32 v249, 1.0, v249
	v_fmac_f32_e32 v246, v246, v212
	v_fmac_f32_e32 v247, v247, v213
	v_fmac_f32_e32 v248, v248, v214
	v_fmac_f32_e32 v249, v249, v215
	v_mfma_f32_32x32x16_bf16 v[34:49], v[98:101], v[190:193], v[34:49]
	v_rcp_f32_e32 v246, v246
	v_rcp_f32_e32 v247, v247
	v_rcp_f32_e32 v248, v248
	v_rcp_f32_e32 v249, v249
	v_fma_f32 v246, -v212, v246, v246
	v_fma_f32 v247, -v213, v247, v247
	v_fma_f32 v248, -v214, v248, v248
	v_fma_f32 v249, -v215, v249, v249
	v_cvt_pk_bf16_f32 v238, v246, v247
	v_cvt_pk_bf16_f32 v239, v248, v249
	ds_write_b128 v211, v[236:239] offset:0
	s_waitcnt lgkmcnt(0)
	s_barrier
	s_bfe_u32 s20, s19, 0x10006
	s_lshl_b32 s21, s20, 7
	s_lshl_b32 s20, s20, 13
	s_add_u32 s20, s20, 0x30000
	s_add_u32 s22, s14, s20
	s_addc_u32 s23, s15, 0
	s_add_u32 s24, s22, 0x1000
	s_addc_u32 s25, s23, 0
	global_load_dwordx4 v[98:101], v210, s[22:23] offset:0
	global_load_dwordx4 v[102:105], v210, s[22:23] offset:1024
	global_load_dwordx4 v[106:109], v210, s[22:23] offset:2048
	global_load_dwordx4 v[110:113], v210, s[22:23] offset:3072
	global_load_dwordx4 v[114:117], v210, s[24:25] offset:0
	global_load_dwordx4 v[118:121], v210, s[24:25] offset:1024
	global_load_dwordx4 v[122:125], v210, s[24:25] offset:2048
	global_load_dwordx4 v[126:129], v210, s[24:25] offset:3072
	v_or_b32_e32 v250, s21, v230
	global_load_dwordx4 v[130:133], v250, s[4:5] offset:0
	global_load_dwordx4 v[134:137], v250, s[4:5] offset:32
	global_load_dwordx4 v[138:141], v250, s[4:5] offset:64
	global_load_dwordx4 v[142:145], v250, s[4:5] offset:96
	global_load_dwordx4 v[146:149], v250, s[6:7] offset:0
	global_load_dwordx4 v[150:153], v250, s[6:7] offset:32
	global_load_dwordx4 v[154:157], v250, s[6:7] offset:64
	global_load_dwordx4 v[158:161], v250, s[6:7] offset:96
	s_load_dword s26, s[8:9], 0x0
	v_mfma_f32_32x32x16_bf16 v[82:97], v[78:81], v[162:165], v[82:97]
	v_exp_f32_e32 v212, v36
	v_exp_f32_e32 v213, v40
	v_exp_f32_e32 v214, v44
	v_exp_f32_e32 v215, v48
	v_mfma_f32_32x32x16_bf16 v[82:97], v[74:77], v[166:169], v[82:97]
	v_exp_f32_e32 v216, v34
	v_fma_f32 v251, v212, s12, s12
	v_exp_f32_e32 v217, v38
	v_fma_f32 v252, v213, s12, s12
	v_exp_f32_e32 v218, v42
	v_fma_f32 v253, v214, s12, s12
	v_exp_f32_e32 v219, v46
	v_fma_f32 v254, v215, s12, s12
	v_mfma_f32_32x32x16_bf16 v[82:97], v[70:73], v[224:227], v[82:97]
	v_exp_f32_e32 v220, v35
	v_fmac_f32_e32 v251, v216, v251
	v_exp_f32_e32 v221, v39
	v_fmac_f32_e32 v252, v217, v252
	v_exp_f32_e32 v222, v43
	v_fmac_f32_e32 v253, v218, v253
	v_exp_f32_e32 v223, v47
	v_fmac_f32_e32 v254, v219, v254
	v_mfma_f32_32x32x16_bf16 v[82:97], v[66:69], v[174:177], v[82:97]
	v_rcp_f32_e32 v216, v251
	v_add_f32_e32 v220, 1.0, v220
	v_rcp_f32_e32 v217, v252
	v_add_f32_e32 v221, 1.0, v221
	v_rcp_f32_e32 v218, v253
	v_add_f32_e32 v222, 1.0, v222
	v_rcp_f32_e32 v219, v254
	v_add_f32_e32 v223, 1.0, v223
	v_mfma_f32_32x32x16_bf16 v[82:97], v[62:65], v[178:181], v[82:97]
	v_rcp_f32_e32 v220, v220
	v_fma_f32 v240, -v212, v216, v216
	v_rcp_f32_e32 v221, v221
	v_fma_f32 v241, -v213, v217, v217
	v_rcp_f32_e32 v222, v222
	v_fma_f32 v242, -v214, v218, v218
	v_rcp_f32_e32 v223, v223
	v_fma_f32 v243, -v215, v219, v219
	v_mfma_f32_32x32x16_bf16 v[82:97], v[58:61], v[182:185], v[82:97]
	v_exp_f32_e32 v246, v37
	v_fma_f32 v202, v220, v202, v240
	v_exp_f32_e32 v247, v41
	v_fma_f32 v203, v221, v203, v241
	v_exp_f32_e32 v248, v45
	v_fma_f32 v204, v222, v204, v242
	v_exp_f32_e32 v249, v49
	v_fma_f32 v205, v223, v205, v243
	v_mfma_f32_32x32x16_bf16 v[82:97], v[54:57], v[186:189], v[82:97]
	v_exp_f32_e32 v212, v202
	v_add_f32_e32 v246, 1.0, v246
	v_exp_f32_e32 v213, v203
	v_add_f32_e32 v247, 1.0, v247
	v_exp_f32_e32 v214, v204
	v_add_f32_e32 v248, 1.0, v248
	v_exp_f32_e32 v215, v205
	v_add_f32_e32 v249, 1.0, v249
	v_fmac_f32_e32 v246, v246, v212
	v_fmac_f32_e32 v247, v247, v213
	v_fmac_f32_e32 v248, v248, v214
	v_fmac_f32_e32 v249, v249, v215
	v_mfma_f32_32x32x16_bf16 v[82:97], v[50:53], v[190:193], v[82:97]
	v_rcp_f32_e32 v246, v246
	v_rcp_f32_e32 v247, v247
	v_rcp_f32_e32 v248, v248
	v_rcp_f32_e32 v249, v249
	v_fma_f32 v246, -v212, v246, v246
	v_fma_f32 v247, -v213, v247, v247
	v_fma_f32 v248, -v214, v248, v248
	v_fma_f32 v249, -v215, v249, v249
	v_cvt_pk_bf16_f32 v224, v246, v247
	v_cvt_pk_bf16_f32 v225, v248, v249
	s_waitcnt lgkmcnt(0)
	v_exp_f32_e32 v212, v84
	v_exp_f32_e32 v213, v88
	v_exp_f32_e32 v214, v92
	v_exp_f32_e32 v215, v96
	v_exp_f32_e32 v216, v82
	v_fma_f32 v251, v212, s12, s12
	v_exp_f32_e32 v217, v86
	v_fma_f32 v252, v213, s12, s12
	v_exp_f32_e32 v218, v90
	v_fma_f32 v253, v214, s12, s12
	v_exp_f32_e32 v219, v94
	v_fma_f32 v254, v215, s12, s12
	v_exp_f32_e32 v220, v83
	v_fmac_f32_e32 v251, v216, v251
	v_exp_f32_e32 v221, v87
	v_fmac_f32_e32 v252, v217, v252
	v_exp_f32_e32 v222, v91
	v_fmac_f32_e32 v253, v218, v253
	v_exp_f32_e32 v223, v95
	v_fmac_f32_e32 v254, v219, v254
	v_rcp_f32_e32 v216, v251
	v_add_f32_e32 v220, 1.0, v220
	v_rcp_f32_e32 v217, v252
	v_add_f32_e32 v221, 1.0, v221
	v_rcp_f32_e32 v218, v253
	v_add_f32_e32 v222, 1.0, v222
	v_rcp_f32_e32 v219, v254
	v_add_f32_e32 v223, 1.0, v223
	v_rcp_f32_e32 v220, v220
	v_fma_f32 v240, -v212, v216, v216
	v_rcp_f32_e32 v221, v221
	v_fma_f32 v241, -v213, v217, v217
	v_rcp_f32_e32 v222, v222
	v_fma_f32 v242, -v214, v218, v218
	v_rcp_f32_e32 v223, v223
	v_fma_f32 v243, -v215, v219, v219
	v_exp_f32_e32 v246, v85
	v_fma_f32 v206, v220, v206, v240
	v_exp_f32_e32 v247, v89
	v_fma_f32 v207, v221, v207, v241
	v_exp_f32_e32 v248, v93
	v_fma_f32 v208, v222, v208, v242
	v_exp_f32_e32 v249, v97
	v_fma_f32 v209, v223, v209, v243
	v_exp_f32_e32 v212, v206
	v_add_f32_e32 v246, 1.0, v246
	v_exp_f32_e32 v213, v207
	v_add_f32_e32 v247, 1.0, v247
	v_exp_f32_e32 v214, v208
	v_add_f32_e32 v248, 1.0, v248
	v_exp_f32_e32 v215, v209
	v_add_f32_e32 v249, 1.0, v249
	v_fmac_f32_e32 v246, v246, v212
	v_fmac_f32_e32 v247, v247, v213
	v_fmac_f32_e32 v248, v248, v214
	v_fmac_f32_e32 v249, v249, v215
	v_rcp_f32_e32 v246, v246
	v_rcp_f32_e32 v247, v247
	v_rcp_f32_e32 v248, v248
	v_rcp_f32_e32 v249, v249
	v_fma_f32 v246, -v212, v246, v246
	v_fma_f32 v247, -v213, v247, v247
	v_fma_f32 v248, -v214, v248, v248
	v_fma_f32 v249, -v215, v249, v249
	v_cvt_pk_bf16_f32 v226, v246, v247
	v_cvt_pk_bf16_f32 v227, v248, v249
	ds_write_b128 v211, v[224:227] offset:8192
	s_waitcnt lgkmcnt(0)
	s_barrier
	s_lshl_b32 s20, s19, 6
	s_and_b32 s20, s20, 0x2000
	v_or_b32_e32 v20, s20, v210
	ds_read_b128 v[162:165], v20 offset:0
	ds_read_b128 v[166:169], v20 offset:1024
	ds_read_b128 v[170:173], v20 offset:2048
	ds_read_b128 v[174:177], v20 offset:3072
	ds_read_b128 v[178:181], v20 offset:4096
	ds_read_b128 v[182:185], v20 offset:5120
	ds_read_b128 v[186:189], v20 offset:6144
	ds_read_b128 v[190:193], v20 offset:7168
	s_bfe_u32 s20, s19, 0x10006
	s_lshl_b32 s20, s20, 9
	s_and_b32 s21, s19, 0x80
	s_or_b32 s20, s20, s21
	v_lshlrev_b32_e32 v19, 2, v229
	v_add3_u32 v19, s20, v19, v228
	s_waitcnt vmcnt(0)
	s_waitcnt lgkmcnt(7)
	v_mfma_f32_32x32x16_bf16 v[2:17], v[98:101], v[162:165], 0
	s_waitcnt lgkmcnt(6)
	v_mfma_f32_32x32x16_bf16 v[2:17], v[102:105], v[166:169], v[2:17]
	s_waitcnt lgkmcnt(5)
	v_mfma_f32_32x32x16_bf16 v[2:17], v[106:109], v[170:173], v[2:17]
	s_waitcnt lgkmcnt(4)
	v_mfma_f32_32x32x16_bf16 v[2:17], v[110:113], v[174:177], v[2:17]
	s_waitcnt lgkmcnt(3)
	v_mfma_f32_32x32x16_bf16 v[2:17], v[114:117], v[178:181], v[2:17]
	s_waitcnt lgkmcnt(2)
	v_mfma_f32_32x32x16_bf16 v[2:17], v[118:121], v[182:185], v[2:17]
	s_waitcnt lgkmcnt(1)
	v_mfma_f32_32x32x16_bf16 v[2:17], v[122:125], v[186:189], v[2:17]
	s_waitcnt lgkmcnt(0)
	v_mfma_f32_32x32x16_bf16 v[2:17], v[126:129], v[190:193], v[2:17]
	s_nop 15
	s_nop 3
	v_add_f32_e32 v2, v2, v130
	v_add_f32_e32 v3, v3, v131
	v_add_f32_e32 v4, v4, v132
	v_add_f32_e32 v5, v5, v133
	v_add_f32_e32 v6, v6, v134
	v_add_f32_e32 v7, v7, v135
	v_add_f32_e32 v8, v8, v136
	v_add_f32_e32 v9, v9, v137
	v_add_f32_e32 v10, v10, v138
	v_add_f32_e32 v11, v11, v139
	v_add_f32_e32 v12, v12, v140
	v_add_f32_e32 v13, v13, v141
	v_add_f32_e32 v14, v14, v142
	v_add_f32_e32 v15, v15, v143
	v_add_f32_e32 v16, v16, v144
	v_add_f32_e32 v17, v17, v145
	v_max_f32_e32 v2, 0, v2
	v_max_f32_e32 v3, 0, v3
	v_max_f32_e32 v4, 0, v4
	v_max_f32_e32 v5, 0, v5
	v_max_f32_e32 v6, 0, v6
	v_max_f32_e32 v7, 0, v7
	v_max_f32_e32 v8, 0, v8
	v_max_f32_e32 v9, 0, v9
	v_max_f32_e32 v10, 0, v10
	v_max_f32_e32 v11, 0, v11
	v_max_f32_e32 v12, 0, v12
	v_max_f32_e32 v13, 0, v13
	v_max_f32_e32 v14, 0, v14
	v_max_f32_e32 v15, 0, v15
	v_max_f32_e32 v16, 0, v16
	v_max_f32_e32 v17, 0, v17
	v_fma_f32 v18, v2, v146, 0
	v_fmac_f32_e32 v18, v3, v147
	v_fmac_f32_e32 v18, v4, v148
	v_fmac_f32_e32 v18, v5, v149
	v_fmac_f32_e32 v18, v6, v150
	v_fmac_f32_e32 v18, v7, v151
	v_fmac_f32_e32 v18, v8, v152
	v_fmac_f32_e32 v18, v9, v153
	v_fmac_f32_e32 v18, v10, v154
	v_fmac_f32_e32 v18, v11, v155
	v_fmac_f32_e32 v18, v12, v156
	v_fmac_f32_e32 v18, v13, v157
	v_fmac_f32_e32 v18, v14, v158
	v_fmac_f32_e32 v18, v15, v159
	v_fmac_f32_e32 v18, v16, v160
	v_fmac_f32_e32 v18, v17, v161
	ds_write_b32 v19, v18 offset:35904
	s_branch .LBB1_40
.Llight_w3:
	ds_read_b128 v[82:85], v234 offset:128
	ds_read_b128 v[86:89], v234 offset:144
	ds_read_b128 v[90:93], v234 offset:160
	ds_read_b128 v[94:97], v234 offset:176
	ds_read2_b32 v[244:245], v232 offset1:32
	v_exp_f32_e32 v212, v4
	v_exp_f32_e32 v213, v8
	v_exp_f32_e32 v214, v12
	v_exp_f32_e32 v215, v16
	v_exp_f32_e32 v216, v2
	v_fma_f32 v251, v212, s12, s12
	v_exp_f32_e32 v217, v6
	v_fma_f32 v252, v213, s12, s12
	v_exp_f32_e32 v218, v10
	v_fma_f32 v253, v214, s12, s12
	v_exp_f32_e32 v219, v14
	v_fma_f32 v254, v215, s12, s12
	v_fmac_f32_e32 v251, v216, v251
	v_fmac_f32_e32 v252, v217, v252
	v_fmac_f32_e32 v253, v218, v253
	v_fmac_f32_e32 v254, v219, v254
	v_rcp_f32_e32 v216, v251
	v_rcp_f32_e32 v217, v252
	v_rcp_f32_e32 v218, v253
	v_rcp_f32_e32 v219, v254
	v_exp_f32_e32 v246, v5
	v_fma_f32 v194, -v212, v216, v216
	v_exp_f32_e32 v247, v9
	v_fma_f32 v195, -v213, v217, v217
	v_exp_f32_e32 v248, v13
	v_fma_f32 v196, -v214, v218, v218
	v_exp_f32_e32 v249, v17
	v_fma_f32 v197, -v215, v219, v219
	v_exp_f32_e32 v212, v194
	v_add_f32_e32 v246, 1.0, v246
	v_exp_f32_e32 v213, v195
	v_add_f32_e32 v247, 1.0, v247
	v_exp_f32_e32 v214, v196
	v_add_f32_e32 v248, 1.0, v248
	v_exp_f32_e32 v215, v197
	v_add_f32_e32 v249, 1.0, v249
	v_fmac_f32_e32 v246, v246, v212
	v_fmac_f32_e32 v247, v247, v213
	v_fmac_f32_e32 v248, v248, v214
	v_fmac_f32_e32 v249, v249, v215
	v_rcp_f32_e32 v246, v246
	v_rcp_f32_e32 v247, v247
	v_rcp_f32_e32 v248, v248
	v_rcp_f32_e32 v249, v249
	v_fma_f32 v246, -v212, v246, v246
	v_fma_f32 v247, -v213, v247, v247
	v_fma_f32 v248, -v214, v248, v248
	v_fma_f32 v249, -v215, v249, v249
	v_cvt_pk_bf16_f32 v236, v246, v247
	v_cvt_pk_bf16_f32 v237, v248, v249
	s_waitcnt lgkmcnt(0)
	v_add_u32_e32 v233, v231, v244
	ds_read_b128 v[2:5], v233 offset:0
	ds_read_b128 v[6:9], v233 offset:16
	ds_read_b128 v[10:13], v233 offset:32
	ds_read_b128 v[14:17], v233 offset:48
	v_exp_f32_e32 v212, v20
	v_exp_f32_e32 v213, v24
	v_exp_f32_e32 v214, v28
	v_exp_f32_e32 v215, v32
	v_exp_f32_e32 v216, v18
	v_fma_f32 v251, v212, s12, s12
	v_exp_f32_e32 v217, v22
	v_fma_f32 v252, v213, s12, s12
	v_exp_f32_e32 v218, v26
	v_fma_f32 v253, v214, s12, s12
	v_exp_f32_e32 v219, v30
	v_fma_f32 v254, v215, s12, s12
	v_fmac_f32_e32 v251, v216, v251
	v_fmac_f32_e32 v252, v217, v252
	v_fmac_f32_e32 v253, v218, v253
	v_fmac_f32_e32 v254, v219, v254
	v_rcp_f32_e32 v216, v251
	v_rcp_f32_e32 v217, v252
	v_rcp_f32_e32 v218, v253
	v_rcp_f32_e32 v219, v254
	v_exp_f32_e32 v246, v21
	v_fma_f32 v198, -v212, v216, v216
	v_exp_f32_e32 v247, v25
	v_fma_f32 v199, -v213, v217, v217
	v_exp_f32_e32 v248, v29
	v_fma_f32 v200, -v214, v218, v218
	v_exp_f32_e32 v249, v33
	v_fma_f32 v201, -v215, v219, v219
	v_exp_f32_e32 v212, v198
	v_add_f32_e32 v246, 1.0, v246
	v_exp_f32_e32 v213, v199
	v_add_f32_e32 v247, 1.0, v247
	v_exp_f32_e32 v214, v200
	v_add_f32_e32 v248, 1.0, v248
	v_exp_f32_e32 v215, v201
	v_add_f32_e32 v249, 1.0, v249
	v_fmac_f32_e32 v246, v246, v212
	v_fmac_f32_e32 v247, v247, v213
	v_fmac_f32_e32 v248, v248, v214
	v_fmac_f32_e32 v249, v249, v215
	v_rcp_f32_e32 v246, v246
	v_rcp_f32_e32 v247, v247
	v_rcp_f32_e32 v248, v248
	v_rcp_f32_e32 v249, v249
	v_fma_f32 v246, -v212, v246, v246
	v_fma_f32 v247, -v213, v247, v247
	v_fma_f32 v248, -v214, v248, v248
	v_fma_f32 v249, -v215, v249, v249
	v_cvt_pk_bf16_f32 v238, v246, v247
	v_cvt_pk_bf16_f32 v239, v248, v249
	ds_write_b128 v211, v[236:239] offset:0
	ds_read_b128 v[18:21], v233 offset:128
	ds_read_b128 v[22:25], v233 offset:144
	ds_read_b128 v[26:29], v233 offset:160
	ds_read_b128 v[30:33], v233 offset:176
	v_exp_f32_e32 v212, v36
	v_exp_f32_e32 v213, v40
	v_exp_f32_e32 v214, v44
	v_exp_f32_e32 v215, v48
	s_waitcnt lgkmcnt(4)
	s_barrier
	ds_read_b128 v[130:133], v210 offset:0
	ds_read_b128 v[134:137], v210 offset:1024
	v_exp_f32_e32 v216, v34
	v_fma_f32 v251, v212, s12, s12
	v_exp_f32_e32 v217, v38
	v_fma_f32 v252, v213, s12, s12
	v_exp_f32_e32 v218, v42
	v_fma_f32 v253, v214, s12, s12
	v_exp_f32_e32 v219, v46
	v_fma_f32 v254, v215, s12, s12
	ds_read_b128 v[138:141], v210 offset:2048
	v_fmac_f32_e32 v251, v216, v251
	v_fmac_f32_e32 v252, v217, v252
	v_fmac_f32_e32 v253, v218, v253
	v_fmac_f32_e32 v254, v219, v254
	ds_read_b128 v[146:149], v210 offset:4096
	ds_read_b128 v[150:153], v210 offset:5120
	v_rcp_f32_e32 v216, v251
	v_rcp_f32_e32 v217, v252
	v_rcp_f32_e32 v218, v253
	v_rcp_f32_e32 v219, v254
	ds_read_b128 v[154:157], v210 offset:6144
	ds_read_b128 v[158:161], v210 offset:7168
	v_exp_f32_e32 v246, v37
	v_fma_f32 v202, -v212, v216, v216
	v_exp_f32_e32 v247, v41
	v_fma_f32 v203, -v213, v217, v217
	v_exp_f32_e32 v248, v45
	v_fma_f32 v204, -v214, v218, v218
	v_exp_f32_e32 v249, v49
	v_fma_f32 v205, -v215, v219, v219
	v_exp_f32_e32 v212, v202
	v_add_f32_e32 v246, 1.0, v246
	v_exp_f32_e32 v213, v203
	v_add_f32_e32 v247, 1.0, v247
	v_exp_f32_e32 v214, v204
	v_add_f32_e32 v248, 1.0, v248
	v_exp_f32_e32 v215, v205
	v_add_f32_e32 v249, 1.0, v249
	v_fmac_f32_e32 v246, v246, v212
	v_fmac_f32_e32 v247, v247, v213
	v_fmac_f32_e32 v248, v248, v214
	v_fmac_f32_e32 v249, v249, v215
	v_rcp_f32_e32 v246, v246
	v_rcp_f32_e32 v247, v247
	v_rcp_f32_e32 v248, v248
	v_rcp_f32_e32 v249, v249
	v_fma_f32 v246, -v212, v246, v246
	v_fma_f32 v247, -v213, v247, v247
	v_fma_f32 v248, -v214, v248, v248
	v_fma_f32 v249, -v215, v249, v249
	v_cvt_pk_bf16_f32 v224, v246, v247
	v_cvt_pk_bf16_f32 v225, v248, v249
	s_waitcnt lgkmcnt(0)
	v_mfma_f32_32x32x16_bf16 v[2:17], v[126:129], v[130:133], v[2:17]
	v_add_u32_e32 v234, v231, v245
	ds_read_b128 v[34:37], v234 offset:0
	ds_read_b128 v[38:41], v234 offset:16
	ds_read_b128 v[42:45], v234 offset:32
	ds_read_b128 v[46:49], v234 offset:48
	v_add_u32_e32 v232, 0x100, v232
	v_exp_f32_e32 v212, v84
	v_exp_f32_e32 v213, v88
	v_exp_f32_e32 v214, v92
	v_exp_f32_e32 v215, v96
	v_mfma_f32_32x32x16_bf16 v[2:17], v[122:125], v[134:137], v[2:17]
	v_exp_f32_e32 v216, v82
	v_fma_f32 v251, v212, s12, s12
	v_exp_f32_e32 v217, v86
	v_fma_f32 v252, v213, s12, s12
	v_exp_f32_e32 v218, v90
	v_fma_f32 v253, v214, s12, s12
	v_exp_f32_e32 v219, v94
	v_fma_f32 v254, v215, s12, s12
	v_mfma_f32_32x32x16_bf16 v[2:17], v[118:121], v[138:141], v[2:17]
	v_fmac_f32_e32 v251, v216, v251
	v_fmac_f32_e32 v252, v217, v252
	v_fmac_f32_e32 v253, v218, v253
	v_fmac_f32_e32 v254, v219, v254
	v_mfma_f32_32x32x16_bf16 v[2:17], v[114:117], v[236:239], v[2:17]
	v_rcp_f32_e32 v216, v251
	v_rcp_f32_e32 v217, v252
	v_rcp_f32_e32 v218, v253
	v_rcp_f32_e32 v219, v254
	v_mfma_f32_32x32x16_bf16 v[2:17], v[110:113], v[146:149], v[2:17]
	v_exp_f32_e32 v246, v85
	v_fma_f32 v206, -v212, v216, v216
	v_exp_f32_e32 v247, v89
	v_fma_f32 v207, -v213, v217, v217
	v_exp_f32_e32 v248, v93
	v_fma_f32 v208, -v214, v218, v218
	v_exp_f32_e32 v249, v97
	v_fma_f32 v209, -v215, v219, v219
	v_mfma_f32_32x32x16_bf16 v[2:17], v[106:109], v[150:153], v[2:17]
	v_mfma_f32_32x32x16_bf16 v[2:17], v[102:105], v[154:157], v[2:17]
	v_exp_f32_e32 v212, v206
	v_add_f32_e32 v246, 1.0, v246
	v_exp_f32_e32 v213, v207
	v_add_f32_e32 v247, 1.0, v247
	v_exp_f32_e32 v214, v208
	v_add_f32_e32 v248, 1.0, v248
	v_exp_f32_e32 v215, v209
	v_add_f32_e32 v249, 1.0, v249
	v_fmac_f32_e32 v246, v246, v212
	v_fmac_f32_e32 v247, v247, v213
	v_fmac_f32_e32 v248, v248, v214
	v_fmac_f32_e32 v249, v249, v215
	v_mfma_f32_32x32x16_bf16 v[2:17], v[98:101], v[158:161], v[2:17]
	v_rcp_f32_e32 v246, v246
	v_rcp_f32_e32 v247, v247
	v_rcp_f32_e32 v248, v248
	v_rcp_f32_e32 v249, v249
	v_fma_f32 v246, -v212, v246, v246
	v_fma_f32 v247, -v213, v247, v247
	v_fma_f32 v248, -v214, v248, v248
	v_fma_f32 v249, -v215, v249, v249
	v_cvt_pk_bf16_f32 v226, v246, v247
	v_cvt_pk_bf16_f32 v227, v248, v249
	ds_write_b128 v211, v[224:227] offset:8192
	.p2align 6
.Llight_loop_w3:
	v_mfma_f32_32x32x16_bf16 v[18:33], v[78:81], v[130:133], v[18:33]
	ds_read_b128 v[82:85], v234 offset:128
	ds_read_b128 v[86:89], v234 offset:144
	ds_read_b128 v[90:93], v234 offset:160
	ds_read_b128 v[94:97], v234 offset:176
	ds_read2_b32 v[244:245], v232 offset1:32
	v_exp_f32_e32 v212, v4
	v_exp_f32_e32 v213, v8
	v_exp_f32_e32 v214, v12
	v_exp_f32_e32 v215, v16
	s_waitcnt lgkmcnt(5)
	s_barrier
	v_mfma_f32_32x32x16_bf16 v[18:33], v[74:77], v[134:137], v[18:33]
	ds_read_b128 v[162:165], v210 offset:8192
	ds_read_b128 v[166:169], v210 offset:9216
	v_exp_f32_e32 v216, v2
	v_fma_f32 v251, v212, s12, s12
	v_exp_f32_e32 v217, v6
	v_fma_f32 v252, v213, s12, s12
	v_exp_f32_e32 v218, v10
	v_fma_f32 v253, v214, s12, s12
	v_exp_f32_e32 v219, v14
	v_fma_f32 v254, v215, s12, s12
	v_mfma_f32_32x32x16_bf16 v[18:33], v[70:73], v[138:141], v[18:33]
	ds_read_b128 v[170:173], v210 offset:10240
	v_exp_f32_e32 v220, v3
	v_fmac_f32_e32 v251, v216, v251
	v_exp_f32_e32 v221, v7
	v_fmac_f32_e32 v252, v217, v252
	v_exp_f32_e32 v222, v11
	v_fmac_f32_e32 v253, v218, v253
	v_exp_f32_e32 v223, v15
	v_fmac_f32_e32 v254, v219, v254
	v_mfma_f32_32x32x16_bf16 v[18:33], v[66:69], v[236:239], v[18:33]
	ds_read_b128 v[178:181], v210 offset:12288
	ds_read_b128 v[182:185], v210 offset:13312
	v_rcp_f32_e32 v216, v251
	v_add_f32_e32 v220, 1.0, v220
	v_rcp_f32_e32 v217, v252
	v_add_f32_e32 v221, 1.0, v221
	v_rcp_f32_e32 v218, v253
	v_add_f32_e32 v222, 1.0, v222
	v_rcp_f32_e32 v219, v254
	v_add_f32_e32 v223, 1.0, v223
	v_mfma_f32_32x32x16_bf16 v[18:33], v[62:65], v[146:149], v[18:33]
	ds_read_b128 v[186:189], v210 offset:14336
	ds_read_b128 v[190:193], v210 offset:15360
	v_rcp_f32_e32 v220, v220
	v_fma_f32 v240, -v212, v216, v216
	v_rcp_f32_e32 v221, v221
	v_fma_f32 v241, -v213, v217, v217
	v_rcp_f32_e32 v222, v222
	v_fma_f32 v242, -v214, v218, v218
	v_rcp_f32_e32 v223, v223
	v_fma_f32 v243, -v215, v219, v219
	v_mfma_f32_32x32x16_bf16 v[18:33], v[58:61], v[150:153], v[18:33]
	v_exp_f32_e32 v246, v5
	v_fma_f32 v194, v220, v194, v240
	v_exp_f32_e32 v247, v9
	v_fma_f32 v195, v221, v195, v241
	v_exp_f32_e32 v248, v13
	v_fma_f32 v196, v222, v196, v242
	v_exp_f32_e32 v249, v17
	v_fma_f32 v197, v223, v197, v243
	v_mfma_f32_32x32x16_bf16 v[18:33], v[54:57], v[154:157], v[18:33]
	v_exp_f32_e32 v212, v194
	v_add_f32_e32 v246, 1.0, v246
	v_exp_f32_e32 v213, v195
	v_add_f32_e32 v247, 1.0, v247
	v_exp_f32_e32 v214, v196
	v_add_f32_e32 v248, 1.0, v248
	v_exp_f32_e32 v215, v197
	v_add_f32_e32 v249, 1.0, v249
	v_fmac_f32_e32 v246, v246, v212
	v_fmac_f32_e32 v247, v247, v213
	v_fmac_f32_e32 v248, v248, v214
	v_fmac_f32_e32 v249, v249, v215
	v_mfma_f32_32x32x16_bf16 v[18:33], v[50:53], v[158:161], v[18:33]
	v_rcp_f32_e32 v246, v246
	v_rcp_f32_e32 v247, v247
	v_rcp_f32_e32 v248, v248
	v_rcp_f32_e32 v249, v249
	v_fma_f32 v246, -v212, v246, v246
	v_fma_f32 v247, -v213, v247, v247
	v_fma_f32 v248, -v214, v248, v248
	v_fma_f32 v249, -v215, v249, v249
	v_cvt_pk_bf16_f32 v236, v246, v247
	v_cvt_pk_bf16_f32 v237, v248, v249
	s_waitcnt lgkmcnt(0)
	v_mfma_f32_32x32x16_bf16 v[34:49], v[126:129], v[162:165], v[34:49]
	v_add_u32_e32 v233, v231, v244
	ds_read_b128 v[2:5], v233 offset:0
	ds_read_b128 v[6:9], v233 offset:16
	ds_read_b128 v[10:13], v233 offset:32
	ds_read_b128 v[14:17], v233 offset:48
	v_exp_f32_e32 v212, v20
	v_exp_f32_e32 v213, v24
	v_exp_f32_e32 v214, v28
	v_exp_f32_e32 v215, v32
	v_mfma_f32_32x32x16_bf16 v[34:49], v[122:125], v[166:169], v[34:49]
	v_exp_f32_e32 v216, v18
	v_fma_f32 v251, v212, s12, s12
	v_exp_f32_e32 v217, v22
	v_fma_f32 v252, v213, s12, s12
	v_exp_f32_e32 v218, v26
	v_fma_f32 v253, v214, s12, s12
	v_exp_f32_e32 v219, v30
	v_fma_f32 v254, v215, s12, s12
	v_mfma_f32_32x32x16_bf16 v[34:49], v[118:121], v[170:173], v[34:49]
	v_exp_f32_e32 v220, v19
	v_fmac_f32_e32 v251, v216, v251
	v_exp_f32_e32 v221, v23
	v_fmac_f32_e32 v252, v217, v252
	v_exp_f32_e32 v222, v27
	v_fmac_f32_e32 v253, v218, v253
	v_exp_f32_e32 v223, v31
	v_fmac_f32_e32 v254, v219, v254
	v_mfma_f32_32x32x16_bf16 v[34:49], v[114:117], v[224:227], v[34:49]
	v_rcp_f32_e32 v216, v251
	v_add_f32_e32 v220, 1.0, v220
	v_rcp_f32_e32 v217, v252
	v_add_f32_e32 v221, 1.0, v221
	v_rcp_f32_e32 v218, v253
	v_add_f32_e32 v222, 1.0, v222
	v_rcp_f32_e32 v219, v254
	v_add_f32_e32 v223, 1.0, v223
	v_mfma_f32_32x32x16_bf16 v[34:49], v[110:113], v[178:181], v[34:49]
	v_rcp_f32_e32 v220, v220
	v_fma_f32 v240, -v212, v216, v216
	v_rcp_f32_e32 v221, v221
	v_fma_f32 v241, -v213, v217, v217
	v_rcp_f32_e32 v222, v222
	v_fma_f32 v242, -v214, v218, v218
	v_rcp_f32_e32 v223, v223
	v_fma_f32 v243, -v215, v219, v219
	v_mfma_f32_32x32x16_bf16 v[34:49], v[106:109], v[182:185], v[34:49]
	v_exp_f32_e32 v246, v21
	v_fma_f32 v198, v220, v198, v240
	v_exp_f32_e32 v247, v25
	v_fma_f32 v199, v221, v199, v241
	v_exp_f32_e32 v248, v29
	v_fma_f32 v200, v222, v200, v242
	v_exp_f32_e32 v249, v33
	v_fma_f32 v201, v223, v201, v243
	v_mfma_f32_32x32x16_bf16 v[34:49], v[102:105], v[186:189], v[34:49]
	v_exp_f32_e32 v212, v198
	v_add_f32_e32 v246, 1.0, v246
	v_exp_f32_e32 v213, v199
	v_add_f32_e32 v247, 1.0, v247
	v_exp_f32_e32 v214, v200
	v_add_f32_e32 v248, 1.0, v248
	v_exp_f32_e32 v215, v201
	v_add_f32_e32 v249, 1.0, v249
	v_fmac_f32_e32 v246, v246, v212
	v_fmac_f32_e32 v247, v247, v213
	v_fmac_f32_e32 v248, v248, v214
	v_fmac_f32_e32 v249, v249, v215
	v_mfma_f32_32x32x16_bf16 v[34:49], v[98:101], v[190:193], v[34:49]
	v_rcp_f32_e32 v246, v246
	v_rcp_f32_e32 v247, v247
	v_rcp_f32_e32 v248, v248
	v_rcp_f32_e32 v249, v249
	v_fma_f32 v246, -v212, v246, v246
	v_fma_f32 v247, -v213, v247, v247
	v_fma_f32 v248, -v214, v248, v248
	v_fma_f32 v249, -v215, v249, v249
	v_cvt_pk_bf16_f32 v238, v246, v247
	v_cvt_pk_bf16_f32 v239, v248, v249
	ds_write_b128 v211, v[236:239] offset:0
	v_mfma_f32_32x32x16_bf16 v[82:97], v[78:81], v[162:165], v[82:97]
	ds_read_b128 v[18:21], v233 offset:128
	ds_read_b128 v[22:25], v233 offset:144
	ds_read_b128 v[26:29], v233 offset:160
	ds_read_b128 v[30:33], v233 offset:176
	v_exp_f32_e32 v212, v36
	v_exp_f32_e32 v213, v40
	v_exp_f32_e32 v214, v44
	v_exp_f32_e32 v215, v48
	s_waitcnt lgkmcnt(4)
	s_barrier
	v_mfma_f32_32x32x16_bf16 v[82:97], v[74:77], v[166:169], v[82:97]
	ds_read_b128 v[130:133], v210 offset:0
	ds_read_b128 v[134:137], v210 offset:1024
	v_exp_f32_e32 v216, v34
	v_fma_f32 v251, v212, s12, s12
	v_exp_f32_e32 v217, v38
	v_fma_f32 v252, v213, s12, s12
	v_exp_f32_e32 v218, v42
	v_fma_f32 v253, v214, s12, s12
	v_exp_f32_e32 v219, v46
	v_fma_f32 v254, v215, s12, s12
	v_mfma_f32_32x32x16_bf16 v[82:97], v[70:73], v[170:173], v[82:97]
	ds_read_b128 v[138:141], v210 offset:2048
	v_exp_f32_e32 v220, v35
	v_fmac_f32_e32 v251, v216, v251
	v_exp_f32_e32 v221, v39
	v_fmac_f32_e32 v252, v217, v252
	v_exp_f32_e32 v222, v43
	v_fmac_f32_e32 v253, v218, v253
	v_exp_f32_e32 v223, v47
	v_fmac_f32_e32 v254, v219, v254
	v_mfma_f32_32x32x16_bf16 v[82:97], v[66:69], v[224:227], v[82:97]
	ds_read_b128 v[146:149], v210 offset:4096
	ds_read_b128 v[150:153], v210 offset:5120
	v_rcp_f32_e32 v216, v251
	v_add_f32_e32 v220, 1.0, v220
	v_rcp_f32_e32 v217, v252
	v_add_f32_e32 v221, 1.0, v221
	v_rcp_f32_e32 v218, v253
	v_add_f32_e32 v222, 1.0, v222
	v_rcp_f32_e32 v219, v254
	v_add_f32_e32 v223, 1.0, v223
	v_mfma_f32_32x32x16_bf16 v[82:97], v[62:65], v[178:181], v[82:97]
	ds_read_b128 v[154:157], v210 offset:6144
	ds_read_b128 v[158:161], v210 offset:7168
	v_rcp_f32_e32 v220, v220
	v_fma_f32 v240, -v212, v216, v216
	v_rcp_f32_e32 v221, v221
	v_fma_f32 v241, -v213, v217, v217
	v_rcp_f32_e32 v222, v222
	v_fma_f32 v242, -v214, v218, v218
	v_rcp_f32_e32 v223, v223
	v_fma_f32 v243, -v215, v219, v219
	v_mfma_f32_32x32x16_bf16 v[82:97], v[58:61], v[182:185], v[82:97]
	v_exp_f32_e32 v246, v37
	v_fma_f32 v202, v220, v202, v240
	v_exp_f32_e32 v247, v41
	v_fma_f32 v203, v221, v203, v241
	v_exp_f32_e32 v248, v45
	v_fma_f32 v204, v222, v204, v242
	v_exp_f32_e32 v249, v49
	v_fma_f32 v205, v223, v205, v243
	v_mfma_f32_32x32x16_bf16 v[82:97], v[54:57], v[186:189], v[82:97]
	v_exp_f32_e32 v212, v202
	v_add_f32_e32 v246, 1.0, v246
	v_exp_f32_e32 v213, v203
	v_add_f32_e32 v247, 1.0, v247
	v_exp_f32_e32 v214, v204
	v_add_f32_e32 v248, 1.0, v248
	v_exp_f32_e32 v215, v205
	v_add_f32_e32 v249, 1.0, v249
	v_fmac_f32_e32 v246, v246, v212
	v_fmac_f32_e32 v247, v247, v213
	v_fmac_f32_e32 v248, v248, v214
	v_fmac_f32_e32 v249, v249, v215
	v_mfma_f32_32x32x16_bf16 v[82:97], v[50:53], v[190:193], v[82:97]
	v_rcp_f32_e32 v246, v246
	v_rcp_f32_e32 v247, v247
	v_rcp_f32_e32 v248, v248
	v_rcp_f32_e32 v249, v249
	v_fma_f32 v246, -v212, v246, v246
	v_fma_f32 v247, -v213, v247, v247
	v_fma_f32 v248, -v214, v248, v248
	v_fma_f32 v249, -v215, v249, v249
	v_cvt_pk_bf16_f32 v224, v246, v247
	v_cvt_pk_bf16_f32 v225, v248, v249
	s_waitcnt lgkmcnt(0)
	v_mfma_f32_32x32x16_bf16 v[2:17], v[126:129], v[130:133], v[2:17]
	v_add_u32_e32 v234, v231, v245
	ds_read_b128 v[34:37], v234 offset:0
	ds_read_b128 v[38:41], v234 offset:16
	ds_read_b128 v[42:45], v234 offset:32
	ds_read_b128 v[46:49], v234 offset:48
	v_add_u32_e32 v232, 0x100, v232
	v_exp_f32_e32 v212, v84
	v_exp_f32_e32 v213, v88
	v_exp_f32_e32 v214, v92
	v_exp_f32_e32 v215, v96
	v_mfma_f32_32x32x16_bf16 v[2:17], v[122:125], v[134:137], v[2:17]
	v_exp_f32_e32 v216, v82
	v_fma_f32 v251, v212, s12, s12
	v_exp_f32_e32 v217, v86
	v_fma_f32 v252, v213, s12, s12
	v_exp_f32_e32 v218, v90
	v_fma_f32 v253, v214, s12, s12
	v_exp_f32_e32 v219, v94
	v_fma_f32 v254, v215, s12, s12
	v_mfma_f32_32x32x16_bf16 v[2:17], v[118:121], v[138:141], v[2:17]
	v_exp_f32_e32 v220, v83
	v_fmac_f32_e32 v251, v216, v251
	v_exp_f32_e32 v221, v87
	v_fmac_f32_e32 v252, v217, v252
	v_exp_f32_e32 v222, v91
	v_fmac_f32_e32 v253, v218, v253
	v_exp_f32_e32 v223, v95
	v_fmac_f32_e32 v254, v219, v254
	v_mfma_f32_32x32x16_bf16 v[2:17], v[114:117], v[236:239], v[2:17]
	v_rcp_f32_e32 v216, v251
	v_add_f32_e32 v220, 1.0, v220
	v_rcp_f32_e32 v217, v252
	v_add_f32_e32 v221, 1.0, v221
	v_rcp_f32_e32 v218, v253
	v_add_f32_e32 v222, 1.0, v222
	v_rcp_f32_e32 v219, v254
	v_add_f32_e32 v223, 1.0, v223
	v_mfma_f32_32x32x16_bf16 v[2:17], v[110:113], v[146:149], v[2:17]
	v_rcp_f32_e32 v220, v220
	v_fma_f32 v240, -v212, v216, v216
	v_rcp_f32_e32 v221, v221
	v_fma_f32 v241, -v213, v217, v217
	v_rcp_f32_e32 v222, v222
	v_fma_f32 v242, -v214, v218, v218
	v_rcp_f32_e32 v223, v223
	v_fma_f32 v243, -v215, v219, v219
	v_mfma_f32_32x32x16_bf16 v[2:17], v[106:109], v[150:153], v[2:17]
	v_exp_f32_e32 v246, v85
	v_fma_f32 v206, v220, v206, v240
	v_exp_f32_e32 v247, v89
	v_fma_f32 v207, v221, v207, v241
	v_exp_f32_e32 v248, v93
	v_fma_f32 v208, v222, v208, v242
	v_exp_f32_e32 v249, v97
	v_fma_f32 v209, v223, v209, v243
	v_mfma_f32_32x32x16_bf16 v[2:17], v[102:105], v[154:157], v[2:17]
	v_exp_f32_e32 v212, v206
	v_add_f32_e32 v246, 1.0, v246
	v_exp_f32_e32 v213, v207
	v_add_f32_e32 v247, 1.0, v247
	v_exp_f32_e32 v214, v208
	v_add_f32_e32 v248, 1.0, v248
	v_exp_f32_e32 v215, v209
	v_add_f32_e32 v249, 1.0, v249
	v_fmac_f32_e32 v246, v246, v212
	v_fmac_f32_e32 v247, v247, v213
	v_fmac_f32_e32 v248, v248, v214
	v_fmac_f32_e32 v249, v249, v215
	v_mfma_f32_32x32x16_bf16 v[2:17], v[98:101], v[158:161], v[2:17]
	v_rcp_f32_e32 v246, v246
	v_rcp_f32_e32 v247, v247
	v_rcp_f32_e32 v248, v248
	v_rcp_f32_e32 v249, v249
	v_fma_f32 v246, -v212, v246, v246
	v_fma_f32 v247, -v213, v247, v247
	v_fma_f32 v248, -v214, v248, v248
	v_fma_f32 v249, -v215, v249, v249
	v_cvt_pk_bf16_f32 v226, v246, v247
	v_cvt_pk_bf16_f32 v227, v248, v249
	ds_write_b128 v211, v[224:227] offset:8192
	s_sub_u32 s16, s16, 1
	s_cmp_lg_u32 s16, 0
	s_cbranch_scc1 .Llight_loop_w3
	v_mfma_f32_32x32x16_bf16 v[18:33], v[78:81], v[130:133], v[18:33]
	ds_read_b128 v[82:85], v234 offset:128
	ds_read_b128 v[86:89], v234 offset:144
	ds_read_b128 v[90:93], v234 offset:160
	ds_read_b128 v[94:97], v234 offset:176
	v_exp_f32_e32 v212, v4
	v_exp_f32_e32 v213, v8
	v_exp_f32_e32 v214, v12
	v_exp_f32_e32 v215, v16
	s_waitcnt lgkmcnt(4)
	s_barrier
	v_mfma_f32_32x32x16_bf16 v[18:33], v[74:77], v[134:137], v[18:33]
	ds_read_b128 v[162:165], v210 offset:8192
	ds_read_b128 v[166:169], v210 offset:9216
	v_exp_f32_e32 v216, v2
	v_fma_f32 v251, v212, s12, s12
	v_exp_f32_e32 v217, v6
	v_fma_f32 v252, v213, s12, s12
	v_exp_f32_e32 v218, v10
	v_fma_f32 v253, v214, s12, s12
	v_exp_f32_e32 v219, v14
	v_fma_f32 v254, v215, s12, s12
	v_mfma_f32_32x32x16_bf16 v[18:33], v[70:73], v[138:141], v[18:33]
	ds_read_b128 v[170:173], v210 offset:10240
	v_exp_f32_e32 v220, v3
	v_fmac_f32_e32 v251, v216, v251
	v_exp_f32_e32 v221, v7
	v_fmac_f32_e32 v252, v217, v252
	v_exp_f32_e32 v222, v11
	v_fmac_f32_e32 v253, v218, v253
	v_exp_f32_e32 v223, v15
	v_fmac_f32_e32 v254, v219, v254
	v_mfma_f32_32x32x16_bf16 v[18:33], v[66:69], v[236:239], v[18:33]
	ds_read_b128 v[178:181], v210 offset:12288
	ds_read_b128 v[182:185], v210 offset:13312
	v_rcp_f32_e32 v216, v251
	v_add_f32_e32 v220, 1.0, v220
	v_rcp_f32_e32 v217, v252
	v_add_f32_e32 v221, 1.0, v221
	v_rcp_f32_e32 v218, v253
	v_add_f32_e32 v222, 1.0, v222
	v_rcp_f32_e32 v219, v254
	v_add_f32_e32 v223, 1.0, v223
	v_mfma_f32_32x32x16_bf16 v[18:33], v[62:65], v[146:149], v[18:33]
	ds_read_b128 v[186:189], v210 offset:14336
	ds_read_b128 v[190:193], v210 offset:15360
	v_rcp_f32_e32 v220, v220
	v_fma_f32 v240, -v212, v216, v216
	v_rcp_f32_e32 v221, v221
	v_fma_f32 v241, -v213, v217, v217
	v_rcp_f32_e32 v222, v222
	v_fma_f32 v242, -v214, v218, v218
	v_rcp_f32_e32 v223, v223
	v_fma_f32 v243, -v215, v219, v219
	v_mfma_f32_32x32x16_bf16 v[18:33], v[58:61], v[150:153], v[18:33]
	v_exp_f32_e32 v246, v5
	v_fma_f32 v194, v220, v194, v240
	v_exp_f32_e32 v247, v9
	v_fma_f32 v195, v221, v195, v241
	v_exp_f32_e32 v248, v13
	v_fma_f32 v196, v222, v196, v242
	v_exp_f32_e32 v249, v17
	v_fma_f32 v197, v223, v197, v243
	v_mfma_f32_32x32x16_bf16 v[18:33], v[54:57], v[154:157], v[18:33]
	v_exp_f32_e32 v212, v194
	v_add_f32_e32 v246, 1.0, v246
	v_exp_f32_e32 v213, v195
	v_add_f32_e32 v247, 1.0, v247
	v_exp_f32_e32 v214, v196
	v_add_f32_e32 v248, 1.0, v248
	v_exp_f32_e32 v215, v197
	v_add_f32_e32 v249, 1.0, v249
	v_fmac_f32_e32 v246, v246, v212
	v_fmac_f32_e32 v247, v247, v213
	v_fmac_f32_e32 v248, v248, v214
	v_fmac_f32_e32 v249, v249, v215
	v_mfma_f32_32x32x16_bf16 v[18:33], v[50:53], v[158:161], v[18:33]
	v_rcp_f32_e32 v246, v246
	v_rcp_f32_e32 v247, v247
	v_rcp_f32_e32 v248, v248
	v_rcp_f32_e32 v249, v249
	v_fma_f32 v246, -v212, v246, v246
	v_fma_f32 v247, -v213, v247, v247
	v_fma_f32 v248, -v214, v248, v248
	v_fma_f32 v249, -v215, v249, v249
	v_cvt_pk_bf16_f32 v236, v246, v247
	v_cvt_pk_bf16_f32 v237, v248, v249
	s_waitcnt lgkmcnt(0)
	v_mfma_f32_32x32x16_bf16 v[34:49], v[126:129], v[162:165], v[34:49]
	v_exp_f32_e32 v212, v20
	v_exp_f32_e32 v213, v24
	v_exp_f32_e32 v214, v28
	v_exp_f32_e32 v215, v32
	v_mfma_f32_32x32x16_bf16 v[34:49], v[122:125], v[166:169], v[34:49]
	v_exp_f32_e32 v216, v18
	v_fma_f32 v251, v212, s12, s12
	v_exp_f32_e32 v217, v22
	v_fma_f32 v252, v213, s12, s12
	v_exp_f32_e32 v218, v26
	v_fma_f32 v253, v214, s12, s12
	v_exp_f32_e32 v219, v30
	v_fma_f32 v254, v215, s12, s12
	v_mfma_f32_32x32x16_bf16 v[34:49], v[118:121], v[170:173], v[34:49]
	v_exp_f32_e32 v220, v19
	v_fmac_f32_e32 v251, v216, v251
	v_exp_f32_e32 v221, v23
	v_fmac_f32_e32 v252, v217, v252
	v_exp_f32_e32 v222, v27
	v_fmac_f32_e32 v253, v218, v253
	v_exp_f32_e32 v223, v31
	v_fmac_f32_e32 v254, v219, v254
	v_mfma_f32_32x32x16_bf16 v[34:49], v[114:117], v[224:227], v[34:49]
	v_rcp_f32_e32 v216, v251
	v_add_f32_e32 v220, 1.0, v220
	v_rcp_f32_e32 v217, v252
	v_add_f32_e32 v221, 1.0, v221
	v_rcp_f32_e32 v218, v253
	v_add_f32_e32 v222, 1.0, v222
	v_rcp_f32_e32 v219, v254
	v_add_f32_e32 v223, 1.0, v223
	v_mfma_f32_32x32x16_bf16 v[34:49], v[110:113], v[178:181], v[34:49]
	v_rcp_f32_e32 v220, v220
	v_fma_f32 v240, -v212, v216, v216
	v_rcp_f32_e32 v221, v221
	v_fma_f32 v241, -v213, v217, v217
	v_rcp_f32_e32 v222, v222
	v_fma_f32 v242, -v214, v218, v218
	v_rcp_f32_e32 v223, v223
	v_fma_f32 v243, -v215, v219, v219
	v_mfma_f32_32x32x16_bf16 v[34:49], v[106:109], v[182:185], v[34:49]
	v_exp_f32_e32 v246, v21
	v_fma_f32 v198, v220, v198, v240
	v_exp_f32_e32 v247, v25
	v_fma_f32 v199, v221, v199, v241
	v_exp_f32_e32 v248, v29
	v_fma_f32 v200, v222, v200, v242
	v_exp_f32_e32 v249, v33
	v_fma_f32 v201, v223, v201, v243
	v_mfma_f32_32x32x16_bf16 v[34:49], v[102:105], v[186:189], v[34:49]
	v_exp_f32_e32 v212, v198
	v_add_f32_e32 v246, 1.0, v246
	v_exp_f32_e32 v213, v199
	v_add_f32_e32 v247, 1.0, v247
	v_exp_f32_e32 v214, v200
	v_add_f32_e32 v248, 1.0, v248
	v_exp_f32_e32 v215, v201
	v_add_f32_e32 v249, 1.0, v249
	v_fmac_f32_e32 v246, v246, v212
	v_fmac_f32_e32 v247, v247, v213
	v_fmac_f32_e32 v248, v248, v214
	v_fmac_f32_e32 v249, v249, v215
	v_mfma_f32_32x32x16_bf16 v[34:49], v[98:101], v[190:193], v[34:49]
	v_rcp_f32_e32 v246, v246
	v_rcp_f32_e32 v247, v247
	v_rcp_f32_e32 v248, v248
	v_rcp_f32_e32 v249, v249
	v_fma_f32 v246, -v212, v246, v246
	v_fma_f32 v247, -v213, v247, v247
	v_fma_f32 v248, -v214, v248, v248
	v_fma_f32 v249, -v215, v249, v249
	v_cvt_pk_bf16_f32 v238, v246, v247
	v_cvt_pk_bf16_f32 v239, v248, v249
	ds_write_b128 v211, v[236:239] offset:0
	s_waitcnt lgkmcnt(0)
	s_barrier
	s_bfe_u32 s20, s19, 0x10006
	s_lshl_b32 s21, s20, 7
	s_lshl_b32 s20, s20, 13
	s_add_u32 s20, s20, 0x30000
	s_add_u32 s22, s14, s20
	s_addc_u32 s23, s15, 0
	s_add_u32 s24, s22, 0x1000
	s_addc_u32 s25, s23, 0
	global_load_dwordx4 v[98:101], v210, s[22:23] offset:0
	global_load_dwordx4 v[102:105], v210, s[22:23] offset:1024
	global_load_dwordx4 v[106:109], v210, s[22:23] offset:2048
	global_load_dwordx4 v[110:113], v210, s[22:23] offset:3072
	global_load_dwordx4 v[114:117], v210, s[24:25] offset:0
	global_load_dwordx4 v[118:121], v210, s[24:25] offset:1024
	global_load_dwordx4 v[122:125], v210, s[24:25] offset:2048
	global_load_dwordx4 v[126:129], v210, s[24:25] offset:3072
	v_or_b32_e32 v250, s21, v230
	global_load_dwordx4 v[130:133], v250, s[4:5] offset:0
	global_load_dwordx4 v[134:137], v250, s[4:5] offset:32
	global_load_dwordx4 v[138:141], v250, s[4:5] offset:64
	global_load_dwordx4 v[142:145], v250, s[4:5] offset:96
	global_load_dwordx4 v[146:149], v250, s[6:7] offset:0
	global_load_dwordx4 v[150:153], v250, s[6:7] offset:32
	global_load_dwordx4 v[154:157], v250, s[6:7] offset:64
	global_load_dwordx4 v[158:161], v250, s[6:7] offset:96
	s_load_dword s26, s[8:9], 0x0
	v_mfma_f32_32x32x16_bf16 v[82:97], v[78:81], v[162:165], v[82:97]
	v_exp_f32_e32 v212, v36
	v_exp_f32_e32 v213, v40
	v_exp_f32_e32 v214, v44
	v_exp_f32_e32 v215, v48
	v_mfma_f32_32x32x16_bf16 v[82:97], v[74:77], v[166:169], v[82:97]
	v_exp_f32_e32 v216, v34
	v_fma_f32 v251, v212, s12, s12
	v_exp_f32_e32 v217, v38
	v_fma_f32 v252, v213, s12, s12
	v_exp_f32_e32 v218, v42
	v_fma_f32 v253, v214, s12, s12
	v_exp_f32_e32 v219, v46
	v_fma_f32 v254, v215, s12, s12
	v_mfma_f32_32x32x16_bf16 v[82:97], v[70:73], v[170:173], v[82:97]
	v_exp_f32_e32 v220, v35
	v_fmac_f32_e32 v251, v216, v251
	v_exp_f32_e32 v221, v39
	v_fmac_f32_e32 v252, v217, v252
	v_exp_f32_e32 v222, v43
	v_fmac_f32_e32 v253, v218, v253
	v_exp_f32_e32 v223, v47
	v_fmac_f32_e32 v254, v219, v254
	v_mfma_f32_32x32x16_bf16 v[82:97], v[66:69], v[224:227], v[82:97]
	v_rcp_f32_e32 v216, v251
	v_add_f32_e32 v220, 1.0, v220
	v_rcp_f32_e32 v217, v252
	v_add_f32_e32 v221, 1.0, v221
	v_rcp_f32_e32 v218, v253
	v_add_f32_e32 v222, 1.0, v222
	v_rcp_f32_e32 v219, v254
	v_add_f32_e32 v223, 1.0, v223
	v_mfma_f32_32x32x16_bf16 v[82:97], v[62:65], v[178:181], v[82:97]
	v_rcp_f32_e32 v220, v220
	v_fma_f32 v240, -v212, v216, v216
	v_rcp_f32_e32 v221, v221
	v_fma_f32 v241, -v213, v217, v217
	v_rcp_f32_e32 v222, v222
	v_fma_f32 v242, -v214, v218, v218
	v_rcp_f32_e32 v223, v223
	v_fma_f32 v243, -v215, v219, v219
	v_mfma_f32_32x32x16_bf16 v[82:97], v[58:61], v[182:185], v[82:97]
	v_exp_f32_e32 v246, v37
	v_fma_f32 v202, v220, v202, v240
	v_exp_f32_e32 v247, v41
	v_fma_f32 v203, v221, v203, v241
	v_exp_f32_e32 v248, v45
	v_fma_f32 v204, v222, v204, v242
	v_exp_f32_e32 v249, v49
	v_fma_f32 v205, v223, v205, v243
	v_mfma_f32_32x32x16_bf16 v[82:97], v[54:57], v[186:189], v[82:97]
	v_exp_f32_e32 v212, v202
	v_add_f32_e32 v246, 1.0, v246
	v_exp_f32_e32 v213, v203
	v_add_f32_e32 v247, 1.0, v247
	v_exp_f32_e32 v214, v204
	v_add_f32_e32 v248, 1.0, v248
	v_exp_f32_e32 v215, v205
	v_add_f32_e32 v249, 1.0, v249
	v_fmac_f32_e32 v246, v246, v212
	v_fmac_f32_e32 v247, v247, v213
	v_fmac_f32_e32 v248, v248, v214
	v_fmac_f32_e32 v249, v249, v215
	v_mfma_f32_32x32x16_bf16 v[82:97], v[50:53], v[190:193], v[82:97]
	v_rcp_f32_e32 v246, v246
	v_rcp_f32_e32 v247, v247
	v_rcp_f32_e32 v248, v248
	v_rcp_f32_e32 v249, v249
	v_fma_f32 v246, -v212, v246, v246
	v_fma_f32 v247, -v213, v247, v247
	v_fma_f32 v248, -v214, v248, v248
	v_fma_f32 v249, -v215, v249, v249
	v_cvt_pk_bf16_f32 v224, v246, v247
	v_cvt_pk_bf16_f32 v225, v248, v249
	s_waitcnt lgkmcnt(0)
	v_exp_f32_e32 v212, v84
	v_exp_f32_e32 v213, v88
	v_exp_f32_e32 v214, v92
	v_exp_f32_e32 v215, v96
	v_exp_f32_e32 v216, v82
	v_fma_f32 v251, v212, s12, s12
	v_exp_f32_e32 v217, v86
	v_fma_f32 v252, v213, s12, s12
	v_exp_f32_e32 v218, v90
	v_fma_f32 v253, v214, s12, s12
	v_exp_f32_e32 v219, v94
	v_fma_f32 v254, v215, s12, s12
	v_exp_f32_e32 v220, v83
	v_fmac_f32_e32 v251, v216, v251
	v_exp_f32_e32 v221, v87
	v_fmac_f32_e32 v252, v217, v252
	v_exp_f32_e32 v222, v91
	v_fmac_f32_e32 v253, v218, v253
	v_exp_f32_e32 v223, v95
	v_fmac_f32_e32 v254, v219, v254
	v_rcp_f32_e32 v216, v251
	v_add_f32_e32 v220, 1.0, v220
	v_rcp_f32_e32 v217, v252
	v_add_f32_e32 v221, 1.0, v221
	v_rcp_f32_e32 v218, v253
	v_add_f32_e32 v222, 1.0, v222
	v_rcp_f32_e32 v219, v254
	v_add_f32_e32 v223, 1.0, v223
	v_rcp_f32_e32 v220, v220
	v_fma_f32 v240, -v212, v216, v216
	v_rcp_f32_e32 v221, v221
	v_fma_f32 v241, -v213, v217, v217
	v_rcp_f32_e32 v222, v222
	v_fma_f32 v242, -v214, v218, v218
	v_rcp_f32_e32 v223, v223
	v_fma_f32 v243, -v215, v219, v219
	v_exp_f32_e32 v246, v85
	v_fma_f32 v206, v220, v206, v240
	v_exp_f32_e32 v247, v89
	v_fma_f32 v207, v221, v207, v241
	v_exp_f32_e32 v248, v93
	v_fma_f32 v208, v222, v208, v242
	v_exp_f32_e32 v249, v97
	v_fma_f32 v209, v223, v209, v243
	v_exp_f32_e32 v212, v206
	v_add_f32_e32 v246, 1.0, v246
	v_exp_f32_e32 v213, v207
	v_add_f32_e32 v247, 1.0, v247
	v_exp_f32_e32 v214, v208
	v_add_f32_e32 v248, 1.0, v248
	v_exp_f32_e32 v215, v209
	v_add_f32_e32 v249, 1.0, v249
	v_fmac_f32_e32 v246, v246, v212
	v_fmac_f32_e32 v247, v247, v213
	v_fmac_f32_e32 v248, v248, v214
	v_fmac_f32_e32 v249, v249, v215
	v_rcp_f32_e32 v246, v246
	v_rcp_f32_e32 v247, v247
	v_rcp_f32_e32 v248, v248
	v_rcp_f32_e32 v249, v249
	v_fma_f32 v246, -v212, v246, v246
	v_fma_f32 v247, -v213, v247, v247
	v_fma_f32 v248, -v214, v248, v248
	v_fma_f32 v249, -v215, v249, v249
	v_cvt_pk_bf16_f32 v226, v246, v247
	v_cvt_pk_bf16_f32 v227, v248, v249
	ds_write_b128 v211, v[224:227] offset:8192
	s_waitcnt lgkmcnt(0)
	s_barrier
	s_lshl_b32 s20, s19, 6
	s_and_b32 s20, s20, 0x2000
	v_or_b32_e32 v20, s20, v210
	ds_read_b128 v[162:165], v20 offset:0
	ds_read_b128 v[166:169], v20 offset:1024
	ds_read_b128 v[170:173], v20 offset:2048
	ds_read_b128 v[174:177], v20 offset:3072
	ds_read_b128 v[178:181], v20 offset:4096
	ds_read_b128 v[182:185], v20 offset:5120
	ds_read_b128 v[186:189], v20 offset:6144
	ds_read_b128 v[190:193], v20 offset:7168
	s_bfe_u32 s20, s19, 0x10006
	s_lshl_b32 s20, s20, 9
	s_and_b32 s21, s19, 0x80
	s_or_b32 s20, s20, s21
	v_lshlrev_b32_e32 v19, 2, v229
	v_add3_u32 v19, s20, v19, v228
	s_waitcnt vmcnt(0)
	s_waitcnt lgkmcnt(7)
	v_mfma_f32_32x32x16_bf16 v[2:17], v[98:101], v[162:165], 0
	s_waitcnt lgkmcnt(6)
	v_mfma_f32_32x32x16_bf16 v[2:17], v[102:105], v[166:169], v[2:17]
	s_waitcnt lgkmcnt(5)
	v_mfma_f32_32x32x16_bf16 v[2:17], v[106:109], v[170:173], v[2:17]
	s_waitcnt lgkmcnt(4)
	v_mfma_f32_32x32x16_bf16 v[2:17], v[110:113], v[174:177], v[2:17]
	s_waitcnt lgkmcnt(3)
	v_mfma_f32_32x32x16_bf16 v[2:17], v[114:117], v[178:181], v[2:17]
	s_waitcnt lgkmcnt(2)
	v_mfma_f32_32x32x16_bf16 v[2:17], v[118:121], v[182:185], v[2:17]
	s_waitcnt lgkmcnt(1)
	v_mfma_f32_32x32x16_bf16 v[2:17], v[122:125], v[186:189], v[2:17]
	s_waitcnt lgkmcnt(0)
	v_mfma_f32_32x32x16_bf16 v[2:17], v[126:129], v[190:193], v[2:17]
	s_nop 15
	s_nop 3
	v_add_f32_e32 v2, v2, v130
	v_add_f32_e32 v3, v3, v131
	v_add_f32_e32 v4, v4, v132
	v_add_f32_e32 v5, v5, v133
	v_add_f32_e32 v6, v6, v134
	v_add_f32_e32 v7, v7, v135
	v_add_f32_e32 v8, v8, v136
	v_add_f32_e32 v9, v9, v137
	v_add_f32_e32 v10, v10, v138
	v_add_f32_e32 v11, v11, v139
	v_add_f32_e32 v12, v12, v140
	v_add_f32_e32 v13, v13, v141
	v_add_f32_e32 v14, v14, v142
	v_add_f32_e32 v15, v15, v143
	v_add_f32_e32 v16, v16, v144
	v_add_f32_e32 v17, v17, v145
	v_max_f32_e32 v2, 0, v2
	v_max_f32_e32 v3, 0, v3
	v_max_f32_e32 v4, 0, v4
	v_max_f32_e32 v5, 0, v5
	v_max_f32_e32 v6, 0, v6
	v_max_f32_e32 v7, 0, v7
	v_max_f32_e32 v8, 0, v8
	v_max_f32_e32 v9, 0, v9
	v_max_f32_e32 v10, 0, v10
	v_max_f32_e32 v11, 0, v11
	v_max_f32_e32 v12, 0, v12
	v_max_f32_e32 v13, 0, v13
	v_max_f32_e32 v14, 0, v14
	v_max_f32_e32 v15, 0, v15
	v_max_f32_e32 v16, 0, v16
	v_max_f32_e32 v17, 0, v17
	v_fma_f32 v18, v2, v146, 0
	v_fmac_f32_e32 v18, v3, v147
	v_fmac_f32_e32 v18, v4, v148
	v_fmac_f32_e32 v18, v5, v149
	v_fmac_f32_e32 v18, v6, v150
	v_fmac_f32_e32 v18, v7, v151
	v_fmac_f32_e32 v18, v8, v152
	v_fmac_f32_e32 v18, v9, v153
	v_fmac_f32_e32 v18, v10, v154
	v_fmac_f32_e32 v18, v11, v155
	v_fmac_f32_e32 v18, v12, v156
	v_fmac_f32_e32 v18, v13, v157
	v_fmac_f32_e32 v18, v14, v158
	v_fmac_f32_e32 v18, v15, v159
	v_fmac_f32_e32 v18, v16, v160
	v_fmac_f32_e32 v18, v17, v161
	ds_write_b32 v19, v18 offset:35904
	s_branch .LBB1_40
